# speedup vs baseline: 1.0185x; 1.0185x over previous
.LBB0_2:
	s_or_b64 exec, exec, s[80:81]
	v_lshl_add_u32 v1, v206, 2, s22
	s_add_i32 s19, s19, 0x22200
	ds_write_b32 v1, v72
	v_lshl_or_b32 v1, v124, 3, s19
	v_lshl_add_u32 v187, v67, 2, s22
	s_movk_i32 s22, 0x110
	v_mad_u32_u24 v186, v67, s22, v1
	s_add_i32 s22, s7, 0x180
	v_and_b32_e32 v102, 15, v0
	s_lshl_b32 s27, s34, 8
	s_and_b32 s25, s22, 0x380
	s_add_i32 s22, s7, 0x280
	v_lshlrev_b32_e32 v66, 2, v124
	v_mul_u32_u24_e32 v1, 0x110, v102
	v_and_b32_e32 v209, 48, v0
	s_and_b32 s23, s22, 0x380
	s_add_i32 s22, s7, 0x300
	v_mov_b32_e32 v67, 0x200
	s_addk_i32 s27, 0x380
	v_or_b32_e32 v133, s7, v66
	v_add3_u32 v1, s19, v1, v209
	s_lshl_b32 s19, s35, 15
	v_lshlrev_b32_e32 v210, 4, v206
	v_or_b32_e32 v189, s24, v66
	s_xor_b32 s24, s7, 0x200
	s_and_b32 s22, s22, 0x300
	v_bitop3_b32 v197, s7, v66, v67 bitop3:0xde
	s_and_b32 s7, s27, 0x380
	v_lshrrev_b32_e32 v185, 4, v206
	s_ashr_i32 s11, s10, 31
	v_or_b32_e32 v184, s19, v210
	v_or_b32_e32 v188, s26, v66
	v_or_b32_e32 v198, s25, v66
	v_or_b32_e32 v196, s23, v66
	v_or_b32_e32 v195, s22, v66
	v_or_b32_e32 v194, s7, v66
	v_mov_b32_e32 v102, v133
	v_and_b32_e32 v248, 2, v206
	v_cmp_ne_u32_e32 vcc, 0, v248
	v_mov_b32_e32 v249, 0x44444444
	v_mov_b32_e32 v250, 0xeeeeeeee
	s_nop 1
	v_cndmask_b32_e32 v223, v249, v250, vcc
	v_lshrrev_b32_e32 v248, 4, v206
	v_lshl_add_u32 v248, v248, 4, 1
	v_add_u32_e32 v249, 0, v248
	v_cvt_f32_u32_e32 v249, v249
	v_add_u32_e32 v250, 1, v248
	v_cvt_f32_u32_e32 v250, v250
	v_cvt_pk_bf16_f32 v232, v249, v250
	v_add_u32_e32 v249, 2, v248
	v_cvt_f32_u32_e32 v249, v249
	v_add_u32_e32 v250, 3, v248
	v_cvt_f32_u32_e32 v250, v250
	v_cvt_pk_bf16_f32 v233, v249, v250
	v_add_u32_e32 v249, 4, v248
	v_cvt_f32_u32_e32 v249, v249
	v_add_u32_e32 v250, 5, v248
	v_cvt_f32_u32_e32 v250, v250
	v_cvt_pk_bf16_f32 v234, v249, v250
	v_add_u32_e32 v249, 6, v248
	v_cvt_f32_u32_e32 v249, v249
	v_add_u32_e32 v250, 7, v248
	v_cvt_f32_u32_e32 v250, v250
	v_cvt_pk_bf16_f32 v235, v249, v250
	v_add_u32_e32 v249, 8, v248
	v_cvt_f32_u32_e32 v249, v249
	v_add_u32_e32 v250, 9, v248
	v_cvt_f32_u32_e32 v250, v250
	v_cvt_pk_bf16_f32 v236, v249, v250
	v_add_u32_e32 v249, 10, v248
	v_cvt_f32_u32_e32 v249, v249
	v_add_u32_e32 v250, 11, v248
	v_cvt_f32_u32_e32 v250, v250
	v_cvt_pk_bf16_f32 v237, v249, v250
	v_add_u32_e32 v249, 12, v248
	v_cvt_f32_u32_e32 v249, v249
	v_add_u32_e32 v250, 13, v248
	v_cvt_f32_u32_e32 v250, v250
	v_cvt_pk_bf16_f32 v238, v249, v250
	v_add_u32_e32 v249, 14, v248
	v_cvt_f32_u32_e32 v249, v249
	v_add_u32_e32 v250, 15, v248
	v_cvt_f32_u32_e32 v250, v250
	v_cvt_pk_bf16_f32 v239, v249, v250
	v_and_b32_e32 v248, 15, v206
	v_lshrrev_b32_e32 v249, 2, v248
	v_and_b32_e32 v250, 1, v248
	v_lshl_add_u32 v249, v249, 1, v250
	v_and_b32_e32 v250, 3, v249
	v_lshrrev_b32_e32 v251, 4, v206
	v_cmp_eq_u32_e32 vcc, v250, v251
	v_lshrrev_b32_e32 v249, 2, v249
	v_cmp_ne_u32_e64 s[78:79], 0, v249
	v_mov_b32_e32 v250, 0x3f80
	v_mov_b32_e32 v251, 0x3f800000
	s_nop 1
	v_cndmask_b32_e64 v250, v250, v251, s[78:79]
	v_cndmask_b32_e32 v252, 0, v250, vcc
	s_lshr_b32 s77, s19, 15
	s_mulk_i32 s77, 0x1100
	s_add_i32 s77, s77, 0x22200
	v_lshrrev_b32_e32 v248, 4, v206
	v_and_b32_e32 v249, 1, v248
	v_lshrrev_b32_e32 v250, 1, v248
	v_lshlrev_b32_e32 v249, 6, v249
	v_lshl_add_u32 v253, v250, 1, v249
	v_and_b32_e32 v248, 15, v206
	v_cmp_eq_u32_e64 s[78:79], 0, v248
	v_mov_b32_e32 v244, v252
	v_mov_b32_e32 v245, 0
	v_mov_b32_e32 v246, 0
	v_mov_b32_e32 v247, 0
	v_mov_b64_e32 v[240:241], 0
	v_mov_b64_e32 v[242:243], 0
	s_nop 1
	v_smfmac_f32_16x16x64_bf16 v[240:243], v[244:247], v[232:239], v223
	s_nop 15
	s_nop 3
	s_and_saveexec_b64 s[80:81], s[78:79]
	v_cvt_u32_f32_e32 v248, v240
	v_add_u32_e32 v248, -1, v248
	v_lshl_add_u32 v248, v248, 2, s77
	v_add_u32_e32 v249, 0, v253
	ds_write_b32 v248, v249
	v_cvt_u32_f32_e32 v248, v241
	v_add_u32_e32 v248, -1, v248
	v_lshl_add_u32 v248, v248, 2, s77
	v_add_u32_e32 v249, 32, v253
	ds_write_b32 v248, v249
	v_cvt_u32_f32_e32 v248, v242
	v_add_u32_e32 v248, -1, v248
	v_lshl_add_u32 v248, v248, 2, s77
	v_add_u32_e32 v249, 16, v253
	ds_write_b32 v248, v249
	v_cvt_u32_f32_e32 v248, v243
	v_add_u32_e32 v248, -1, v248
	v_lshl_add_u32 v248, v248, 2, s77
	v_add_u32_e32 v249, 48, v253
	ds_write_b32 v248, v249
	s_or_b64 exec, exec, s[80:81]
	v_mov_b32_e32 v244, 0
	v_mov_b32_e32 v245, v252
	v_mov_b32_e32 v246, 0
	v_mov_b32_e32 v247, 0
	v_mov_b64_e32 v[240:241], 0
	v_mov_b64_e32 v[242:243], 0
	s_nop 1
	v_smfmac_f32_16x16x64_bf16 v[240:243], v[244:247], v[232:239], v223
	s_nop 15
	s_nop 3
	s_and_saveexec_b64 s[80:81], s[78:79]
	v_cvt_u32_f32_e32 v248, v240
	v_add_u32_e32 v248, -1, v248
	v_lshl_add_u32 v248, v248, 2, s77
	v_add_u32_e32 v249, 4, v253
	ds_write_b32 v248, v249
	v_cvt_u32_f32_e32 v248, v241
	v_add_u32_e32 v248, -1, v248
	v_lshl_add_u32 v248, v248, 2, s77
	v_add_u32_e32 v249, 36, v253
	ds_write_b32 v248, v249
	v_cvt_u32_f32_e32 v248, v242
	v_add_u32_e32 v248, -1, v248
	v_lshl_add_u32 v248, v248, 2, s77
	v_add_u32_e32 v249, 20, v253
	ds_write_b32 v248, v249
	v_cvt_u32_f32_e32 v248, v243
	v_add_u32_e32 v248, -1, v248
	v_lshl_add_u32 v248, v248, 2, s77
	v_add_u32_e32 v249, 52, v253
	ds_write_b32 v248, v249
	s_or_b64 exec, exec, s[80:81]
	v_mov_b32_e32 v244, 0
	v_mov_b32_e32 v245, 0
	v_mov_b32_e32 v246, v252
	v_mov_b32_e32 v247, 0
	v_mov_b64_e32 v[240:241], 0
	v_mov_b64_e32 v[242:243], 0
	s_nop 1
	v_smfmac_f32_16x16x64_bf16 v[240:243], v[244:247], v[232:239], v223
	s_nop 15
	s_nop 3
	s_and_saveexec_b64 s[80:81], s[78:79]
	v_cvt_u32_f32_e32 v248, v240
	v_add_u32_e32 v248, -1, v248
	v_lshl_add_u32 v248, v248, 2, s77
	v_add_u32_e32 v249, 8, v253
	ds_write_b32 v248, v249
	v_cvt_u32_f32_e32 v248, v241
	v_add_u32_e32 v248, -1, v248
	v_lshl_add_u32 v248, v248, 2, s77
	v_add_u32_e32 v249, 40, v253
	ds_write_b32 v248, v249
	v_cvt_u32_f32_e32 v248, v242
	v_add_u32_e32 v248, -1, v248
	v_lshl_add_u32 v248, v248, 2, s77
	v_add_u32_e32 v249, 24, v253
	ds_write_b32 v248, v249
	v_cvt_u32_f32_e32 v248, v243
	v_add_u32_e32 v248, -1, v248
	v_lshl_add_u32 v248, v248, 2, s77
	v_add_u32_e32 v249, 56, v253
	ds_write_b32 v248, v249
	s_or_b64 exec, exec, s[80:81]
	v_mov_b32_e32 v244, 0
	v_mov_b32_e32 v245, 0
	v_mov_b32_e32 v246, 0
	v_mov_b32_e32 v247, v252
	v_mov_b64_e32 v[240:241], 0
	v_mov_b64_e32 v[242:243], 0
	s_nop 1
	v_smfmac_f32_16x16x64_bf16 v[240:243], v[244:247], v[232:239], v223
	s_nop 15
	s_nop 3
	s_and_saveexec_b64 s[80:81], s[78:79]
	v_cvt_u32_f32_e32 v248, v240
	v_add_u32_e32 v248, -1, v248
	v_lshl_add_u32 v248, v248, 2, s77
	v_add_u32_e32 v249, 12, v253
	ds_write_b32 v248, v249
	v_cvt_u32_f32_e32 v248, v241
	v_add_u32_e32 v248, -1, v248
	v_lshl_add_u32 v248, v248, 2, s77
	v_add_u32_e32 v249, 44, v253
	ds_write_b32 v248, v249
	v_cvt_u32_f32_e32 v248, v242
	v_add_u32_e32 v248, -1, v248
	v_lshl_add_u32 v248, v248, 2, s77
	v_add_u32_e32 v249, 28, v253
	ds_write_b32 v248, v249
	v_cvt_u32_f32_e32 v248, v243
	v_add_u32_e32 v248, -1, v248
	v_lshl_add_u32 v248, v248, 2, s77
	v_add_u32_e32 v249, 60, v253
	ds_write_b32 v248, v249
	s_or_b64 exec, exec, s[80:81]
	v_bfe_u32 v248, v206, 3, 2
	v_lshrrev_b32_e32 v249, 5, v206
	v_lshlrev_b32_e32 v248, 4, v248
	v_lshl_or_b32 v248, v249, 3, v248
	v_and_b32_e32 v249, 7, v206
	v_or_b32_e32 v248, v248, v249
	v_lshl_add_u32 v248, v248, 2, s77
	s_waitcnt lgkmcnt(0)
	ds_read_b32 v254, v248
	v_and_b32_e32 v248, 15, v206
	v_bfe_u32 v249, v248, 1, 2
	v_lshrrev_b32_e32 v250, 3, v248
	v_lshlrev_b32_e32 v249, 4, v249
	v_lshl_or_b32 v249, v250, 3, v249
	v_and_b32_e32 v250, 1, v248
	v_lshl_or_b32 v249, v250, 2, v249
	v_lshl_add_u32 v249, v249, 2, s77
	ds_read_b128 v[248:251], v249
	s_lshr_b32 s76, s19, 6
	s_add_i32 s76, s76, 0x20000
	v_lshrrev_b32_e32 v252, 4, v206
	v_lshl_add_u32 v252, v252, 7, s76
	s_waitcnt lgkmcnt(0)
	v_add_u32_e32 v248, v252, v248
	v_add_u32_e32 v249, v252, v249
	v_add_u32_e32 v250, v252, v250
	v_add_u32_e32 v251, v252, v251
	v_cvt_pk_bf16_f32 v236, v224, v225
	v_cvt_pk_bf16_f32 v237, v226, v227
	v_lshlrev_b32_e32 v238, 16, v236
	v_and_b32_e32 v239, 0xffff0000, v236
	v_lshlrev_b32_e32 v240, 16, v237
	v_and_b32_e32 v241, 0xffff0000, v237
	v_sub_f32_e32 v238, v224, v238
	v_sub_f32_e32 v239, v225, v239
	v_sub_f32_e32 v240, v226, v240
	v_sub_f32_e32 v241, v227, v241
	v_cvt_pk_bf16_f32 v238, v238, v239
	v_cvt_pk_bf16_f32 v239, v240, v241
	ds_write_b16 v248, v236
	ds_write_b16_d16_hi v249, v236
	ds_write_b16 v250, v237
	ds_write_b16_d16_hi v251, v237
	ds_write_b16 v248, v238 offset:2176
	ds_write_b16_d16_hi v249, v238 offset:2176
	ds_write_b16 v250, v239 offset:2176
	ds_write_b16_d16_hi v251, v239 offset:2176
	ds_read_b32 v232, v187 offset:192
	ds_read_b32 v234, v187 offset:200
	ds_read_b32 v236, v187 offset:208
	ds_read_b32 v238, v187 offset:216
	ds_read_b32 v240, v187 offset:224
	ds_read_b32 v242, v187 offset:232
	ds_read_b32 v244, v187 offset:240
	ds_read_b32 v246, v187 offset:248
	v_or_b32_e32 v103, 48, v132
	v_add_u32_e32 v104, 1, v102
	v_cmp_eq_u32_e32 vcc, v102, v103
	v_add_u32_e32 v105, 3, v102
	v_add_u32_e32 v106, 2, v102
	v_cndmask_b32_e64 v72, 0, 1.0, vcc
	v_cmp_eq_u32_e32 vcc, v104, v103
	v_or_b32_e32 v107, 50, v132
	v_or_b32_e32 v108, 52, v132
	v_cndmask_b32_e64 v73, 0, 1.0, vcc
	v_cmp_eq_u32_e32 vcc, v105, v103
	s_waitcnt lgkmcnt(0)
	s_waitcnt vmcnt(23)
	v_pk_fma_f32 v[68:69], v[232:233], v[68:69], v[72:73] op_sel_hi:[0,1,1] neg_lo:[1,0,0] neg_hi:[1,0,0]
	v_cvt_pk_bf16_f32 v68, v68, v69
	v_cndmask_b32_e64 v73, 0, 1.0, vcc
	v_cmp_eq_u32_e32 vcc, v106, v103
	v_or_b32_e32 v109, 54, v132
	v_or_b32_e32 v110, 56, v132
	v_cndmask_b32_e64 v72, 0, 1.0, vcc
	v_pk_fma_f32 v[66:67], v[232:233], v[70:71], v[72:73] op_sel_hi:[0,1,1] neg_lo:[1,0,0] neg_hi:[1,0,0]
	v_cvt_pk_bf16_f32 v69, v66, v67
	ds_write_b64 v186, v[68:69]
	v_cmp_eq_u32_e32 vcc, v102, v107
	v_or_b32_e32 v111, 58, v132
	v_or_b32_e32 v112, 60, v132
	v_cndmask_b32_e64 v68, 0, 1.0, vcc
	v_cmp_eq_u32_e32 vcc, v104, v107
	v_or_b32_e32 v113, 62, v132
	v_or_b32_e32 v193, 2, v132
	v_cndmask_b32_e64 v69, 0, 1.0, vcc
	v_cmp_eq_u32_e32 vcc, v105, v107
	s_waitcnt vmcnt(22)
	v_pk_fma_f32 v[68:69], v[234:235], v[78:79], v[68:69] op_sel_hi:[0,1,1] neg_lo:[1,0,0] neg_hi:[1,0,0]
	v_cvt_pk_bf16_f32 v68, v68, v69
	v_cndmask_b32_e64 v71, 0, 1.0, vcc
	v_cmp_eq_u32_e32 vcc, v106, v107
	v_or_b32_e32 v192, 4, v132
	v_or_b32_e32 v190, 6, v132
	v_cndmask_b32_e64 v70, 0, 1.0, vcc
	v_pk_fma_f32 v[66:67], v[234:235], v[80:81], v[70:71] op_sel_hi:[0,1,1] neg_lo:[1,0,0] neg_hi:[1,0,0]
	v_cvt_pk_bf16_f32 v69, v66, v67
	ds_write_b64 v186, v[68:69] offset:544
	v_cmp_eq_u32_e32 vcc, v102, v108
	v_or_b32_e32 v149, 8, v132
	v_or_b32_e32 v148, 10, v132
	v_cndmask_b32_e64 v68, 0, 1.0, vcc
	v_cmp_eq_u32_e32 vcc, v104, v108
	v_or_b32_e32 v147, 12, v132
	v_or_b32_e32 v146, 14, v132
	v_cndmask_b32_e64 v69, 0, 1.0, vcc
	v_cmp_eq_u32_e32 vcc, v105, v108
	s_waitcnt vmcnt(21)
	v_pk_fma_f32 v[68:69], v[236:237], v[82:83], v[68:69] op_sel_hi:[0,1,1] neg_lo:[1,0,0] neg_hi:[1,0,0]
	v_cvt_pk_bf16_f32 v68, v68, v69
	v_cndmask_b32_e64 v71, 0, 1.0, vcc
	v_cmp_eq_u32_e32 vcc, v106, v108
	s_nop 1
	v_cndmask_b32_e64 v70, 0, 1.0, vcc
	v_pk_fma_f32 v[66:67], v[236:237], v[84:85], v[70:71] op_sel_hi:[0,1,1] neg_lo:[1,0,0] neg_hi:[1,0,0]
	v_cvt_pk_bf16_f32 v69, v66, v67
	ds_write_b64 v186, v[68:69] offset:1088
	v_cmp_eq_u32_e32 vcc, v102, v109
	s_nop 1
	v_cndmask_b32_e64 v68, 0, 1.0, vcc
	v_cmp_eq_u32_e32 vcc, v104, v109
	s_nop 1
	v_cndmask_b32_e64 v69, 0, 1.0, vcc
	v_cmp_eq_u32_e32 vcc, v105, v109
	s_waitcnt vmcnt(20)
	v_pk_fma_f32 v[68:69], v[238:239], v[90:91], v[68:69] op_sel_hi:[0,1,1] neg_lo:[1,0,0] neg_hi:[1,0,0]
	v_cvt_pk_bf16_f32 v68, v68, v69
	v_cndmask_b32_e64 v71, 0, 1.0, vcc
	v_cmp_eq_u32_e32 vcc, v106, v109
	s_nop 1
	v_cndmask_b32_e64 v70, 0, 1.0, vcc
	v_pk_fma_f32 v[66:67], v[238:239], v[92:93], v[70:71] op_sel_hi:[0,1,1] neg_lo:[1,0,0] neg_hi:[1,0,0]
	v_cvt_pk_bf16_f32 v69, v66, v67
	ds_write_b64 v186, v[68:69] offset:1632
	v_cmp_eq_u32_e32 vcc, v102, v110
	s_nop 1
	v_cndmask_b32_e64 v68, 0, 1.0, vcc
	v_cmp_eq_u32_e32 vcc, v104, v110
	s_nop 1
	v_cndmask_b32_e64 v69, 0, 1.0, vcc
	v_cmp_eq_u32_e32 vcc, v105, v110
	s_waitcnt vmcnt(19)
	v_pk_fma_f32 v[68:69], v[240:241], v[98:99], v[68:69] op_sel_hi:[0,1,1] neg_lo:[1,0,0] neg_hi:[1,0,0]
	v_cvt_pk_bf16_f32 v68, v68, v69
	v_cndmask_b32_e64 v71, 0, 1.0, vcc
	v_cmp_eq_u32_e32 vcc, v106, v110
	s_nop 1
	v_cndmask_b32_e64 v70, 0, 1.0, vcc
	v_pk_fma_f32 v[66:67], v[240:241], v[100:101], v[70:71] op_sel_hi:[0,1,1] neg_lo:[1,0,0] neg_hi:[1,0,0]
	v_cvt_pk_bf16_f32 v69, v66, v67
	ds_write_b64 v186, v[68:69] offset:2176
	v_cmp_eq_u32_e32 vcc, v102, v111
	s_nop 1
	v_cndmask_b32_e64 v68, 0, 1.0, vcc
	v_cmp_eq_u32_e32 vcc, v104, v111
	s_nop 1
	v_cndmask_b32_e64 v69, 0, 1.0, vcc
	v_cmp_eq_u32_e32 vcc, v105, v111
	s_waitcnt vmcnt(18)
	v_pk_fma_f32 v[62:63], v[242:243], v[62:63], v[68:69] op_sel_hi:[0,1,1] neg_lo:[1,0,0] neg_hi:[1,0,0]
	v_cvt_pk_bf16_f32 v62, v62, v63
	v_cndmask_b32_e64 v69, 0, 1.0, vcc
	v_cmp_eq_u32_e32 vcc, v106, v111
	s_nop 1
	v_cndmask_b32_e64 v68, 0, 1.0, vcc
	v_pk_fma_f32 v[64:65], v[242:243], v[64:65], v[68:69] op_sel_hi:[0,1,1] neg_lo:[1,0,0] neg_hi:[1,0,0]
	v_cvt_pk_bf16_f32 v63, v64, v65
	ds_write_b64 v186, v[62:63] offset:2720
	v_cmp_eq_u32_e32 vcc, v102, v112
	s_nop 1
	v_cndmask_b32_e64 v64, 0, 1.0, vcc
	v_cmp_eq_u32_e32 vcc, v104, v112
	s_nop 1
	v_cndmask_b32_e64 v65, 0, 1.0, vcc
	v_cmp_eq_u32_e32 vcc, v105, v112
	s_waitcnt vmcnt(17)
	v_pk_fma_f32 v[54:55], v[244:245], v[54:55], v[64:65] op_sel_hi:[0,1,1] neg_lo:[1,0,0] neg_hi:[1,0,0]
	v_cvt_pk_bf16_f32 v54, v54, v55
	v_cndmask_b32_e64 v65, 0, 1.0, vcc
	v_cmp_eq_u32_e32 vcc, v106, v112
	s_nop 1
	v_cndmask_b32_e64 v64, 0, 1.0, vcc
	v_pk_fma_f32 v[56:57], v[244:245], v[56:57], v[64:65] op_sel_hi:[0,1,1] neg_lo:[1,0,0] neg_hi:[1,0,0]
	v_cvt_pk_bf16_f32 v55, v56, v57
	ds_write_b64 v186, v[54:55] offset:3264
	v_cmp_eq_u32_e32 vcc, v102, v113
	s_nop 1
	v_cndmask_b32_e64 v56, 0, 1.0, vcc
	v_cmp_eq_u32_e32 vcc, v104, v113
	s_nop 1
	v_cndmask_b32_e64 v57, 0, 1.0, vcc
	v_cmp_eq_u32_e32 vcc, v105, v113
	s_waitcnt vmcnt(16)
	v_pk_fma_f32 v[46:47], v[246:247], v[46:47], v[56:57] op_sel_hi:[0,1,1] neg_lo:[1,0,0] neg_hi:[1,0,0]
	v_cvt_pk_bf16_f32 v46, v46, v47
	v_cndmask_b32_e64 v57, 0, 1.0, vcc
	v_cmp_eq_u32_e32 vcc, v106, v113
	s_nop 1
	v_cndmask_b32_e64 v56, 0, 1.0, vcc
	v_pk_fma_f32 v[48:49], v[246:247], v[48:49], v[56:57] op_sel_hi:[0,1,1] neg_lo:[1,0,0] neg_hi:[1,0,0]
	v_cvt_pk_bf16_f32 v47, v48, v49
	ds_write_b64 v186, v[46:47] offset:3808
	ds_read_b128 v[232:235], v1
	ds_read_b128 v[236:239], v1 offset:64
	ds_read_b128 v[240:243], v1 offset:128
	ds_read_b128 v[244:247], v1 offset:192
	s_waitcnt lgkmcnt(0)
	ds_write_b128 v184, v[232:235]
	ds_write_b128 v184, v[236:239] offset:1024
	ds_write_b128 v184, v[240:243] offset:2048
	ds_write_b128 v184, v[244:247] offset:3072
	ds_read_b32 v232, v187 offset:192
	ds_read_b32 v234, v187 offset:200
	ds_read_b32 v236, v187 offset:208
	ds_read_b32 v238, v187 offset:216
	ds_read_b32 v240, v187 offset:224
	ds_read_b32 v242, v187 offset:232
	ds_read_b32 v244, v187 offset:240
	ds_read_b32 v246, v187 offset:248
	s_lshl_b32 s30, s25, 2
	s_mov_b32 s31, s21
	v_lshl_add_u64 v[46:47], v[126:127], 0, s[30:31]
	v_lshl_add_u64 v[48:49], v[128:129], 0, s[30:31]
	v_lshl_add_u64 v[54:55], v[134:135], 0, s[30:31]
	v_lshl_add_u64 v[56:57], v[136:137], 0, s[30:31]
	v_lshl_add_u64 v[62:63], v[138:139], 0, s[30:31]
	v_lshl_add_u64 v[64:65], v[140:141], 0, s[30:31]
	v_lshl_add_u64 v[98:99], v[142:143], 0, s[30:31]
	v_lshl_add_u64 v[100:101], v[144:145], 0, s[30:31]
	global_load_dwordx4 v[90:93], v[46:47], off nt
	global_load_dwordx4 v[82:85], v[48:49], off nt
	global_load_dwordx4 v[78:81], v[54:55], off nt
	global_load_dwordx4 v[70:73], v[56:57], off nt
	global_load_dwordx4 v[66:69], v[62:63], off nt
	s_nop 0
	global_load_dwordx4 v[62:65], v[64:65], off nt
	s_nop 0
	global_load_dwordx4 v[54:57], v[98:99], off nt
	global_load_dwordx4 v[46:49], v[100:101], off nt
	v_mov_b32_e32 v99, v189
	v_add_u32_e32 v102, 1, v99
	v_cmp_eq_u32_e32 vcc, v99, v103
	v_add_u32_e32 v104, 3, v99
	v_add_u32_e32 v105, 2, v99
	v_cndmask_b32_e64 v100, 0, 1.0, vcc
	v_cmp_eq_u32_e32 vcc, v102, v103
	s_nop 1
	v_cndmask_b32_e64 v101, 0, 1.0, vcc
	v_cmp_eq_u32_e32 vcc, v104, v103
	s_waitcnt lgkmcnt(0)
	s_waitcnt vmcnt(23)
	v_pk_fma_f32 v[94:95], v[232:233], v[94:95], v[100:101] op_sel_hi:[0,1,1] neg_lo:[1,0,0] neg_hi:[1,0,0]
	v_cvt_pk_bf16_f32 v94, v94, v95
	v_cndmask_b32_e64 v101, 0, 1.0, vcc
	v_cmp_eq_u32_e32 vcc, v105, v103
	s_nop 1
	v_cndmask_b32_e64 v100, 0, 1.0, vcc
	v_pk_fma_f32 v[96:97], v[232:233], v[96:97], v[100:101] op_sel_hi:[0,1,1] neg_lo:[1,0,0] neg_hi:[1,0,0]
	v_cvt_pk_bf16_f32 v95, v96, v97
	ds_write_b64 v186, v[94:95]
	v_cmp_eq_u32_e32 vcc, v99, v107
	s_nop 1
	v_cndmask_b32_e64 v96, 0, 1.0, vcc
	v_cmp_eq_u32_e32 vcc, v102, v107
	s_nop 1
	v_cndmask_b32_e64 v97, 0, 1.0, vcc
	v_cmp_eq_u32_e32 vcc, v104, v107
	s_waitcnt vmcnt(22)
	v_pk_fma_f32 v[86:87], v[234:235], v[86:87], v[96:97] op_sel_hi:[0,1,1] neg_lo:[1,0,0] neg_hi:[1,0,0]
	v_cvt_pk_bf16_f32 v86, v86, v87
	v_cndmask_b32_e64 v97, 0, 1.0, vcc
	v_cmp_eq_u32_e32 vcc, v105, v107
	s_nop 1
	v_cndmask_b32_e64 v96, 0, 1.0, vcc
	v_pk_fma_f32 v[88:89], v[234:235], v[88:89], v[96:97] op_sel_hi:[0,1,1] neg_lo:[1,0,0] neg_hi:[1,0,0]
	v_cvt_pk_bf16_f32 v87, v88, v89
	ds_write_b64 v186, v[86:87] offset:544
	v_cmp_eq_u32_e32 vcc, v99, v108
	s_nop 1
	v_cndmask_b32_e64 v88, 0, 1.0, vcc
	v_cmp_eq_u32_e32 vcc, v102, v108
	s_nop 1
	v_cndmask_b32_e64 v89, 0, 1.0, vcc
	v_cmp_eq_u32_e32 vcc, v104, v108
	s_waitcnt vmcnt(21)
	v_pk_fma_f32 v[74:75], v[236:237], v[74:75], v[88:89] op_sel_hi:[0,1,1] neg_lo:[1,0,0] neg_hi:[1,0,0]
	v_cvt_pk_bf16_f32 v74, v74, v75
	v_cndmask_b32_e64 v89, 0, 1.0, vcc
	v_cmp_eq_u32_e32 vcc, v105, v108
	s_nop 1
	v_cndmask_b32_e64 v88, 0, 1.0, vcc
	v_pk_fma_f32 v[76:77], v[236:237], v[76:77], v[88:89] op_sel_hi:[0,1,1] neg_lo:[1,0,0] neg_hi:[1,0,0]
	v_cvt_pk_bf16_f32 v75, v76, v77
	ds_write_b64 v186, v[74:75] offset:1088
	v_cmp_eq_u32_e32 vcc, v99, v109
	s_nop 1
	v_cndmask_b32_e64 v76, 0, 1.0, vcc
	v_cmp_eq_u32_e32 vcc, v102, v109
	s_nop 1
	v_cndmask_b32_e64 v77, 0, 1.0, vcc
	v_cmp_eq_u32_e32 vcc, v104, v109
	s_waitcnt vmcnt(20)
	v_pk_fma_f32 v[58:59], v[238:239], v[58:59], v[76:77] op_sel_hi:[0,1,1] neg_lo:[1,0,0] neg_hi:[1,0,0]
	v_cvt_pk_bf16_f32 v58, v58, v59
	v_cndmask_b32_e64 v77, 0, 1.0, vcc
	v_cmp_eq_u32_e32 vcc, v105, v109
	s_nop 1
	v_cndmask_b32_e64 v76, 0, 1.0, vcc
	v_pk_fma_f32 v[60:61], v[238:239], v[60:61], v[76:77] op_sel_hi:[0,1,1] neg_lo:[1,0,0] neg_hi:[1,0,0]
	v_cvt_pk_bf16_f32 v59, v60, v61
	ds_write_b64 v186, v[58:59] offset:1632
	v_cmp_eq_u32_e32 vcc, v99, v110
	s_nop 1
	v_cndmask_b32_e64 v60, 0, 1.0, vcc
	v_cmp_eq_u32_e32 vcc, v102, v110
	s_nop 1
	v_cndmask_b32_e64 v61, 0, 1.0, vcc
	v_cmp_eq_u32_e32 vcc, v104, v110
	s_waitcnt vmcnt(19)
	v_pk_fma_f32 v[50:51], v[240:241], v[50:51], v[60:61] op_sel_hi:[0,1,1] neg_lo:[1,0,0] neg_hi:[1,0,0]
	v_cvt_pk_bf16_f32 v50, v50, v51
	v_cndmask_b32_e64 v61, 0, 1.0, vcc
	v_cmp_eq_u32_e32 vcc, v105, v110
	s_nop 1
	v_cndmask_b32_e64 v60, 0, 1.0, vcc
	v_pk_fma_f32 v[52:53], v[240:241], v[52:53], v[60:61] op_sel_hi:[0,1,1] neg_lo:[1,0,0] neg_hi:[1,0,0]
	v_cvt_pk_bf16_f32 v51, v52, v53
	ds_write_b64 v186, v[50:51] offset:2176
	v_cmp_eq_u32_e32 vcc, v99, v111
	s_nop 1
	v_cndmask_b32_e64 v52, 0, 1.0, vcc
	v_cmp_eq_u32_e32 vcc, v102, v111
	s_nop 1
	v_cndmask_b32_e64 v53, 0, 1.0, vcc
	v_cmp_eq_u32_e32 vcc, v104, v111
	s_waitcnt vmcnt(18)
	v_pk_fma_f32 v[42:43], v[242:243], v[42:43], v[52:53] op_sel_hi:[0,1,1] neg_lo:[1,0,0] neg_hi:[1,0,0]
	v_cvt_pk_bf16_f32 v42, v42, v43
	v_cndmask_b32_e64 v53, 0, 1.0, vcc
	v_cmp_eq_u32_e32 vcc, v105, v111
	s_nop 1
	v_cndmask_b32_e64 v52, 0, 1.0, vcc
	v_pk_fma_f32 v[44:45], v[242:243], v[44:45], v[52:53] op_sel_hi:[0,1,1] neg_lo:[1,0,0] neg_hi:[1,0,0]
	v_cvt_pk_bf16_f32 v43, v44, v45
	ds_write_b64 v186, v[42:43] offset:2720
	v_cmp_eq_u32_e32 vcc, v99, v112
	s_nop 1
	v_cndmask_b32_e64 v44, 0, 1.0, vcc
	v_cmp_eq_u32_e32 vcc, v102, v112
	s_nop 1
	v_cndmask_b32_e64 v45, 0, 1.0, vcc
	v_cmp_eq_u32_e32 vcc, v104, v112
	s_waitcnt vmcnt(17)
	v_pk_fma_f32 v[38:39], v[244:245], v[38:39], v[44:45] op_sel_hi:[0,1,1] neg_lo:[1,0,0] neg_hi:[1,0,0]
	v_cvt_pk_bf16_f32 v38, v38, v39
	v_cndmask_b32_e64 v45, 0, 1.0, vcc
	v_cmp_eq_u32_e32 vcc, v105, v112
	s_nop 1
	v_cndmask_b32_e64 v44, 0, 1.0, vcc
	v_pk_fma_f32 v[40:41], v[244:245], v[40:41], v[44:45] op_sel_hi:[0,1,1] neg_lo:[1,0,0] neg_hi:[1,0,0]
	v_cvt_pk_bf16_f32 v39, v40, v41
	ds_write_b64 v186, v[38:39] offset:3264
	v_cmp_eq_u32_e32 vcc, v99, v113
	s_nop 1
	v_cndmask_b32_e64 v40, 0, 1.0, vcc
	v_cmp_eq_u32_e32 vcc, v102, v113
	s_nop 1
	v_cndmask_b32_e64 v41, 0, 1.0, vcc
	v_cmp_eq_u32_e32 vcc, v104, v113
	s_waitcnt vmcnt(16)
	v_pk_fma_f32 v[34:35], v[246:247], v[34:35], v[40:41] op_sel_hi:[0,1,1] neg_lo:[1,0,0] neg_hi:[1,0,0]
	v_cvt_pk_bf16_f32 v34, v34, v35
	v_cndmask_b32_e64 v41, 0, 1.0, vcc
	v_cmp_eq_u32_e32 vcc, v105, v113
	s_nop 1
	v_cndmask_b32_e64 v40, 0, 1.0, vcc
	v_pk_fma_f32 v[36:37], v[246:247], v[36:37], v[40:41] op_sel_hi:[0,1,1] neg_lo:[1,0,0] neg_hi:[1,0,0]
	v_cvt_pk_bf16_f32 v35, v36, v37
	ds_write_b64 v186, v[34:35] offset:3808
	ds_read_b128 v[232:235], v1
	ds_read_b128 v[236:239], v1 offset:64
	ds_read_b128 v[240:243], v1 offset:128
	ds_read_b128 v[244:247], v1 offset:192
	s_waitcnt lgkmcnt(0)
	ds_write_b128 v184, v[232:235] offset:4096
	ds_write_b128 v184, v[236:239] offset:5120
	ds_write_b128 v184, v[240:243] offset:6144
	ds_write_b128 v184, v[244:247] offset:7168
	ds_read_b32 v232, v187 offset:192
	ds_read_b32 v234, v187 offset:200
	ds_read_b32 v236, v187 offset:208
	ds_read_b32 v238, v187 offset:216
	ds_read_b32 v240, v187 offset:224
	ds_read_b32 v242, v187 offset:232
	ds_read_b32 v244, v187 offset:240
	ds_read_b32 v246, v187 offset:248
	s_lshl_b32 s28, s24, 2
	s_mov_b32 s29, s21
	v_lshl_add_u64 v[34:35], v[126:127], 0, s[28:29]
	v_lshl_add_u64 v[36:37], v[128:129], 0, s[28:29]
	v_lshl_add_u64 v[38:39], v[134:135], 0, s[28:29]
	v_lshl_add_u64 v[40:41], v[136:137], 0, s[28:29]
	v_lshl_add_u64 v[42:43], v[138:139], 0, s[28:29]
	v_lshl_add_u64 v[44:45], v[140:141], 0, s[28:29]
	v_lshl_add_u64 v[50:51], v[142:143], 0, s[28:29]
	v_lshl_add_u64 v[52:53], v[144:145], 0, s[28:29]
	global_load_dwordx4 v[122:125], v[34:35], off nt
	global_load_dwordx4 v[114:117], v[36:37], off nt
	global_load_dwordx4 v[106:109], v[38:39], off nt
	global_load_dwordx4 v[86:89], v[40:41], off nt
	global_load_dwordx4 v[74:77], v[42:43], off nt
	s_nop 0
	global_load_dwordx4 v[42:45], v[44:45], off nt
	s_nop 0
	global_load_dwordx4 v[38:41], v[50:51], off nt
	global_load_dwordx4 v[34:37], v[52:53], off nt
	v_mov_b32_e32 v50, v188
	s_waitcnt lgkmcnt(0)
	s_waitcnt vmcnt(23)
	v_pk_fma_f32 v[30:31], v[232:233], v[30:31], 0 op_sel_hi:[0,1,0] neg_lo:[1,0,0] neg_hi:[1,0,0]
	v_pk_fma_f32 v[32:33], v[232:233], v[32:33], 0 op_sel_hi:[0,1,0] neg_lo:[1,0,0] neg_hi:[1,0,0]
	v_cvt_pk_bf16_f32 v30, v30, v31
	v_cvt_pk_bf16_f32 v31, v32, v33
	ds_write_b64 v186, v[30:31]
	s_waitcnt vmcnt(22)
	v_pk_fma_f32 v[26:27], v[234:235], v[26:27], 0 op_sel_hi:[0,1,0] neg_lo:[1,0,0] neg_hi:[1,0,0]
	v_pk_fma_f32 v[28:29], v[234:235], v[28:29], 0 op_sel_hi:[0,1,0] neg_lo:[1,0,0] neg_hi:[1,0,0]
	v_cvt_pk_bf16_f32 v26, v26, v27
	v_cvt_pk_bf16_f32 v27, v28, v29
	ds_write_b64 v186, v[26:27] offset:544
	s_waitcnt vmcnt(21)
	v_pk_fma_f32 v[22:23], v[236:237], v[22:23], 0 op_sel_hi:[0,1,0] neg_lo:[1,0,0] neg_hi:[1,0,0]
	v_pk_fma_f32 v[24:25], v[236:237], v[24:25], 0 op_sel_hi:[0,1,0] neg_lo:[1,0,0] neg_hi:[1,0,0]
	v_cvt_pk_bf16_f32 v22, v22, v23
	v_cvt_pk_bf16_f32 v23, v24, v25
	ds_write_b64 v186, v[22:23] offset:1088
	s_waitcnt vmcnt(20)
	v_pk_fma_f32 v[18:19], v[238:239], v[18:19], 0 op_sel_hi:[0,1,0] neg_lo:[1,0,0] neg_hi:[1,0,0]
	v_pk_fma_f32 v[20:21], v[238:239], v[20:21], 0 op_sel_hi:[0,1,0] neg_lo:[1,0,0] neg_hi:[1,0,0]
	v_cvt_pk_bf16_f32 v18, v18, v19
	v_cvt_pk_bf16_f32 v19, v20, v21
	ds_write_b64 v186, v[18:19] offset:1632
	s_waitcnt vmcnt(19)
	v_pk_fma_f32 v[14:15], v[240:241], v[14:15], 0 op_sel_hi:[0,1,0] neg_lo:[1,0,0] neg_hi:[1,0,0]
	v_pk_fma_f32 v[16:17], v[240:241], v[16:17], 0 op_sel_hi:[0,1,0] neg_lo:[1,0,0] neg_hi:[1,0,0]
	v_cvt_pk_bf16_f32 v14, v14, v15
	v_cvt_pk_bf16_f32 v15, v16, v17
	ds_write_b64 v186, v[14:15] offset:2176
	s_waitcnt vmcnt(18)
	v_pk_fma_f32 v[10:11], v[242:243], v[10:11], 0 op_sel_hi:[0,1,0] neg_lo:[1,0,0] neg_hi:[1,0,0]
	v_pk_fma_f32 v[12:13], v[242:243], v[12:13], 0 op_sel_hi:[0,1,0] neg_lo:[1,0,0] neg_hi:[1,0,0]
	v_cvt_pk_bf16_f32 v10, v10, v11
	v_cvt_pk_bf16_f32 v11, v12, v13
	ds_write_b64 v186, v[10:11] offset:2720
	s_waitcnt vmcnt(17)
	v_pk_fma_f32 v[6:7], v[244:245], v[6:7], 0 op_sel_hi:[0,1,0] neg_lo:[1,0,0] neg_hi:[1,0,0]
	v_pk_fma_f32 v[8:9], v[244:245], v[8:9], 0 op_sel_hi:[0,1,0] neg_lo:[1,0,0] neg_hi:[1,0,0]
	v_cvt_pk_bf16_f32 v6, v6, v7
	v_cvt_pk_bf16_f32 v7, v8, v9
	ds_write_b64 v186, v[6:7] offset:3264
	s_waitcnt vmcnt(16)
	v_pk_fma_f32 v[2:3], v[246:247], v[2:3], 0 op_sel_hi:[0,1,0] neg_lo:[1,0,0] neg_hi:[1,0,0]
	v_pk_fma_f32 v[4:5], v[246:247], v[4:5], 0 op_sel_hi:[0,1,0] neg_lo:[1,0,0] neg_hi:[1,0,0]
	v_cvt_pk_bf16_f32 v2, v2, v3
	v_cvt_pk_bf16_f32 v3, v4, v5
	ds_write_b64 v186, v[2:3] offset:3808
	ds_read_b128 v[232:235], v1
	ds_read_b128 v[236:239], v1 offset:64
	ds_read_b128 v[240:243], v1 offset:128
	ds_read_b128 v[244:247], v1 offset:192
	s_waitcnt lgkmcnt(0)
	ds_write_b128 v184, v[232:235] offset:8192
	ds_write_b128 v184, v[236:239] offset:9216
	ds_write_b128 v184, v[240:243] offset:10240
	ds_write_b128 v184, v[244:247] offset:11264
	ds_read_b32 v232, v187 offset:192
	ds_read_b32 v234, v187 offset:200
	ds_read_b32 v236, v187 offset:208
	ds_read_b32 v238, v187 offset:216
	ds_read_b32 v240, v187 offset:224
	ds_read_b32 v242, v187 offset:232
	ds_read_b32 v244, v187 offset:240
	ds_read_b32 v246, v187 offset:248
	s_lshl_b32 s26, s23, 2
	s_mov_b32 s27, s21
	v_lshl_add_u64 v[2:3], v[126:127], 0, s[26:27]
	v_lshl_add_u64 v[4:5], v[128:129], 0, s[26:27]
	v_lshl_add_u64 v[6:7], v[134:135], 0, s[26:27]
	v_lshl_add_u64 v[8:9], v[136:137], 0, s[26:27]
	v_lshl_add_u64 v[10:11], v[138:139], 0, s[26:27]
	v_lshl_add_u64 v[12:13], v[140:141], 0, s[26:27]
	v_lshl_add_u64 v[14:15], v[142:143], 0, s[26:27]
	v_lshl_add_u64 v[16:17], v[144:145], 0, s[26:27]
	global_load_dwordx4 v[118:121], v[2:3], off nt
	global_load_dwordx4 v[110:113], v[4:5], off nt
	global_load_dwordx4 v[102:105], v[6:7], off nt
	global_load_dwordx4 v[98:101], v[8:9], off nt
	global_load_dwordx4 v[58:61], v[10:11], off nt
	global_load_dwordx4 v[50:53], v[12:13], off nt
	global_load_dwordx4 v[30:33], v[14:15], off nt
	global_load_dwordx4 v[22:25], v[16:17], off nt
	v_mov_b32_e32 v2, v198
	s_waitcnt lgkmcnt(0)
	s_waitcnt vmcnt(23)
	v_pk_fma_f32 v[4:5], v[232:233], v[90:91], 0 op_sel_hi:[0,1,0] neg_lo:[1,0,0] neg_hi:[1,0,0]
	v_pk_fma_f32 v[2:3], v[232:233], v[92:93], 0 op_sel_hi:[0,1,0] neg_lo:[1,0,0] neg_hi:[1,0,0]
	v_cvt_pk_bf16_f32 v4, v4, v5
	v_cvt_pk_bf16_f32 v5, v2, v3
	ds_write_b64 v186, v[4:5]
	s_waitcnt vmcnt(22)
	v_pk_fma_f32 v[4:5], v[234:235], v[82:83], 0 op_sel_hi:[0,1,0] neg_lo:[1,0,0] neg_hi:[1,0,0]
	v_pk_fma_f32 v[2:3], v[234:235], v[84:85], 0 op_sel_hi:[0,1,0] neg_lo:[1,0,0] neg_hi:[1,0,0]
	v_cvt_pk_bf16_f32 v4, v4, v5
	v_cvt_pk_bf16_f32 v5, v2, v3
	ds_write_b64 v186, v[4:5] offset:544
	s_waitcnt vmcnt(21)
	v_pk_fma_f32 v[4:5], v[236:237], v[78:79], 0 op_sel_hi:[0,1,0] neg_lo:[1,0,0] neg_hi:[1,0,0]
	v_pk_fma_f32 v[2:3], v[236:237], v[80:81], 0 op_sel_hi:[0,1,0] neg_lo:[1,0,0] neg_hi:[1,0,0]
	v_cvt_pk_bf16_f32 v4, v4, v5
	v_cvt_pk_bf16_f32 v5, v2, v3
	ds_write_b64 v186, v[4:5] offset:1088
	s_waitcnt vmcnt(20)
	v_pk_fma_f32 v[4:5], v[238:239], v[70:71], 0 op_sel_hi:[0,1,0] neg_lo:[1,0,0] neg_hi:[1,0,0]
	v_pk_fma_f32 v[2:3], v[238:239], v[72:73], 0 op_sel_hi:[0,1,0] neg_lo:[1,0,0] neg_hi:[1,0,0]
	v_cvt_pk_bf16_f32 v4, v4, v5
	v_cvt_pk_bf16_f32 v5, v2, v3
	ds_write_b64 v186, v[4:5] offset:1632
	s_waitcnt vmcnt(19)
	v_pk_fma_f32 v[4:5], v[240:241], v[66:67], 0 op_sel_hi:[0,1,0] neg_lo:[1,0,0] neg_hi:[1,0,0]
	v_pk_fma_f32 v[2:3], v[240:241], v[68:69], 0 op_sel_hi:[0,1,0] neg_lo:[1,0,0] neg_hi:[1,0,0]
	v_cvt_pk_bf16_f32 v4, v4, v5
	v_cvt_pk_bf16_f32 v5, v2, v3
	ds_write_b64 v186, v[4:5] offset:2176
	s_waitcnt vmcnt(18)
	v_pk_fma_f32 v[4:5], v[242:243], v[62:63], 0 op_sel_hi:[0,1,0] neg_lo:[1,0,0] neg_hi:[1,0,0]
	v_pk_fma_f32 v[2:3], v[242:243], v[64:65], 0 op_sel_hi:[0,1,0] neg_lo:[1,0,0] neg_hi:[1,0,0]
	v_cvt_pk_bf16_f32 v4, v4, v5
	v_cvt_pk_bf16_f32 v5, v2, v3
	ds_write_b64 v186, v[4:5] offset:2720
	s_waitcnt vmcnt(17)
	v_pk_fma_f32 v[4:5], v[244:245], v[54:55], 0 op_sel_hi:[0,1,0] neg_lo:[1,0,0] neg_hi:[1,0,0]
	v_pk_fma_f32 v[2:3], v[244:245], v[56:57], 0 op_sel_hi:[0,1,0] neg_lo:[1,0,0] neg_hi:[1,0,0]
	v_cvt_pk_bf16_f32 v4, v4, v5
	v_cvt_pk_bf16_f32 v5, v2, v3
	ds_write_b64 v186, v[4:5] offset:3264
	s_waitcnt vmcnt(16)
	v_pk_fma_f32 v[4:5], v[246:247], v[46:47], 0 op_sel_hi:[0,1,0] neg_lo:[1,0,0] neg_hi:[1,0,0]
	v_pk_fma_f32 v[2:3], v[246:247], v[48:49], 0 op_sel_hi:[0,1,0] neg_lo:[1,0,0] neg_hi:[1,0,0]
	v_cvt_pk_bf16_f32 v4, v4, v5
	v_cvt_pk_bf16_f32 v5, v2, v3
	ds_write_b64 v186, v[4:5] offset:3808
	ds_read_b128 v[232:235], v1
	ds_read_b128 v[236:239], v1 offset:64
	ds_read_b128 v[240:243], v1 offset:128
	ds_read_b128 v[244:247], v1 offset:192
	s_waitcnt lgkmcnt(0)
	ds_write_b128 v184, v[232:235] offset:12288
	ds_write_b128 v184, v[236:239] offset:13312
	ds_write_b128 v184, v[240:243] offset:14336
	ds_write_b128 v184, v[244:247] offset:15360
	ds_read_b32 v232, v187 offset:192
	ds_read_b32 v234, v187 offset:200
	ds_read_b32 v236, v187 offset:208
	ds_read_b32 v238, v187 offset:216
	ds_read_b32 v240, v187 offset:224
	ds_read_b32 v242, v187 offset:232
	ds_read_b32 v244, v187 offset:240
	ds_read_b32 v246, v187 offset:248
	s_lshl_b32 s24, s22, 2
	s_mov_b32 s25, s21
	v_lshl_add_u64 v[2:3], v[126:127], 0, s[24:25]
	v_lshl_add_u64 v[6:7], v[134:135], 0, s[24:25]
	v_lshl_add_u64 v[8:9], v[136:137], 0, s[24:25]
	v_lshl_add_u64 v[14:15], v[142:143], 0, s[24:25]
	v_lshl_add_u64 v[4:5], v[128:129], 0, s[24:25]
	v_lshl_add_u64 v[10:11], v[138:139], 0, s[24:25]
	v_lshl_add_u64 v[12:13], v[140:141], 0, s[24:25]
	v_lshl_add_u64 v[18:19], v[144:145], 0, s[24:25]
	global_load_dwordx4 v[94:97], v[2:3], off nt
	global_load_dwordx4 v[90:93], v[4:5], off nt
	global_load_dwordx4 v[82:85], v[6:7], off nt
	global_load_dwordx4 v[70:73], v[8:9], off nt
	global_load_dwordx4 v[54:57], v[10:11], off nt
	global_load_dwordx4 v[26:29], v[12:13], off nt
	s_nop 0
	global_load_dwordx4 v[14:17], v[14:15], off nt
	s_nop 0
	global_load_dwordx4 v[6:9], v[18:19], off nt
	v_mov_b32_e32 v2, v197
	s_waitcnt lgkmcnt(0)
	s_waitcnt vmcnt(23)
	v_pk_fma_f32 v[4:5], v[232:233], v[122:123], 0 op_sel_hi:[0,1,0] neg_lo:[1,0,0] neg_hi:[1,0,0]
	v_pk_fma_f32 v[2:3], v[232:233], v[124:125], 0 op_sel_hi:[0,1,0] neg_lo:[1,0,0] neg_hi:[1,0,0]
	v_cvt_pk_bf16_f32 v4, v4, v5
	v_cvt_pk_bf16_f32 v5, v2, v3
	ds_write_b64 v186, v[4:5]
	s_waitcnt vmcnt(22)
	v_pk_fma_f32 v[4:5], v[234:235], v[114:115], 0 op_sel_hi:[0,1,0] neg_lo:[1,0,0] neg_hi:[1,0,0]
	v_pk_fma_f32 v[2:3], v[234:235], v[116:117], 0 op_sel_hi:[0,1,0] neg_lo:[1,0,0] neg_hi:[1,0,0]
	v_cvt_pk_bf16_f32 v4, v4, v5
	v_cvt_pk_bf16_f32 v5, v2, v3
	ds_write_b64 v186, v[4:5] offset:544
	s_waitcnt vmcnt(21)
	v_pk_fma_f32 v[4:5], v[236:237], v[106:107], 0 op_sel_hi:[0,1,0] neg_lo:[1,0,0] neg_hi:[1,0,0]
	v_pk_fma_f32 v[2:3], v[236:237], v[108:109], 0 op_sel_hi:[0,1,0] neg_lo:[1,0,0] neg_hi:[1,0,0]
	v_cvt_pk_bf16_f32 v4, v4, v5
	v_cvt_pk_bf16_f32 v5, v2, v3
	ds_write_b64 v186, v[4:5] offset:1088
	s_waitcnt vmcnt(20)
	v_pk_fma_f32 v[4:5], v[238:239], v[86:87], 0 op_sel_hi:[0,1,0] neg_lo:[1,0,0] neg_hi:[1,0,0]
	v_pk_fma_f32 v[2:3], v[238:239], v[88:89], 0 op_sel_hi:[0,1,0] neg_lo:[1,0,0] neg_hi:[1,0,0]
	v_cvt_pk_bf16_f32 v4, v4, v5
	v_cvt_pk_bf16_f32 v5, v2, v3
	ds_write_b64 v186, v[4:5] offset:1632
	s_waitcnt vmcnt(19)
	v_pk_fma_f32 v[4:5], v[240:241], v[74:75], 0 op_sel_hi:[0,1,0] neg_lo:[1,0,0] neg_hi:[1,0,0]
	v_pk_fma_f32 v[2:3], v[240:241], v[76:77], 0 op_sel_hi:[0,1,0] neg_lo:[1,0,0] neg_hi:[1,0,0]
	v_cvt_pk_bf16_f32 v4, v4, v5
	v_cvt_pk_bf16_f32 v5, v2, v3
	ds_write_b64 v186, v[4:5] offset:2176
	s_waitcnt vmcnt(18)
	v_pk_fma_f32 v[4:5], v[242:243], v[42:43], 0 op_sel_hi:[0,1,0] neg_lo:[1,0,0] neg_hi:[1,0,0]
	v_pk_fma_f32 v[2:3], v[242:243], v[44:45], 0 op_sel_hi:[0,1,0] neg_lo:[1,0,0] neg_hi:[1,0,0]
	v_cvt_pk_bf16_f32 v4, v4, v5
	v_cvt_pk_bf16_f32 v5, v2, v3
	ds_write_b64 v186, v[4:5] offset:2720
	s_waitcnt vmcnt(17)
	v_pk_fma_f32 v[4:5], v[244:245], v[38:39], 0 op_sel_hi:[0,1,0] neg_lo:[1,0,0] neg_hi:[1,0,0]
	v_pk_fma_f32 v[2:3], v[244:245], v[40:41], 0 op_sel_hi:[0,1,0] neg_lo:[1,0,0] neg_hi:[1,0,0]
	v_cvt_pk_bf16_f32 v4, v4, v5
	v_cvt_pk_bf16_f32 v5, v2, v3
	ds_write_b64 v186, v[4:5] offset:3264
	s_waitcnt vmcnt(16)
	v_pk_fma_f32 v[4:5], v[246:247], v[34:35], 0 op_sel_hi:[0,1,0] neg_lo:[1,0,0] neg_hi:[1,0,0]
	v_pk_fma_f32 v[2:3], v[246:247], v[36:37], 0 op_sel_hi:[0,1,0] neg_lo:[1,0,0] neg_hi:[1,0,0]
	v_cvt_pk_bf16_f32 v4, v4, v5
	v_cvt_pk_bf16_f32 v5, v2, v3
	ds_write_b64 v186, v[4:5] offset:3808
	ds_read_b128 v[232:235], v1
	ds_read_b128 v[236:239], v1 offset:64
	ds_read_b128 v[240:243], v1 offset:128
	ds_read_b128 v[244:247], v1 offset:192
	s_waitcnt lgkmcnt(0)
	ds_write_b128 v184, v[232:235] offset:16384
	ds_write_b128 v184, v[236:239] offset:17408
	ds_write_b128 v184, v[240:243] offset:18432
	ds_write_b128 v184, v[244:247] offset:19456
	ds_read_b32 v232, v187 offset:192
	ds_read_b32 v234, v187 offset:200
	ds_read_b32 v236, v187 offset:208
	ds_read_b32 v238, v187 offset:216
	ds_read_b32 v240, v187 offset:224
	ds_read_b32 v242, v187 offset:232
	ds_read_b32 v244, v187 offset:240
	ds_read_b32 v246, v187 offset:248
	s_lshl_b32 s22, s7, 2
	s_mov_b32 s23, s21
	v_lshl_add_u64 v[2:3], v[126:127], 0, s[22:23]
	v_lshl_add_u64 v[4:5], v[128:129], 0, s[22:23]
	v_lshl_add_u64 v[10:11], v[134:135], 0, s[22:23]
	v_lshl_add_u64 v[12:13], v[136:137], 0, s[22:23]
	v_lshl_add_u64 v[34:35], v[138:139], 0, s[22:23]
	v_lshl_add_u64 v[36:37], v[140:141], 0, s[22:23]
	v_lshl_add_u64 v[46:47], v[142:143], 0, s[22:23]
	v_lshl_add_u64 v[48:49], v[144:145], 0, s[22:23]
	global_load_dwordx4 v[86:89], v[2:3], off nt
	global_load_dwordx4 v[78:81], v[4:5], off nt
	global_load_dwordx4 v[66:69], v[10:11], off nt
	global_load_dwordx4 v[42:45], v[12:13], off nt
	global_load_dwordx4 v[38:41], v[34:35], off nt
	global_load_dwordx4 v[18:21], v[36:37], off nt
	s_nop 0
	global_load_dwordx4 v[10:13], v[46:47], off nt
	global_load_dwordx4 v[2:5], v[48:49], off nt
	v_mov_b32_e32 v34, v196
	s_waitcnt lgkmcnt(0)
	s_waitcnt vmcnt(23)
	v_pk_fma_f32 v[36:37], v[232:233], v[118:119], 0 op_sel_hi:[0,1,0] neg_lo:[1,0,0] neg_hi:[1,0,0]
	v_pk_fma_f32 v[34:35], v[232:233], v[120:121], 0 op_sel_hi:[0,1,0] neg_lo:[1,0,0] neg_hi:[1,0,0]
	v_cvt_pk_bf16_f32 v36, v36, v37
	v_cvt_pk_bf16_f32 v37, v34, v35
	ds_write_b64 v186, v[36:37]
	s_waitcnt vmcnt(22)
	v_pk_fma_f32 v[36:37], v[234:235], v[110:111], 0 op_sel_hi:[0,1,0] neg_lo:[1,0,0] neg_hi:[1,0,0]
	v_pk_fma_f32 v[34:35], v[234:235], v[112:113], 0 op_sel_hi:[0,1,0] neg_lo:[1,0,0] neg_hi:[1,0,0]
	v_cvt_pk_bf16_f32 v36, v36, v37
	v_cvt_pk_bf16_f32 v37, v34, v35
	ds_write_b64 v186, v[36:37] offset:544
	s_waitcnt vmcnt(21)
	v_pk_fma_f32 v[36:37], v[236:237], v[102:103], 0 op_sel_hi:[0,1,0] neg_lo:[1,0,0] neg_hi:[1,0,0]
	v_pk_fma_f32 v[34:35], v[236:237], v[104:105], 0 op_sel_hi:[0,1,0] neg_lo:[1,0,0] neg_hi:[1,0,0]
	v_cvt_pk_bf16_f32 v36, v36, v37
	v_cvt_pk_bf16_f32 v37, v34, v35
	ds_write_b64 v186, v[36:37] offset:1088
	s_waitcnt vmcnt(20)
	v_pk_fma_f32 v[36:37], v[238:239], v[98:99], 0 op_sel_hi:[0,1,0] neg_lo:[1,0,0] neg_hi:[1,0,0]
	v_pk_fma_f32 v[34:35], v[238:239], v[100:101], 0 op_sel_hi:[0,1,0] neg_lo:[1,0,0] neg_hi:[1,0,0]
	v_cvt_pk_bf16_f32 v36, v36, v37
	v_cvt_pk_bf16_f32 v37, v34, v35
	ds_write_b64 v186, v[36:37] offset:1632
	s_waitcnt vmcnt(19)
	v_pk_fma_f32 v[36:37], v[240:241], v[58:59], 0 op_sel_hi:[0,1,0] neg_lo:[1,0,0] neg_hi:[1,0,0]
	v_pk_fma_f32 v[34:35], v[240:241], v[60:61], 0 op_sel_hi:[0,1,0] neg_lo:[1,0,0] neg_hi:[1,0,0]
	v_cvt_pk_bf16_f32 v36, v36, v37
	v_cvt_pk_bf16_f32 v37, v34, v35
	ds_write_b64 v186, v[36:37] offset:2176
	s_waitcnt vmcnt(18)
	v_pk_fma_f32 v[36:37], v[242:243], v[50:51], 0 op_sel_hi:[0,1,0] neg_lo:[1,0,0] neg_hi:[1,0,0]
	v_pk_fma_f32 v[34:35], v[242:243], v[52:53], 0 op_sel_hi:[0,1,0] neg_lo:[1,0,0] neg_hi:[1,0,0]
	v_cvt_pk_bf16_f32 v36, v36, v37
	v_cvt_pk_bf16_f32 v37, v34, v35
	ds_write_b64 v186, v[36:37] offset:2720
	s_waitcnt vmcnt(17)
	v_pk_fma_f32 v[30:31], v[244:245], v[30:31], 0 op_sel_hi:[0,1,0] neg_lo:[1,0,0] neg_hi:[1,0,0]
	v_pk_fma_f32 v[32:33], v[244:245], v[32:33], 0 op_sel_hi:[0,1,0] neg_lo:[1,0,0] neg_hi:[1,0,0]
	v_cvt_pk_bf16_f32 v30, v30, v31
	v_cvt_pk_bf16_f32 v31, v32, v33
	ds_write_b64 v186, v[30:31] offset:3264
	s_waitcnt vmcnt(16)
	v_pk_fma_f32 v[22:23], v[246:247], v[22:23], 0 op_sel_hi:[0,1,0] neg_lo:[1,0,0] neg_hi:[1,0,0]
	v_pk_fma_f32 v[24:25], v[246:247], v[24:25], 0 op_sel_hi:[0,1,0] neg_lo:[1,0,0] neg_hi:[1,0,0]
	v_cvt_pk_bf16_f32 v22, v22, v23
	v_cvt_pk_bf16_f32 v23, v24, v25
	ds_write_b64 v186, v[22:23] offset:3808
	ds_read_b128 v[232:235], v1
	ds_read_b128 v[236:239], v1 offset:64
	ds_read_b128 v[240:243], v1 offset:128
	ds_read_b128 v[244:247], v1 offset:192
	s_waitcnt lgkmcnt(0)
	ds_write_b128 v184, v[232:235] offset:20480
	ds_write_b128 v184, v[236:239] offset:21504
	ds_write_b128 v184, v[240:243] offset:22528
	ds_write_b128 v184, v[244:247] offset:23552
	ds_read_b32 v232, v187 offset:192
	ds_read_b32 v234, v187 offset:200
	ds_read_b32 v236, v187 offset:208
	ds_read_b32 v238, v187 offset:216
	ds_read_b32 v240, v187 offset:224
	ds_read_b32 v242, v187 offset:232
	ds_read_b32 v244, v187 offset:240
	ds_read_b32 v246, v187 offset:248
	v_lshl_add_u64 v[22:23], v[130:131], 0, s[30:31]
	s_movk_i32 s7, 0x2000
	v_add_co_u32_e32 v24, vcc, s7, v22
	s_movk_i32 s36, 0x4000
	s_nop 0
	v_addc_co_u32_e32 v25, vcc, 0, v23, vcc
	global_load_dwordx4 v[74:77], v[22:23], off nt
	global_load_dwordx4 v[62:65], v[24:25], off nt
	v_add_co_u32_e32 v24, vcc, s36, v22
	s_movk_i32 s37, 0x6000
	s_nop 0
	v_addc_co_u32_e32 v25, vcc, 0, v23, vcc
	v_add_co_u32_e32 v30, vcc, s37, v22
	s_mov_b32 s38, 0x8000
	s_nop 0
	v_addc_co_u32_e32 v31, vcc, 0, v23, vcc
	global_load_dwordx4 v[58:61], v[24:25], off nt
	global_load_dwordx4 v[46:49], v[30:31], off nt
	v_add_co_u32_e32 v24, vcc, s38, v22
	s_mov_b32 s39, 0xa000
	s_nop 0
	v_addc_co_u32_e32 v25, vcc, 0, v23, vcc
	v_add_co_u32_e32 v34, vcc, s39, v22
	s_mov_b32 s41, 0xc000
	s_nop 0
	v_addc_co_u32_e32 v35, vcc, 0, v23, vcc
	global_load_dwordx4 v[50:53], v[24:25], off nt
	global_load_dwordx4 v[30:33], v[34:35], off nt
	v_add_co_u32_e32 v24, vcc, s41, v22
	s_mov_b32 s42, 0xe000
	s_nop 0
	v_addc_co_u32_e32 v25, vcc, 0, v23, vcc
	v_add_co_u32_e32 v22, vcc, s42, v22
	s_nop 1
	v_addc_co_u32_e32 v23, vcc, 0, v23, vcc
	global_load_dwordx4 v[34:37], v[24:25], off nt
	s_nop 0
	global_load_dwordx4 v[22:25], v[22:23], off nt
	v_mov_b32_e32 v98, v195
	s_waitcnt lgkmcnt(0)
	s_waitcnt vmcnt(23)
	v_pk_fma_f32 v[94:95], v[232:233], v[94:95], 0 op_sel_hi:[0,1,0] neg_lo:[1,0,0] neg_hi:[1,0,0]
	v_pk_fma_f32 v[96:97], v[232:233], v[96:97], 0 op_sel_hi:[0,1,0] neg_lo:[1,0,0] neg_hi:[1,0,0]
	v_cvt_pk_bf16_f32 v94, v94, v95
	v_cvt_pk_bf16_f32 v95, v96, v97
	ds_write_b64 v186, v[94:95]
	s_waitcnt vmcnt(22)
	v_pk_fma_f32 v[90:91], v[234:235], v[90:91], 0 op_sel_hi:[0,1,0] neg_lo:[1,0,0] neg_hi:[1,0,0]
	v_pk_fma_f32 v[92:93], v[234:235], v[92:93], 0 op_sel_hi:[0,1,0] neg_lo:[1,0,0] neg_hi:[1,0,0]
	v_cvt_pk_bf16_f32 v90, v90, v91
	v_cvt_pk_bf16_f32 v91, v92, v93
	ds_write_b64 v186, v[90:91] offset:544
	s_waitcnt vmcnt(21)
	v_pk_fma_f32 v[82:83], v[236:237], v[82:83], 0 op_sel_hi:[0,1,0] neg_lo:[1,0,0] neg_hi:[1,0,0]
	v_pk_fma_f32 v[84:85], v[236:237], v[84:85], 0 op_sel_hi:[0,1,0] neg_lo:[1,0,0] neg_hi:[1,0,0]
	v_cvt_pk_bf16_f32 v82, v82, v83
	v_cvt_pk_bf16_f32 v83, v84, v85
	ds_write_b64 v186, v[82:83] offset:1088
	s_waitcnt vmcnt(20)
	v_pk_fma_f32 v[70:71], v[238:239], v[70:71], 0 op_sel_hi:[0,1,0] neg_lo:[1,0,0] neg_hi:[1,0,0]
	v_pk_fma_f32 v[72:73], v[238:239], v[72:73], 0 op_sel_hi:[0,1,0] neg_lo:[1,0,0] neg_hi:[1,0,0]
	v_cvt_pk_bf16_f32 v70, v70, v71
	v_cvt_pk_bf16_f32 v71, v72, v73
	ds_write_b64 v186, v[70:71] offset:1632
	s_waitcnt vmcnt(19)
	v_pk_fma_f32 v[54:55], v[240:241], v[54:55], 0 op_sel_hi:[0,1,0] neg_lo:[1,0,0] neg_hi:[1,0,0]
	v_pk_fma_f32 v[56:57], v[240:241], v[56:57], 0 op_sel_hi:[0,1,0] neg_lo:[1,0,0] neg_hi:[1,0,0]
	v_cvt_pk_bf16_f32 v54, v54, v55
	v_cvt_pk_bf16_f32 v55, v56, v57
	ds_write_b64 v186, v[54:55] offset:2176
	s_waitcnt vmcnt(18)
	v_pk_fma_f32 v[26:27], v[242:243], v[26:27], 0 op_sel_hi:[0,1,0] neg_lo:[1,0,0] neg_hi:[1,0,0]
	v_pk_fma_f32 v[28:29], v[242:243], v[28:29], 0 op_sel_hi:[0,1,0] neg_lo:[1,0,0] neg_hi:[1,0,0]
	v_cvt_pk_bf16_f32 v26, v26, v27
	v_cvt_pk_bf16_f32 v27, v28, v29
	ds_write_b64 v186, v[26:27] offset:2720
	s_waitcnt vmcnt(17)
	v_pk_fma_f32 v[14:15], v[244:245], v[14:15], 0 op_sel_hi:[0,1,0] neg_lo:[1,0,0] neg_hi:[1,0,0]
	v_pk_fma_f32 v[16:17], v[244:245], v[16:17], 0 op_sel_hi:[0,1,0] neg_lo:[1,0,0] neg_hi:[1,0,0]
	v_cvt_pk_bf16_f32 v14, v14, v15
	v_cvt_pk_bf16_f32 v15, v16, v17
	ds_write_b64 v186, v[14:15] offset:3264
	s_waitcnt vmcnt(16)
	v_pk_fma_f32 v[6:7], v[246:247], v[6:7], 0 op_sel_hi:[0,1,0] neg_lo:[1,0,0] neg_hi:[1,0,0]
	v_pk_fma_f32 v[8:9], v[246:247], v[8:9], 0 op_sel_hi:[0,1,0] neg_lo:[1,0,0] neg_hi:[1,0,0]
	v_cvt_pk_bf16_f32 v6, v6, v7
	v_cvt_pk_bf16_f32 v7, v8, v9
	ds_write_b64 v186, v[6:7] offset:3808
	ds_read_b128 v[232:235], v1
	ds_read_b128 v[236:239], v1 offset:64
	ds_read_b128 v[240:243], v1 offset:128
	ds_read_b128 v[244:247], v1 offset:192
	s_waitcnt lgkmcnt(0)
	ds_write_b128 v184, v[232:235] offset:24576
	ds_write_b128 v184, v[236:239] offset:25600
	ds_write_b128 v184, v[240:243] offset:26624
	ds_write_b128 v184, v[244:247] offset:27648
	ds_read_b32 v232, v187 offset:192
	ds_read_b32 v234, v187 offset:200
	ds_read_b32 v236, v187 offset:208
	ds_read_b32 v238, v187 offset:216
	ds_read_b32 v240, v187 offset:224
	ds_read_b32 v242, v187 offset:232
	ds_read_b32 v244, v187 offset:240
	ds_read_b32 v246, v187 offset:248
	s_mov_b64 s[44:45], 0x10000
	v_lshl_add_u64 v[150:151], v[130:131], 0, s[44:45]
	s_mov_b64 s[44:45], 0x12000
	v_lshl_add_u64 v[152:153], v[130:131], 0, s[44:45]
	s_mov_b64 s[44:45], 0x14000
	v_lshl_add_u64 v[156:157], v[130:131], 0, s[44:45]
	s_mov_b64 s[44:45], 0x16000
	v_lshl_add_u64 v[158:159], v[130:131], 0, s[44:45]
	s_mov_b64 s[44:45], 0x18000
	v_lshl_add_u64 v[160:161], v[130:131], 0, s[44:45]
	s_mov_b64 s[44:45], 0x1a000
	v_lshl_add_u64 v[162:163], v[130:131], 0, s[44:45]
	s_mov_b64 s[44:45], 0x1c000
	v_lshl_add_u64 v[164:165], v[130:131], 0, s[44:45]
	s_mov_b64 s[44:45], 0x1e000
	v_lshl_add_u64 v[6:7], v[150:151], 0, s[30:31]
	v_lshl_add_u64 v[8:9], v[152:153], 0, s[30:31]
	v_lshl_add_u64 v[14:15], v[156:157], 0, s[30:31]
	v_lshl_add_u64 v[16:17], v[158:159], 0, s[30:31]
	v_lshl_add_u64 v[26:27], v[160:161], 0, s[30:31]
	v_lshl_add_u64 v[28:29], v[162:163], 0, s[30:31]
	v_lshl_add_u64 v[166:167], v[130:131], 0, s[44:45]
	v_lshl_add_u64 v[98:99], v[164:165], 0, s[30:31]
	v_lshl_add_u64 v[100:101], v[166:167], 0, s[30:31]
	global_load_dwordx4 v[94:97], v[6:7], off nt
	global_load_dwordx4 v[90:93], v[8:9], off nt
	global_load_dwordx4 v[82:85], v[14:15], off nt
	global_load_dwordx4 v[70:73], v[16:17], off nt
	global_load_dwordx4 v[54:57], v[26:27], off nt
	s_nop 0
	global_load_dwordx4 v[26:29], v[28:29], off nt
	s_nop 0
	global_load_dwordx4 v[14:17], v[98:99], off nt
	global_load_dwordx4 v[6:9], v[100:101], off nt
	v_mov_b32_e32 v98, v194
	s_waitcnt lgkmcnt(0)
	s_waitcnt vmcnt(23)
	v_pk_fma_f32 v[86:87], v[232:233], v[86:87], 0 op_sel_hi:[0,1,0] neg_lo:[1,0,0] neg_hi:[1,0,0]
	v_pk_fma_f32 v[88:89], v[232:233], v[88:89], 0 op_sel_hi:[0,1,0] neg_lo:[1,0,0] neg_hi:[1,0,0]
	v_cvt_pk_bf16_f32 v86, v86, v87
	v_cvt_pk_bf16_f32 v87, v88, v89
	ds_write_b64 v186, v[86:87]
	s_waitcnt vmcnt(22)
	v_pk_fma_f32 v[78:79], v[234:235], v[78:79], 0 op_sel_hi:[0,1,0] neg_lo:[1,0,0] neg_hi:[1,0,0]
	v_pk_fma_f32 v[80:81], v[234:235], v[80:81], 0 op_sel_hi:[0,1,0] neg_lo:[1,0,0] neg_hi:[1,0,0]
	v_cvt_pk_bf16_f32 v78, v78, v79
	v_cvt_pk_bf16_f32 v79, v80, v81
	ds_write_b64 v186, v[78:79] offset:544
	s_waitcnt vmcnt(21)
	v_pk_fma_f32 v[66:67], v[236:237], v[66:67], 0 op_sel_hi:[0,1,0] neg_lo:[1,0,0] neg_hi:[1,0,0]
	v_pk_fma_f32 v[68:69], v[236:237], v[68:69], 0 op_sel_hi:[0,1,0] neg_lo:[1,0,0] neg_hi:[1,0,0]
	v_cvt_pk_bf16_f32 v66, v66, v67
	v_cvt_pk_bf16_f32 v67, v68, v69
	ds_write_b64 v186, v[66:67] offset:1088
	s_waitcnt vmcnt(20)
	v_pk_fma_f32 v[42:43], v[238:239], v[42:43], 0 op_sel_hi:[0,1,0] neg_lo:[1,0,0] neg_hi:[1,0,0]
	v_pk_fma_f32 v[44:45], v[238:239], v[44:45], 0 op_sel_hi:[0,1,0] neg_lo:[1,0,0] neg_hi:[1,0,0]
	v_cvt_pk_bf16_f32 v42, v42, v43
	v_cvt_pk_bf16_f32 v43, v44, v45
	ds_write_b64 v186, v[42:43] offset:1632
	s_waitcnt vmcnt(19)
	v_pk_fma_f32 v[38:39], v[240:241], v[38:39], 0 op_sel_hi:[0,1,0] neg_lo:[1,0,0] neg_hi:[1,0,0]
	v_pk_fma_f32 v[40:41], v[240:241], v[40:41], 0 op_sel_hi:[0,1,0] neg_lo:[1,0,0] neg_hi:[1,0,0]
	v_cvt_pk_bf16_f32 v38, v38, v39
	v_cvt_pk_bf16_f32 v39, v40, v41
	ds_write_b64 v186, v[38:39] offset:2176
	s_waitcnt vmcnt(18)
	v_pk_fma_f32 v[18:19], v[242:243], v[18:19], 0 op_sel_hi:[0,1,0] neg_lo:[1,0,0] neg_hi:[1,0,0]
	v_pk_fma_f32 v[20:21], v[242:243], v[20:21], 0 op_sel_hi:[0,1,0] neg_lo:[1,0,0] neg_hi:[1,0,0]
	v_cvt_pk_bf16_f32 v18, v18, v19
	v_cvt_pk_bf16_f32 v19, v20, v21
	ds_write_b64 v186, v[18:19] offset:2720
	s_waitcnt vmcnt(17)
	v_pk_fma_f32 v[10:11], v[244:245], v[10:11], 0 op_sel_hi:[0,1,0] neg_lo:[1,0,0] neg_hi:[1,0,0]
	v_pk_fma_f32 v[12:13], v[244:245], v[12:13], 0 op_sel_hi:[0,1,0] neg_lo:[1,0,0] neg_hi:[1,0,0]
	v_cvt_pk_bf16_f32 v10, v10, v11
	v_cvt_pk_bf16_f32 v11, v12, v13
	ds_write_b64 v186, v[10:11] offset:3264
	s_waitcnt vmcnt(16)
	v_pk_fma_f32 v[2:3], v[246:247], v[2:3], 0 op_sel_hi:[0,1,0] neg_lo:[1,0,0] neg_hi:[1,0,0]
	v_pk_fma_f32 v[4:5], v[246:247], v[4:5], 0 op_sel_hi:[0,1,0] neg_lo:[1,0,0] neg_hi:[1,0,0]
	v_cvt_pk_bf16_f32 v2, v2, v3
	v_cvt_pk_bf16_f32 v3, v4, v5
	ds_write_b64 v186, v[2:3] offset:3808
	ds_read_b128 v[232:235], v1
	ds_read_b128 v[236:239], v1 offset:64
	ds_read_b128 v[240:243], v1 offset:128
	ds_read_b128 v[244:247], v1 offset:192
	s_waitcnt lgkmcnt(0)
	ds_write_b128 v184, v[232:235] offset:28672
	ds_write_b128 v184, v[236:239] offset:29696
	ds_write_b128 v184, v[240:243] offset:30720
	ds_write_b128 v184, v[244:247] offset:31744
	ds_read_b32 v232, v187 offset:0
	ds_read_b32 v234, v187 offset:8
	ds_read_b32 v236, v187 offset:16
	ds_read_b32 v238, v187 offset:24
	ds_read_b32 v240, v187 offset:32
	ds_read_b32 v242, v187 offset:40
	ds_read_b32 v244, v187 offset:48
	ds_read_b32 v246, v187 offset:56
	s_mov_b64 s[44:45], 0x20000
	v_lshl_add_u64 v[168:169], v[130:131], 0, s[44:45]
	s_mov_b64 s[44:45], 0x22000
	v_lshl_add_u64 v[170:171], v[130:131], 0, s[44:45]
	s_mov_b64 s[44:45], 0x24000
	v_lshl_add_u64 v[172:173], v[130:131], 0, s[44:45]
	s_mov_b64 s[44:45], 0x26000
	v_lshl_add_u64 v[174:175], v[130:131], 0, s[44:45]
	s_mov_b64 s[44:45], 0x28000
	v_lshl_add_u64 v[176:177], v[130:131], 0, s[44:45]
	s_mov_b64 s[44:45], 0x2a000
	v_lshl_add_u64 v[178:179], v[130:131], 0, s[44:45]
	s_mov_b64 s[44:45], 0x2c000
	v_lshl_add_u64 v[180:181], v[130:131], 0, s[44:45]
	s_mov_b64 s[44:45], 0x2e000
	v_lshl_add_u64 v[2:3], v[168:169], 0, s[30:31]
	v_lshl_add_u64 v[4:5], v[170:171], 0, s[30:31]
	v_lshl_add_u64 v[10:11], v[172:173], 0, s[30:31]
	v_lshl_add_u64 v[12:13], v[174:175], 0, s[30:31]
	v_lshl_add_u64 v[18:19], v[176:177], 0, s[30:31]
	v_lshl_add_u64 v[20:21], v[178:179], 0, s[30:31]
	v_lshl_add_u64 v[182:183], v[130:131], 0, s[44:45]
	v_lshl_add_u64 v[42:43], v[180:181], 0, s[30:31]
	v_lshl_add_u64 v[44:45], v[182:183], 0, s[30:31]
	global_load_dwordx4 v[106:109], v[2:3], off nt
	global_load_dwordx4 v[98:101], v[4:5], off nt
	global_load_dwordx4 v[78:81], v[10:11], off nt
	global_load_dwordx4 v[66:69], v[12:13], off nt
	global_load_dwordx4 v[38:41], v[18:19], off nt
	s_nop 0
	global_load_dwordx4 v[18:21], v[20:21], off nt
	s_nop 0
	global_load_dwordx4 v[10:13], v[42:43], off nt
	global_load_dwordx4 v[2:5], v[44:45], off nt
	v_mov_b32_e32 v42, v198
	s_waitcnt lgkmcnt(0)
	s_waitcnt vmcnt(23)
	v_pk_fma_f32 v[44:45], v[232:233], v[74:75], 0 op_sel_hi:[0,1,0] neg_lo:[1,0,0] neg_hi:[1,0,0]
	v_pk_fma_f32 v[42:43], v[232:233], v[76:77], 0 op_sel_hi:[0,1,0] neg_lo:[1,0,0] neg_hi:[1,0,0]
	v_cvt_pk_bf16_f32 v44, v44, v45
	v_cvt_pk_bf16_f32 v45, v42, v43
	ds_write_b64 v186, v[44:45]
	s_waitcnt vmcnt(22)
	v_pk_fma_f32 v[44:45], v[234:235], v[62:63], 0 op_sel_hi:[0,1,0] neg_lo:[1,0,0] neg_hi:[1,0,0]
	v_pk_fma_f32 v[42:43], v[234:235], v[64:65], 0 op_sel_hi:[0,1,0] neg_lo:[1,0,0] neg_hi:[1,0,0]
	v_cvt_pk_bf16_f32 v44, v44, v45
	v_cvt_pk_bf16_f32 v45, v42, v43
	ds_write_b64 v186, v[44:45] offset:544
	s_waitcnt vmcnt(21)
	v_pk_fma_f32 v[44:45], v[236:237], v[58:59], 0 op_sel_hi:[0,1,0] neg_lo:[1,0,0] neg_hi:[1,0,0]
	v_pk_fma_f32 v[42:43], v[236:237], v[60:61], 0 op_sel_hi:[0,1,0] neg_lo:[1,0,0] neg_hi:[1,0,0]
	v_cvt_pk_bf16_f32 v44, v44, v45
	v_cvt_pk_bf16_f32 v45, v42, v43
	ds_write_b64 v186, v[44:45] offset:1088
	s_waitcnt vmcnt(20)
	v_pk_fma_f32 v[44:45], v[238:239], v[46:47], 0 op_sel_hi:[0,1,0] neg_lo:[1,0,0] neg_hi:[1,0,0]
	v_pk_fma_f32 v[42:43], v[238:239], v[48:49], 0 op_sel_hi:[0,1,0] neg_lo:[1,0,0] neg_hi:[1,0,0]
	v_cvt_pk_bf16_f32 v44, v44, v45
	v_cvt_pk_bf16_f32 v45, v42, v43
	ds_write_b64 v186, v[44:45] offset:1632
	s_waitcnt vmcnt(19)
	v_pk_fma_f32 v[44:45], v[240:241], v[50:51], 0 op_sel_hi:[0,1,0] neg_lo:[1,0,0] neg_hi:[1,0,0]
	v_pk_fma_f32 v[42:43], v[240:241], v[52:53], 0 op_sel_hi:[0,1,0] neg_lo:[1,0,0] neg_hi:[1,0,0]
	v_cvt_pk_bf16_f32 v44, v44, v45
	v_cvt_pk_bf16_f32 v45, v42, v43
	ds_write_b64 v186, v[44:45] offset:2176
	s_waitcnt vmcnt(18)
	v_pk_fma_f32 v[30:31], v[242:243], v[30:31], 0 op_sel_hi:[0,1,0] neg_lo:[1,0,0] neg_hi:[1,0,0]
	v_pk_fma_f32 v[32:33], v[242:243], v[32:33], 0 op_sel_hi:[0,1,0] neg_lo:[1,0,0] neg_hi:[1,0,0]
	v_cvt_pk_bf16_f32 v30, v30, v31
	v_cvt_pk_bf16_f32 v31, v32, v33
	ds_write_b64 v186, v[30:31] offset:2720
	s_waitcnt vmcnt(17)
	v_pk_fma_f32 v[32:33], v[244:245], v[34:35], 0 op_sel_hi:[0,1,0] neg_lo:[1,0,0] neg_hi:[1,0,0]
	v_pk_fma_f32 v[30:31], v[244:245], v[36:37], 0 op_sel_hi:[0,1,0] neg_lo:[1,0,0] neg_hi:[1,0,0]
	v_cvt_pk_bf16_f32 v32, v32, v33
	v_cvt_pk_bf16_f32 v33, v30, v31
	ds_write_b64 v186, v[32:33] offset:3264
	s_waitcnt vmcnt(16)
	v_pk_fma_f32 v[22:23], v[246:247], v[22:23], 0 op_sel_hi:[0,1,0] neg_lo:[1,0,0] neg_hi:[1,0,0]
	v_pk_fma_f32 v[24:25], v[246:247], v[24:25], 0 op_sel_hi:[0,1,0] neg_lo:[1,0,0] neg_hi:[1,0,0]
	v_cvt_pk_bf16_f32 v22, v22, v23
	v_cvt_pk_bf16_f32 v23, v24, v25
	ds_write_b64 v186, v[22:23] offset:3808
	ds_read_b32 v232, v187 offset:64
	ds_read_b32 v234, v187 offset:72
	ds_read_b32 v236, v187 offset:80
	ds_read_b32 v238, v187 offset:88
	ds_read_b32 v240, v187 offset:96
	ds_read_b32 v242, v187 offset:104
	ds_read_b32 v244, v187 offset:112
	ds_read_b32 v246, v187 offset:120
	ds_read_b128 a[0:3], v1
	ds_read_b128 a[4:7], v1 offset:64
	ds_read_b128 a[8:11], v1 offset:128
	ds_read_b128 a[12:15], v1 offset:192
	v_lshl_add_u64 v[22:23], v[130:131], 0, s[28:29]
	v_add_co_u32_e32 v24, vcc, s7, v22
	s_nop 1
	v_addc_co_u32_e32 v25, vcc, 0, v23, vcc
	global_load_dwordx4 v[102:105], v[22:23], off nt
	global_load_dwordx4 v[86:89], v[24:25], off nt
	v_add_co_u32_e32 v24, vcc, s36, v22
	s_nop 1
	v_addc_co_u32_e32 v25, vcc, 0, v23, vcc
	v_add_co_u32_e32 v30, vcc, s37, v22
	s_nop 1
	v_addc_co_u32_e32 v31, vcc, 0, v23, vcc
	global_load_dwordx4 v[74:77], v[24:25], off nt
	global_load_dwordx4 v[62:65], v[30:31], off nt
	v_add_co_u32_e32 v24, vcc, s38, v22
	s_nop 1
	v_addc_co_u32_e32 v25, vcc, 0, v23, vcc
	v_add_co_u32_e32 v30, vcc, s39, v22
	s_nop 1
	v_addc_co_u32_e32 v31, vcc, 0, v23, vcc
	global_load_dwordx4 v[58:61], v[24:25], off nt
	global_load_dwordx4 v[46:49], v[30:31], off nt
	v_add_co_u32_e32 v24, vcc, s41, v22
	s_nop 1
	v_addc_co_u32_e32 v25, vcc, 0, v23, vcc
	v_add_co_u32_e32 v22, vcc, s42, v22
	s_nop 1
	v_addc_co_u32_e32 v23, vcc, 0, v23, vcc
	global_load_dwordx4 v[42:45], v[24:25], off nt
	global_load_dwordx4 v[30:33], v[22:23], off nt
	v_mov_b32_e32 v22, v198
	s_waitcnt lgkmcnt(0)
	s_waitcnt vmcnt(23)
	v_pk_fma_f32 v[24:25], v[232:233], v[94:95], 0 op_sel_hi:[0,1,0] neg_lo:[1,0,0] neg_hi:[1,0,0]
	v_pk_fma_f32 v[22:23], v[232:233], v[96:97], 0 op_sel_hi:[0,1,0] neg_lo:[1,0,0] neg_hi:[1,0,0]
	v_cvt_pk_bf16_f32 v24, v24, v25
	v_cvt_pk_bf16_f32 v25, v22, v23
	ds_write_b64 v186, v[24:25]
	s_waitcnt vmcnt(22)
	v_pk_fma_f32 v[24:25], v[234:235], v[90:91], 0 op_sel_hi:[0,1,0] neg_lo:[1,0,0] neg_hi:[1,0,0]
	v_pk_fma_f32 v[22:23], v[234:235], v[92:93], 0 op_sel_hi:[0,1,0] neg_lo:[1,0,0] neg_hi:[1,0,0]
	v_cvt_pk_bf16_f32 v24, v24, v25
	v_cvt_pk_bf16_f32 v25, v22, v23
	ds_write_b64 v186, v[24:25] offset:544
	s_waitcnt vmcnt(21)
	v_pk_fma_f32 v[24:25], v[236:237], v[82:83], 0 op_sel_hi:[0,1,0] neg_lo:[1,0,0] neg_hi:[1,0,0]
	v_pk_fma_f32 v[22:23], v[236:237], v[84:85], 0 op_sel_hi:[0,1,0] neg_lo:[1,0,0] neg_hi:[1,0,0]
	v_cvt_pk_bf16_f32 v24, v24, v25
	v_cvt_pk_bf16_f32 v25, v22, v23
	ds_write_b64 v186, v[24:25] offset:1088
	s_waitcnt vmcnt(20)
	v_pk_fma_f32 v[24:25], v[238:239], v[70:71], 0 op_sel_hi:[0,1,0] neg_lo:[1,0,0] neg_hi:[1,0,0]
	v_pk_fma_f32 v[22:23], v[238:239], v[72:73], 0 op_sel_hi:[0,1,0] neg_lo:[1,0,0] neg_hi:[1,0,0]
	v_cvt_pk_bf16_f32 v24, v24, v25
	v_cvt_pk_bf16_f32 v25, v22, v23
	ds_write_b64 v186, v[24:25] offset:1632
	s_waitcnt vmcnt(19)
	v_pk_fma_f32 v[24:25], v[240:241], v[54:55], 0 op_sel_hi:[0,1,0] neg_lo:[1,0,0] neg_hi:[1,0,0]
	v_pk_fma_f32 v[22:23], v[240:241], v[56:57], 0 op_sel_hi:[0,1,0] neg_lo:[1,0,0] neg_hi:[1,0,0]
	v_cvt_pk_bf16_f32 v24, v24, v25
	v_cvt_pk_bf16_f32 v25, v22, v23
	ds_write_b64 v186, v[24:25] offset:2176
	s_waitcnt vmcnt(18)
	v_pk_fma_f32 v[24:25], v[242:243], v[26:27], 0 op_sel_hi:[0,1,0] neg_lo:[1,0,0] neg_hi:[1,0,0]
	v_pk_fma_f32 v[22:23], v[242:243], v[28:29], 0 op_sel_hi:[0,1,0] neg_lo:[1,0,0] neg_hi:[1,0,0]
	v_cvt_pk_bf16_f32 v24, v24, v25
	v_cvt_pk_bf16_f32 v25, v22, v23
	ds_write_b64 v186, v[24:25] offset:2720
	s_waitcnt vmcnt(17)
	v_pk_fma_f32 v[14:15], v[244:245], v[14:15], 0 op_sel_hi:[0,1,0] neg_lo:[1,0,0] neg_hi:[1,0,0]
	v_pk_fma_f32 v[16:17], v[244:245], v[16:17], 0 op_sel_hi:[0,1,0] neg_lo:[1,0,0] neg_hi:[1,0,0]
	v_cvt_pk_bf16_f32 v14, v14, v15
	v_cvt_pk_bf16_f32 v15, v16, v17
	ds_write_b64 v186, v[14:15] offset:3264
	s_waitcnt vmcnt(16)
	v_pk_fma_f32 v[6:7], v[246:247], v[6:7], 0 op_sel_hi:[0,1,0] neg_lo:[1,0,0] neg_hi:[1,0,0]
	v_pk_fma_f32 v[8:9], v[246:247], v[8:9], 0 op_sel_hi:[0,1,0] neg_lo:[1,0,0] neg_hi:[1,0,0]
	v_cvt_pk_bf16_f32 v6, v6, v7
	v_cvt_pk_bf16_f32 v7, v8, v9
	ds_write_b64 v186, v[6:7] offset:3808
	ds_read_b32 v232, v187 offset:128
	ds_read_b32 v234, v187 offset:136
	ds_read_b32 v236, v187 offset:144
	ds_read_b32 v238, v187 offset:152
	ds_read_b32 v240, v187 offset:160
	ds_read_b32 v242, v187 offset:168
	ds_read_b32 v244, v187 offset:176
	ds_read_b32 v246, v187 offset:184
	ds_read_b128 a[16:19], v1
	ds_read_b128 a[20:23], v1 offset:64
	ds_read_b128 a[24:27], v1 offset:128
	ds_read_b128 a[28:31], v1 offset:192
	v_lshl_add_u64 v[6:7], v[150:151], 0, s[28:29]
	v_lshl_add_u64 v[8:9], v[152:153], 0, s[28:29]
	v_lshl_add_u64 v[14:15], v[156:157], 0, s[28:29]
	v_lshl_add_u64 v[16:17], v[158:159], 0, s[28:29]
	v_lshl_add_u64 v[22:23], v[160:161], 0, s[28:29]
	v_lshl_add_u64 v[24:25], v[162:163], 0, s[28:29]
	v_lshl_add_u64 v[26:27], v[164:165], 0, s[28:29]
	v_lshl_add_u64 v[28:29], v[166:167], 0, s[28:29]
	global_load_dwordx4 v[110:113], v[6:7], off nt
	global_load_dwordx4 v[90:93], v[8:9], off nt
	global_load_dwordx4 v[70:73], v[14:15], off nt
	global_load_dwordx4 v[50:53], v[16:17], off nt
	global_load_dwordx4 v[34:37], v[22:23], off nt
	s_nop 0
	global_load_dwordx4 v[22:25], v[24:25], off nt
	s_nop 0
	global_load_dwordx4 v[14:17], v[26:27], off nt
	global_load_dwordx4 v[6:9], v[28:29], off nt
	s_waitcnt lgkmcnt(0)
	s_waitcnt vmcnt(23)
	v_pk_fma_f32 v[28:29], v[232:233], v[106:107], 0 op_sel_hi:[0,1,0] neg_lo:[1,0,0] neg_hi:[1,0,0]
	v_pk_fma_f32 v[26:27], v[232:233], v[108:109], 0 op_sel_hi:[0,1,0] neg_lo:[1,0,0] neg_hi:[1,0,0]
	v_cvt_pk_bf16_f32 v28, v28, v29
	v_cvt_pk_bf16_f32 v29, v26, v27
	ds_write_b64 v186, v[28:29]
	s_waitcnt vmcnt(22)
	v_pk_fma_f32 v[28:29], v[234:235], v[98:99], 0 op_sel_hi:[0,1,0] neg_lo:[1,0,0] neg_hi:[1,0,0]
	v_pk_fma_f32 v[26:27], v[234:235], v[100:101], 0 op_sel_hi:[0,1,0] neg_lo:[1,0,0] neg_hi:[1,0,0]
	v_cvt_pk_bf16_f32 v28, v28, v29
	v_cvt_pk_bf16_f32 v29, v26, v27
	ds_write_b64 v186, v[28:29] offset:544
	s_waitcnt vmcnt(21)
	v_pk_fma_f32 v[28:29], v[236:237], v[78:79], 0 op_sel_hi:[0,1,0] neg_lo:[1,0,0] neg_hi:[1,0,0]
	v_pk_fma_f32 v[26:27], v[236:237], v[80:81], 0 op_sel_hi:[0,1,0] neg_lo:[1,0,0] neg_hi:[1,0,0]
	v_cvt_pk_bf16_f32 v28, v28, v29
	v_cvt_pk_bf16_f32 v29, v26, v27
	ds_write_b64 v186, v[28:29] offset:1088
	s_waitcnt vmcnt(20)
	v_pk_fma_f32 v[28:29], v[238:239], v[66:67], 0 op_sel_hi:[0,1,0] neg_lo:[1,0,0] neg_hi:[1,0,0]
	v_pk_fma_f32 v[26:27], v[238:239], v[68:69], 0 op_sel_hi:[0,1,0] neg_lo:[1,0,0] neg_hi:[1,0,0]
	v_cvt_pk_bf16_f32 v28, v28, v29
	v_cvt_pk_bf16_f32 v29, v26, v27
	ds_write_b64 v186, v[28:29] offset:1632
	s_waitcnt vmcnt(19)
	v_pk_fma_f32 v[28:29], v[240:241], v[38:39], 0 op_sel_hi:[0,1,0] neg_lo:[1,0,0] neg_hi:[1,0,0]
	v_pk_fma_f32 v[26:27], v[240:241], v[40:41], 0 op_sel_hi:[0,1,0] neg_lo:[1,0,0] neg_hi:[1,0,0]
	v_cvt_pk_bf16_f32 v28, v28, v29
	v_cvt_pk_bf16_f32 v29, v26, v27
	ds_write_b64 v186, v[28:29] offset:2176
	s_waitcnt vmcnt(18)
	v_pk_fma_f32 v[18:19], v[242:243], v[18:19], 0 op_sel_hi:[0,1,0] neg_lo:[1,0,0] neg_hi:[1,0,0]
	v_pk_fma_f32 v[20:21], v[242:243], v[20:21], 0 op_sel_hi:[0,1,0] neg_lo:[1,0,0] neg_hi:[1,0,0]
	v_cvt_pk_bf16_f32 v18, v18, v19
	v_cvt_pk_bf16_f32 v19, v20, v21
	ds_write_b64 v186, v[18:19] offset:2720
	s_waitcnt vmcnt(17)
	v_pk_fma_f32 v[10:11], v[244:245], v[10:11], 0 op_sel_hi:[0,1,0] neg_lo:[1,0,0] neg_hi:[1,0,0]
	v_pk_fma_f32 v[12:13], v[244:245], v[12:13], 0 op_sel_hi:[0,1,0] neg_lo:[1,0,0] neg_hi:[1,0,0]
	v_cvt_pk_bf16_f32 v10, v10, v11
	v_cvt_pk_bf16_f32 v11, v12, v13
	ds_write_b64 v186, v[10:11] offset:3264
	s_waitcnt vmcnt(16)
	v_pk_fma_f32 v[2:3], v[246:247], v[2:3], 0 op_sel_hi:[0,1,0] neg_lo:[1,0,0] neg_hi:[1,0,0]
	v_pk_fma_f32 v[4:5], v[246:247], v[4:5], 0 op_sel_hi:[0,1,0] neg_lo:[1,0,0] neg_hi:[1,0,0]
	v_cvt_pk_bf16_f32 v2, v2, v3
	v_cvt_pk_bf16_f32 v3, v4, v5
	ds_write_b64 v186, v[2:3] offset:3808
	ds_read_b32 v232, v187 offset:0
	ds_read_b32 v234, v187 offset:8
	ds_read_b32 v236, v187 offset:16
	ds_read_b32 v238, v187 offset:24
	ds_read_b32 v240, v187 offset:32
	ds_read_b32 v242, v187 offset:40
	ds_read_b32 v244, v187 offset:48
	ds_read_b32 v246, v187 offset:56
	ds_read_b128 a[32:35], v1
	ds_read_b128 a[36:39], v1 offset:64
	ds_read_b128 a[40:43], v1 offset:128
	ds_read_b128 a[44:47], v1 offset:192
	v_lshl_add_u64 v[2:3], v[168:169], 0, s[28:29]
	v_lshl_add_u64 v[4:5], v[170:171], 0, s[28:29]
	v_lshl_add_u64 v[10:11], v[172:173], 0, s[28:29]
	v_lshl_add_u64 v[12:13], v[174:175], 0, s[28:29]
	v_lshl_add_u64 v[18:19], v[176:177], 0, s[28:29]
	v_lshl_add_u64 v[20:21], v[178:179], 0, s[28:29]
	v_lshl_add_u64 v[26:27], v[180:181], 0, s[28:29]
	v_lshl_add_u64 v[28:29], v[182:183], 0, s[28:29]
	global_load_dwordx4 v[106:109], v[2:3], off nt
	global_load_dwordx4 v[94:97], v[4:5], off nt
	global_load_dwordx4 v[66:69], v[10:11], off nt
	global_load_dwordx4 v[54:57], v[12:13], off nt
	global_load_dwordx4 v[38:41], v[18:19], off nt
	s_nop 0
	global_load_dwordx4 v[18:21], v[20:21], off nt
	s_nop 0
	global_load_dwordx4 v[10:13], v[26:27], off nt
	global_load_dwordx4 v[2:5], v[28:29], off nt
	v_mov_b32_e32 v26, v197
	s_waitcnt lgkmcnt(0)
	s_waitcnt vmcnt(23)
	v_pk_fma_f32 v[28:29], v[232:233], v[102:103], 0 op_sel_hi:[0,1,0] neg_lo:[1,0,0] neg_hi:[1,0,0]
	v_pk_fma_f32 v[26:27], v[232:233], v[104:105], 0 op_sel_hi:[0,1,0] neg_lo:[1,0,0] neg_hi:[1,0,0]
	v_cvt_pk_bf16_f32 v28, v28, v29
	v_cvt_pk_bf16_f32 v29, v26, v27
	ds_write_b64 v186, v[28:29]
	s_waitcnt vmcnt(22)
	v_pk_fma_f32 v[28:29], v[234:235], v[86:87], 0 op_sel_hi:[0,1,0] neg_lo:[1,0,0] neg_hi:[1,0,0]
	v_pk_fma_f32 v[26:27], v[234:235], v[88:89], 0 op_sel_hi:[0,1,0] neg_lo:[1,0,0] neg_hi:[1,0,0]
	v_cvt_pk_bf16_f32 v28, v28, v29
	v_cvt_pk_bf16_f32 v29, v26, v27
	ds_write_b64 v186, v[28:29] offset:544
	s_waitcnt vmcnt(21)
	v_pk_fma_f32 v[28:29], v[236:237], v[74:75], 0 op_sel_hi:[0,1,0] neg_lo:[1,0,0] neg_hi:[1,0,0]
	v_pk_fma_f32 v[26:27], v[236:237], v[76:77], 0 op_sel_hi:[0,1,0] neg_lo:[1,0,0] neg_hi:[1,0,0]
	v_cvt_pk_bf16_f32 v28, v28, v29
	v_cvt_pk_bf16_f32 v29, v26, v27
	ds_write_b64 v186, v[28:29] offset:1088
	s_waitcnt vmcnt(20)
	v_pk_fma_f32 v[28:29], v[238:239], v[62:63], 0 op_sel_hi:[0,1,0] neg_lo:[1,0,0] neg_hi:[1,0,0]
	v_pk_fma_f32 v[26:27], v[238:239], v[64:65], 0 op_sel_hi:[0,1,0] neg_lo:[1,0,0] neg_hi:[1,0,0]
	v_cvt_pk_bf16_f32 v28, v28, v29
	v_cvt_pk_bf16_f32 v29, v26, v27
	ds_write_b64 v186, v[28:29] offset:1632
	s_waitcnt vmcnt(19)
	v_pk_fma_f32 v[28:29], v[240:241], v[58:59], 0 op_sel_hi:[0,1,0] neg_lo:[1,0,0] neg_hi:[1,0,0]
	v_pk_fma_f32 v[26:27], v[240:241], v[60:61], 0 op_sel_hi:[0,1,0] neg_lo:[1,0,0] neg_hi:[1,0,0]
	v_cvt_pk_bf16_f32 v28, v28, v29
	v_cvt_pk_bf16_f32 v29, v26, v27
	ds_write_b64 v186, v[28:29] offset:2176
	s_waitcnt vmcnt(18)
	v_pk_fma_f32 v[28:29], v[242:243], v[46:47], 0 op_sel_hi:[0,1,0] neg_lo:[1,0,0] neg_hi:[1,0,0]
	v_pk_fma_f32 v[26:27], v[242:243], v[48:49], 0 op_sel_hi:[0,1,0] neg_lo:[1,0,0] neg_hi:[1,0,0]
	v_cvt_pk_bf16_f32 v28, v28, v29
	v_cvt_pk_bf16_f32 v29, v26, v27
	ds_write_b64 v186, v[28:29] offset:2720
	s_waitcnt vmcnt(17)
	v_pk_fma_f32 v[28:29], v[244:245], v[42:43], 0 op_sel_hi:[0,1,0] neg_lo:[1,0,0] neg_hi:[1,0,0]
	v_pk_fma_f32 v[26:27], v[244:245], v[44:45], 0 op_sel_hi:[0,1,0] neg_lo:[1,0,0] neg_hi:[1,0,0]
	v_cvt_pk_bf16_f32 v28, v28, v29
	v_cvt_pk_bf16_f32 v29, v26, v27
	ds_write_b64 v186, v[28:29] offset:3264
	s_waitcnt vmcnt(16)
	v_pk_fma_f32 v[28:29], v[246:247], v[30:31], 0 op_sel_hi:[0,1,0] neg_lo:[1,0,0] neg_hi:[1,0,0]
	v_pk_fma_f32 v[26:27], v[246:247], v[32:33], 0 op_sel_hi:[0,1,0] neg_lo:[1,0,0] neg_hi:[1,0,0]
	v_cvt_pk_bf16_f32 v28, v28, v29
	v_cvt_pk_bf16_f32 v29, v26, v27
	ds_write_b64 v186, v[28:29] offset:3808
	ds_read_b32 v232, v187 offset:64
	ds_read_b32 v234, v187 offset:72
	ds_read_b32 v236, v187 offset:80
	ds_read_b32 v238, v187 offset:88
	ds_read_b32 v240, v187 offset:96
	ds_read_b32 v242, v187 offset:104
	ds_read_b32 v244, v187 offset:112
	ds_read_b32 v246, v187 offset:120
	ds_read_b128 a[48:51], v1
	ds_read_b128 a[52:55], v1 offset:64
	ds_read_b128 a[56:59], v1 offset:128
	ds_read_b128 a[60:63], v1 offset:192
	v_lshl_add_u64 v[26:27], v[130:131], 0, s[26:27]
	v_add_co_u32_e32 v28, vcc, s7, v26
	s_nop 1
	v_addc_co_u32_e32 v29, vcc, 0, v27, vcc
	global_load_dwordx4 v[86:89], v[26:27], off nt
	global_load_dwordx4 v[82:85], v[28:29], off nt
	v_add_co_u32_e32 v28, vcc, s36, v26
	s_nop 1
	v_addc_co_u32_e32 v29, vcc, 0, v27, vcc
	v_add_co_u32_e32 v30, vcc, s37, v26
	s_nop 1
	v_addc_co_u32_e32 v31, vcc, 0, v27, vcc
	global_load_dwordx4 v[78:81], v[28:29], off nt
	global_load_dwordx4 v[58:61], v[30:31], off nt
	v_add_co_u32_e32 v28, vcc, s38, v26
	s_nop 1
	v_addc_co_u32_e32 v29, vcc, 0, v27, vcc
	v_add_co_u32_e32 v30, vcc, s39, v26
	s_nop 1
	v_addc_co_u32_e32 v31, vcc, 0, v27, vcc
	global_load_dwordx4 v[46:49], v[28:29], off nt
	global_load_dwordx4 v[42:45], v[30:31], off nt
	v_add_co_u32_e32 v28, vcc, s41, v26
	s_nop 1
	v_addc_co_u32_e32 v29, vcc, 0, v27, vcc
	v_add_co_u32_e32 v26, vcc, s42, v26
	s_nop 1
	v_addc_co_u32_e32 v27, vcc, 0, v27, vcc
	global_load_dwordx4 v[30:33], v[28:29], off nt
	s_nop 0
	global_load_dwordx4 v[26:29], v[26:27], off nt
	v_mov_b32_e32 v62, v197
	s_waitcnt lgkmcnt(0)
	s_waitcnt vmcnt(23)
	v_pk_fma_f32 v[64:65], v[232:233], v[110:111], 0 op_sel_hi:[0,1,0] neg_lo:[1,0,0] neg_hi:[1,0,0]
	v_pk_fma_f32 v[62:63], v[232:233], v[112:113], 0 op_sel_hi:[0,1,0] neg_lo:[1,0,0] neg_hi:[1,0,0]
	v_cvt_pk_bf16_f32 v64, v64, v65
	v_cvt_pk_bf16_f32 v65, v62, v63
	ds_write_b64 v186, v[64:65]
	s_waitcnt vmcnt(22)
	v_pk_fma_f32 v[64:65], v[234:235], v[90:91], 0 op_sel_hi:[0,1,0] neg_lo:[1,0,0] neg_hi:[1,0,0]
	v_pk_fma_f32 v[62:63], v[234:235], v[92:93], 0 op_sel_hi:[0,1,0] neg_lo:[1,0,0] neg_hi:[1,0,0]
	v_cvt_pk_bf16_f32 v64, v64, v65
	v_cvt_pk_bf16_f32 v65, v62, v63
	ds_write_b64 v186, v[64:65] offset:544
	s_waitcnt vmcnt(21)
	v_pk_fma_f32 v[64:65], v[236:237], v[70:71], 0 op_sel_hi:[0,1,0] neg_lo:[1,0,0] neg_hi:[1,0,0]
	v_pk_fma_f32 v[62:63], v[236:237], v[72:73], 0 op_sel_hi:[0,1,0] neg_lo:[1,0,0] neg_hi:[1,0,0]
	v_cvt_pk_bf16_f32 v64, v64, v65
	v_cvt_pk_bf16_f32 v65, v62, v63
	ds_write_b64 v186, v[64:65] offset:1088
	s_waitcnt vmcnt(20)
	v_pk_fma_f32 v[50:51], v[238:239], v[50:51], 0 op_sel_hi:[0,1,0] neg_lo:[1,0,0] neg_hi:[1,0,0]
	v_pk_fma_f32 v[52:53], v[238:239], v[52:53], 0 op_sel_hi:[0,1,0] neg_lo:[1,0,0] neg_hi:[1,0,0]
	v_cvt_pk_bf16_f32 v50, v50, v51
	v_cvt_pk_bf16_f32 v51, v52, v53
	ds_write_b64 v186, v[50:51] offset:1632
	s_waitcnt vmcnt(19)
	v_pk_fma_f32 v[34:35], v[240:241], v[34:35], 0 op_sel_hi:[0,1,0] neg_lo:[1,0,0] neg_hi:[1,0,0]
	v_pk_fma_f32 v[36:37], v[240:241], v[36:37], 0 op_sel_hi:[0,1,0] neg_lo:[1,0,0] neg_hi:[1,0,0]
	v_cvt_pk_bf16_f32 v34, v34, v35
	v_cvt_pk_bf16_f32 v35, v36, v37
	ds_write_b64 v186, v[34:35] offset:2176
	s_waitcnt vmcnt(18)
	v_pk_fma_f32 v[22:23], v[242:243], v[22:23], 0 op_sel_hi:[0,1,0] neg_lo:[1,0,0] neg_hi:[1,0,0]
	v_pk_fma_f32 v[24:25], v[242:243], v[24:25], 0 op_sel_hi:[0,1,0] neg_lo:[1,0,0] neg_hi:[1,0,0]
	v_cvt_pk_bf16_f32 v22, v22, v23
	v_cvt_pk_bf16_f32 v23, v24, v25
	ds_write_b64 v186, v[22:23] offset:2720
	s_waitcnt vmcnt(17)
	v_pk_fma_f32 v[14:15], v[244:245], v[14:15], 0 op_sel_hi:[0,1,0] neg_lo:[1,0,0] neg_hi:[1,0,0]
	v_pk_fma_f32 v[16:17], v[244:245], v[16:17], 0 op_sel_hi:[0,1,0] neg_lo:[1,0,0] neg_hi:[1,0,0]
	v_cvt_pk_bf16_f32 v14, v14, v15
	v_cvt_pk_bf16_f32 v15, v16, v17
	ds_write_b64 v186, v[14:15] offset:3264
	s_waitcnt vmcnt(16)
	v_pk_fma_f32 v[6:7], v[246:247], v[6:7], 0 op_sel_hi:[0,1,0] neg_lo:[1,0,0] neg_hi:[1,0,0]
	v_pk_fma_f32 v[8:9], v[246:247], v[8:9], 0 op_sel_hi:[0,1,0] neg_lo:[1,0,0] neg_hi:[1,0,0]
	v_cvt_pk_bf16_f32 v6, v6, v7
	v_cvt_pk_bf16_f32 v7, v8, v9
	ds_write_b64 v186, v[6:7] offset:3808
	ds_read_b32 v232, v187 offset:128
	ds_read_b32 v234, v187 offset:136
	ds_read_b32 v236, v187 offset:144
	ds_read_b32 v238, v187 offset:152
	ds_read_b32 v240, v187 offset:160
	ds_read_b32 v242, v187 offset:168
	ds_read_b32 v244, v187 offset:176
	ds_read_b32 v246, v187 offset:184
	ds_read_b128 a[64:67], v1
	ds_read_b128 a[68:71], v1 offset:64
	ds_read_b128 a[72:75], v1 offset:128
	ds_read_b128 a[76:79], v1 offset:192
	v_lshl_add_u64 v[6:7], v[150:151], 0, s[26:27]
	v_lshl_add_u64 v[8:9], v[152:153], 0, s[26:27]
	v_lshl_add_u64 v[14:15], v[156:157], 0, s[26:27]
	v_lshl_add_u64 v[16:17], v[158:159], 0, s[26:27]
	v_lshl_add_u64 v[22:23], v[160:161], 0, s[26:27]
	v_lshl_add_u64 v[24:25], v[162:163], 0, s[26:27]
	v_lshl_add_u64 v[70:71], v[164:165], 0, s[26:27]
	v_lshl_add_u64 v[72:73], v[166:167], 0, s[26:27]
	global_load_dwordx4 v[110:113], v[6:7], off nt
	global_load_dwordx4 v[98:101], v[8:9], off nt
	global_load_dwordx4 v[62:65], v[14:15], off nt
	global_load_dwordx4 v[50:53], v[16:17], off nt
	global_load_dwordx4 v[34:37], v[22:23], off nt
	s_nop 0
	global_load_dwordx4 v[22:25], v[24:25], off nt
	s_nop 0
	global_load_dwordx4 v[14:17], v[70:71], off nt
	global_load_dwordx4 v[6:9], v[72:73], off nt
	s_waitcnt lgkmcnt(0)
	s_waitcnt vmcnt(23)
	v_pk_fma_f32 v[72:73], v[232:233], v[106:107], 0 op_sel_hi:[0,1,0] neg_lo:[1,0,0] neg_hi:[1,0,0]
	v_pk_fma_f32 v[70:71], v[232:233], v[108:109], 0 op_sel_hi:[0,1,0] neg_lo:[1,0,0] neg_hi:[1,0,0]
	v_cvt_pk_bf16_f32 v72, v72, v73
	v_cvt_pk_bf16_f32 v73, v70, v71
	ds_write_b64 v186, v[72:73]
	s_waitcnt vmcnt(22)
	v_pk_fma_f32 v[72:73], v[234:235], v[94:95], 0 op_sel_hi:[0,1,0] neg_lo:[1,0,0] neg_hi:[1,0,0]
	v_pk_fma_f32 v[70:71], v[234:235], v[96:97], 0 op_sel_hi:[0,1,0] neg_lo:[1,0,0] neg_hi:[1,0,0]
	v_cvt_pk_bf16_f32 v72, v72, v73
	v_cvt_pk_bf16_f32 v73, v70, v71
	ds_write_b64 v186, v[72:73] offset:544
	s_waitcnt vmcnt(21)
	v_pk_fma_f32 v[66:67], v[236:237], v[66:67], 0 op_sel_hi:[0,1,0] neg_lo:[1,0,0] neg_hi:[1,0,0]
	v_pk_fma_f32 v[68:69], v[236:237], v[68:69], 0 op_sel_hi:[0,1,0] neg_lo:[1,0,0] neg_hi:[1,0,0]
	v_cvt_pk_bf16_f32 v66, v66, v67
	v_cvt_pk_bf16_f32 v67, v68, v69
	ds_write_b64 v186, v[66:67] offset:1088
	s_waitcnt vmcnt(20)
	v_pk_fma_f32 v[54:55], v[238:239], v[54:55], 0 op_sel_hi:[0,1,0] neg_lo:[1,0,0] neg_hi:[1,0,0]
	v_pk_fma_f32 v[56:57], v[238:239], v[56:57], 0 op_sel_hi:[0,1,0] neg_lo:[1,0,0] neg_hi:[1,0,0]
	v_cvt_pk_bf16_f32 v54, v54, v55
	v_cvt_pk_bf16_f32 v55, v56, v57
	ds_write_b64 v186, v[54:55] offset:1632
	s_waitcnt vmcnt(19)
	v_pk_fma_f32 v[38:39], v[240:241], v[38:39], 0 op_sel_hi:[0,1,0] neg_lo:[1,0,0] neg_hi:[1,0,0]
	v_pk_fma_f32 v[40:41], v[240:241], v[40:41], 0 op_sel_hi:[0,1,0] neg_lo:[1,0,0] neg_hi:[1,0,0]
	v_cvt_pk_bf16_f32 v38, v38, v39
	v_cvt_pk_bf16_f32 v39, v40, v41
	ds_write_b64 v186, v[38:39] offset:2176
	s_waitcnt vmcnt(18)
	v_pk_fma_f32 v[18:19], v[242:243], v[18:19], 0 op_sel_hi:[0,1,0] neg_lo:[1,0,0] neg_hi:[1,0,0]
	v_pk_fma_f32 v[20:21], v[242:243], v[20:21], 0 op_sel_hi:[0,1,0] neg_lo:[1,0,0] neg_hi:[1,0,0]
	v_cvt_pk_bf16_f32 v18, v18, v19
	v_cvt_pk_bf16_f32 v19, v20, v21
	ds_write_b64 v186, v[18:19] offset:2720
	s_waitcnt vmcnt(17)
	v_pk_fma_f32 v[10:11], v[244:245], v[10:11], 0 op_sel_hi:[0,1,0] neg_lo:[1,0,0] neg_hi:[1,0,0]
	v_pk_fma_f32 v[12:13], v[244:245], v[12:13], 0 op_sel_hi:[0,1,0] neg_lo:[1,0,0] neg_hi:[1,0,0]
	v_cvt_pk_bf16_f32 v10, v10, v11
	v_cvt_pk_bf16_f32 v11, v12, v13
	ds_write_b64 v186, v[10:11] offset:3264
	s_waitcnt vmcnt(16)
	v_pk_fma_f32 v[2:3], v[246:247], v[2:3], 0 op_sel_hi:[0,1,0] neg_lo:[1,0,0] neg_hi:[1,0,0]
	v_pk_fma_f32 v[4:5], v[246:247], v[4:5], 0 op_sel_hi:[0,1,0] neg_lo:[1,0,0] neg_hi:[1,0,0]
	v_cvt_pk_bf16_f32 v2, v2, v3
	v_cvt_pk_bf16_f32 v3, v4, v5
	ds_write_b64 v186, v[2:3] offset:3808
	ds_read_b32 v232, v187 offset:0
	ds_read_b32 v234, v187 offset:8
	ds_read_b32 v236, v187 offset:16
	ds_read_b32 v238, v187 offset:24
	ds_read_b32 v240, v187 offset:32
	ds_read_b32 v242, v187 offset:40
	ds_read_b32 v244, v187 offset:48
	ds_read_b32 v246, v187 offset:56
	ds_read_b128 a[80:83], v1
	ds_read_b128 a[84:87], v1 offset:64
	ds_read_b128 a[88:91], v1 offset:128
	ds_read_b128 a[92:95], v1 offset:192
	v_lshl_add_u64 v[2:3], v[168:169], 0, s[26:27]
	v_lshl_add_u64 v[4:5], v[170:171], 0, s[26:27]
	v_lshl_add_u64 v[10:11], v[172:173], 0, s[26:27]
	v_lshl_add_u64 v[12:13], v[174:175], 0, s[26:27]
	v_lshl_add_u64 v[18:19], v[176:177], 0, s[26:27]
	v_lshl_add_u64 v[20:21], v[178:179], 0, s[26:27]
	v_lshl_add_u64 v[66:67], v[180:181], 0, s[26:27]
	v_lshl_add_u64 v[68:69], v[182:183], 0, s[26:27]
	global_load_dwordx4 v[106:109], v[2:3], off nt
	global_load_dwordx4 v[94:97], v[4:5], off nt
	global_load_dwordx4 v[74:77], v[10:11], off nt
	global_load_dwordx4 v[54:57], v[12:13], off nt
	global_load_dwordx4 v[38:41], v[18:19], off nt
	s_nop 0
	global_load_dwordx4 v[18:21], v[20:21], off nt
	s_nop 0
	global_load_dwordx4 v[10:13], v[66:67], off nt
	global_load_dwordx4 v[2:5], v[68:69], off nt
	v_mov_b32_e32 v66, v196
	s_waitcnt lgkmcnt(0)
	s_waitcnt vmcnt(23)
	v_pk_fma_f32 v[68:69], v[232:233], v[86:87], 0 op_sel_hi:[0,1,0] neg_lo:[1,0,0] neg_hi:[1,0,0]
	v_pk_fma_f32 v[66:67], v[232:233], v[88:89], 0 op_sel_hi:[0,1,0] neg_lo:[1,0,0] neg_hi:[1,0,0]
	v_cvt_pk_bf16_f32 v68, v68, v69
	v_cvt_pk_bf16_f32 v69, v66, v67
	ds_write_b64 v186, v[68:69]
	s_waitcnt vmcnt(22)
	v_pk_fma_f32 v[68:69], v[234:235], v[82:83], 0 op_sel_hi:[0,1,0] neg_lo:[1,0,0] neg_hi:[1,0,0]
	v_pk_fma_f32 v[66:67], v[234:235], v[84:85], 0 op_sel_hi:[0,1,0] neg_lo:[1,0,0] neg_hi:[1,0,0]
	v_cvt_pk_bf16_f32 v68, v68, v69
	v_cvt_pk_bf16_f32 v69, v66, v67
	ds_write_b64 v186, v[68:69] offset:544
	s_waitcnt vmcnt(21)
	v_pk_fma_f32 v[68:69], v[236:237], v[78:79], 0 op_sel_hi:[0,1,0] neg_lo:[1,0,0] neg_hi:[1,0,0]
	v_pk_fma_f32 v[66:67], v[236:237], v[80:81], 0 op_sel_hi:[0,1,0] neg_lo:[1,0,0] neg_hi:[1,0,0]
	v_cvt_pk_bf16_f32 v68, v68, v69
	v_cvt_pk_bf16_f32 v69, v66, v67
	ds_write_b64 v186, v[68:69] offset:1088
	s_waitcnt vmcnt(20)
	v_pk_fma_f32 v[58:59], v[238:239], v[58:59], 0 op_sel_hi:[0,1,0] neg_lo:[1,0,0] neg_hi:[1,0,0]
	v_pk_fma_f32 v[60:61], v[238:239], v[60:61], 0 op_sel_hi:[0,1,0] neg_lo:[1,0,0] neg_hi:[1,0,0]
	v_cvt_pk_bf16_f32 v58, v58, v59
	v_cvt_pk_bf16_f32 v59, v60, v61
	ds_write_b64 v186, v[58:59] offset:1632
	s_waitcnt vmcnt(19)
	v_pk_fma_f32 v[46:47], v[240:241], v[46:47], 0 op_sel_hi:[0,1,0] neg_lo:[1,0,0] neg_hi:[1,0,0]
	v_pk_fma_f32 v[48:49], v[240:241], v[48:49], 0 op_sel_hi:[0,1,0] neg_lo:[1,0,0] neg_hi:[1,0,0]
	v_cvt_pk_bf16_f32 v46, v46, v47
	v_cvt_pk_bf16_f32 v47, v48, v49
	ds_write_b64 v186, v[46:47] offset:2176
	s_waitcnt vmcnt(18)
	v_pk_fma_f32 v[42:43], v[242:243], v[42:43], 0 op_sel_hi:[0,1,0] neg_lo:[1,0,0] neg_hi:[1,0,0]
	v_pk_fma_f32 v[44:45], v[242:243], v[44:45], 0 op_sel_hi:[0,1,0] neg_lo:[1,0,0] neg_hi:[1,0,0]
	v_cvt_pk_bf16_f32 v42, v42, v43
	v_cvt_pk_bf16_f32 v43, v44, v45
	ds_write_b64 v186, v[42:43] offset:2720
	s_waitcnt vmcnt(17)
	v_pk_fma_f32 v[30:31], v[244:245], v[30:31], 0 op_sel_hi:[0,1,0] neg_lo:[1,0,0] neg_hi:[1,0,0]
	v_pk_fma_f32 v[32:33], v[244:245], v[32:33], 0 op_sel_hi:[0,1,0] neg_lo:[1,0,0] neg_hi:[1,0,0]
	v_cvt_pk_bf16_f32 v30, v30, v31
	v_cvt_pk_bf16_f32 v31, v32, v33
	ds_write_b64 v186, v[30:31] offset:3264
	s_waitcnt vmcnt(16)
	v_pk_fma_f32 v[26:27], v[246:247], v[26:27], 0 op_sel_hi:[0,1,0] neg_lo:[1,0,0] neg_hi:[1,0,0]
	v_pk_fma_f32 v[28:29], v[246:247], v[28:29], 0 op_sel_hi:[0,1,0] neg_lo:[1,0,0] neg_hi:[1,0,0]
	v_cvt_pk_bf16_f32 v26, v26, v27
	v_cvt_pk_bf16_f32 v27, v28, v29
	ds_write_b64 v186, v[26:27] offset:3808
	ds_read_b32 v232, v187 offset:64
	ds_read_b32 v234, v187 offset:72
	ds_read_b32 v236, v187 offset:80
	ds_read_b32 v238, v187 offset:88
	ds_read_b32 v240, v187 offset:96
	ds_read_b32 v242, v187 offset:104
	ds_read_b32 v244, v187 offset:112
	ds_read_b32 v246, v187 offset:120
	ds_read_b128 a[96:99], v1
	ds_read_b128 a[100:103], v1 offset:64
	ds_read_b128 a[104:107], v1 offset:128
	ds_read_b128 a[108:111], v1 offset:192
	v_lshl_add_u64 v[26:27], v[130:131], 0, s[24:25]
	v_add_co_u32_e32 v28, vcc, s7, v26
	s_nop 1
	v_addc_co_u32_e32 v29, vcc, 0, v27, vcc
	global_load_dwordx4 v[102:105], v[26:27], off nt
	global_load_dwordx4 v[90:93], v[28:29], off nt
	v_add_co_u32_e32 v28, vcc, s36, v26
	s_nop 1
	v_addc_co_u32_e32 v29, vcc, 0, v27, vcc
	v_add_co_u32_e32 v30, vcc, s37, v26
	s_nop 1
	v_addc_co_u32_e32 v31, vcc, 0, v27, vcc
	global_load_dwordx4 v[86:89], v[28:29], off nt
	global_load_dwordx4 v[70:73], v[30:31], off nt
	v_add_co_u32_e32 v28, vcc, s38, v26
	s_nop 1
	v_addc_co_u32_e32 v29, vcc, 0, v27, vcc
	v_add_co_u32_e32 v30, vcc, s39, v26
	s_nop 1
	v_addc_co_u32_e32 v31, vcc, 0, v27, vcc
	global_load_dwordx4 v[66:69], v[28:29], off nt
	global_load_dwordx4 v[46:49], v[30:31], off nt
	v_add_co_u32_e32 v28, vcc, s41, v26
	s_nop 1
	v_addc_co_u32_e32 v29, vcc, 0, v27, vcc
	v_add_co_u32_e32 v26, vcc, s42, v26
	s_nop 1
	v_addc_co_u32_e32 v27, vcc, 0, v27, vcc
	global_load_dwordx4 v[42:45], v[28:29], off nt
	global_load_dwordx4 v[30:33], v[26:27], off nt
	v_mov_b32_e32 v26, v196
	s_waitcnt lgkmcnt(0)
	s_waitcnt vmcnt(23)
	v_pk_fma_f32 v[28:29], v[232:233], v[110:111], 0 op_sel_hi:[0,1,0] neg_lo:[1,0,0] neg_hi:[1,0,0]
	v_pk_fma_f32 v[26:27], v[232:233], v[112:113], 0 op_sel_hi:[0,1,0] neg_lo:[1,0,0] neg_hi:[1,0,0]
	v_cvt_pk_bf16_f32 v28, v28, v29
	v_cvt_pk_bf16_f32 v29, v26, v27
	ds_write_b64 v186, v[28:29]
	s_waitcnt vmcnt(22)
	v_pk_fma_f32 v[28:29], v[234:235], v[98:99], 0 op_sel_hi:[0,1,0] neg_lo:[1,0,0] neg_hi:[1,0,0]
	v_pk_fma_f32 v[26:27], v[234:235], v[100:101], 0 op_sel_hi:[0,1,0] neg_lo:[1,0,0] neg_hi:[1,0,0]
	v_cvt_pk_bf16_f32 v28, v28, v29
	v_cvt_pk_bf16_f32 v29, v26, v27
	ds_write_b64 v186, v[28:29] offset:544
	s_waitcnt vmcnt(21)
	v_pk_fma_f32 v[28:29], v[236:237], v[62:63], 0 op_sel_hi:[0,1,0] neg_lo:[1,0,0] neg_hi:[1,0,0]
	v_pk_fma_f32 v[26:27], v[236:237], v[64:65], 0 op_sel_hi:[0,1,0] neg_lo:[1,0,0] neg_hi:[1,0,0]
	v_cvt_pk_bf16_f32 v28, v28, v29
	v_cvt_pk_bf16_f32 v29, v26, v27
	ds_write_b64 v186, v[28:29] offset:1088
	s_waitcnt vmcnt(20)
	v_pk_fma_f32 v[28:29], v[238:239], v[50:51], 0 op_sel_hi:[0,1,0] neg_lo:[1,0,0] neg_hi:[1,0,0]
	v_pk_fma_f32 v[26:27], v[238:239], v[52:53], 0 op_sel_hi:[0,1,0] neg_lo:[1,0,0] neg_hi:[1,0,0]
	v_cvt_pk_bf16_f32 v28, v28, v29
	v_cvt_pk_bf16_f32 v29, v26, v27
	ds_write_b64 v186, v[28:29] offset:1632
	s_waitcnt vmcnt(19)
	v_pk_fma_f32 v[28:29], v[240:241], v[34:35], 0 op_sel_hi:[0,1,0] neg_lo:[1,0,0] neg_hi:[1,0,0]
	v_pk_fma_f32 v[26:27], v[240:241], v[36:37], 0 op_sel_hi:[0,1,0] neg_lo:[1,0,0] neg_hi:[1,0,0]
	v_cvt_pk_bf16_f32 v28, v28, v29
	v_cvt_pk_bf16_f32 v29, v26, v27
	ds_write_b64 v186, v[28:29] offset:2176
	s_waitcnt vmcnt(18)
	v_pk_fma_f32 v[22:23], v[242:243], v[22:23], 0 op_sel_hi:[0,1,0] neg_lo:[1,0,0] neg_hi:[1,0,0]
	v_pk_fma_f32 v[24:25], v[242:243], v[24:25], 0 op_sel_hi:[0,1,0] neg_lo:[1,0,0] neg_hi:[1,0,0]
	v_cvt_pk_bf16_f32 v22, v22, v23
	v_cvt_pk_bf16_f32 v23, v24, v25
	ds_write_b64 v186, v[22:23] offset:2720
	s_waitcnt vmcnt(17)
	v_pk_fma_f32 v[14:15], v[244:245], v[14:15], 0 op_sel_hi:[0,1,0] neg_lo:[1,0,0] neg_hi:[1,0,0]
	v_pk_fma_f32 v[16:17], v[244:245], v[16:17], 0 op_sel_hi:[0,1,0] neg_lo:[1,0,0] neg_hi:[1,0,0]
	v_cvt_pk_bf16_f32 v14, v14, v15
	v_cvt_pk_bf16_f32 v15, v16, v17
	ds_write_b64 v186, v[14:15] offset:3264
	s_waitcnt vmcnt(16)
	v_pk_fma_f32 v[6:7], v[246:247], v[6:7], 0 op_sel_hi:[0,1,0] neg_lo:[1,0,0] neg_hi:[1,0,0]
	v_pk_fma_f32 v[8:9], v[246:247], v[8:9], 0 op_sel_hi:[0,1,0] neg_lo:[1,0,0] neg_hi:[1,0,0]
	v_cvt_pk_bf16_f32 v6, v6, v7
	v_cvt_pk_bf16_f32 v7, v8, v9
	ds_write_b64 v186, v[6:7] offset:3808
	ds_read_b32 v232, v187 offset:128
	ds_read_b32 v234, v187 offset:136
	ds_read_b32 v236, v187 offset:144
	ds_read_b32 v238, v187 offset:152
	ds_read_b32 v240, v187 offset:160
	ds_read_b32 v242, v187 offset:168
	ds_read_b32 v244, v187 offset:176
	ds_read_b32 v246, v187 offset:184
	ds_read_b128 a[112:115], v1
	ds_read_b128 a[116:119], v1 offset:64
	ds_read_b128 a[120:123], v1 offset:128
	ds_read_b128 a[124:127], v1 offset:192
	v_lshl_add_u64 v[6:7], v[150:151], 0, s[24:25]
	v_lshl_add_u64 v[8:9], v[152:153], 0, s[24:25]
	v_lshl_add_u64 v[14:15], v[156:157], 0, s[24:25]
	v_lshl_add_u64 v[16:17], v[158:159], 0, s[24:25]
	v_lshl_add_u64 v[22:23], v[160:161], 0, s[24:25]
	v_lshl_add_u64 v[24:25], v[162:163], 0, s[24:25]
	v_lshl_add_u64 v[26:27], v[164:165], 0, s[24:25]
	v_lshl_add_u64 v[28:29], v[166:167], 0, s[24:25]
	global_load_dwordx4 v[110:113], v[6:7], off nt
	global_load_dwordx4 v[98:101], v[8:9], off nt
	global_load_dwordx4 v[78:81], v[14:15], off nt
	global_load_dwordx4 v[58:61], v[16:17], off nt
	global_load_dwordx4 v[34:37], v[22:23], off nt
	s_nop 0
	global_load_dwordx4 v[22:25], v[24:25], off nt
	s_nop 0
	global_load_dwordx4 v[14:17], v[26:27], off nt
	global_load_dwordx4 v[6:9], v[28:29], off nt
	s_waitcnt lgkmcnt(0)
	s_waitcnt vmcnt(23)
	v_pk_fma_f32 v[28:29], v[232:233], v[106:107], 0 op_sel_hi:[0,1,0] neg_lo:[1,0,0] neg_hi:[1,0,0]
	v_pk_fma_f32 v[26:27], v[232:233], v[108:109], 0 op_sel_hi:[0,1,0] neg_lo:[1,0,0] neg_hi:[1,0,0]
	v_cvt_pk_bf16_f32 v28, v28, v29
	v_cvt_pk_bf16_f32 v29, v26, v27
	ds_write_b64 v186, v[28:29]
	s_waitcnt vmcnt(22)
	v_pk_fma_f32 v[28:29], v[234:235], v[94:95], 0 op_sel_hi:[0,1,0] neg_lo:[1,0,0] neg_hi:[1,0,0]
	v_pk_fma_f32 v[26:27], v[234:235], v[96:97], 0 op_sel_hi:[0,1,0] neg_lo:[1,0,0] neg_hi:[1,0,0]
	v_cvt_pk_bf16_f32 v28, v28, v29
	v_cvt_pk_bf16_f32 v29, v26, v27
	ds_write_b64 v186, v[28:29] offset:544
	s_waitcnt vmcnt(21)
	v_pk_fma_f32 v[28:29], v[236:237], v[74:75], 0 op_sel_hi:[0,1,0] neg_lo:[1,0,0] neg_hi:[1,0,0]
	v_pk_fma_f32 v[26:27], v[236:237], v[76:77], 0 op_sel_hi:[0,1,0] neg_lo:[1,0,0] neg_hi:[1,0,0]
	v_cvt_pk_bf16_f32 v28, v28, v29
	v_cvt_pk_bf16_f32 v29, v26, v27
	ds_write_b64 v186, v[28:29] offset:1088
	s_waitcnt vmcnt(20)
	v_pk_fma_f32 v[28:29], v[238:239], v[54:55], 0 op_sel_hi:[0,1,0] neg_lo:[1,0,0] neg_hi:[1,0,0]
	v_pk_fma_f32 v[26:27], v[238:239], v[56:57], 0 op_sel_hi:[0,1,0] neg_lo:[1,0,0] neg_hi:[1,0,0]
	v_cvt_pk_bf16_f32 v28, v28, v29
	v_cvt_pk_bf16_f32 v29, v26, v27
	ds_write_b64 v186, v[28:29] offset:1632
	s_waitcnt vmcnt(19)
	v_pk_fma_f32 v[28:29], v[240:241], v[38:39], 0 op_sel_hi:[0,1,0] neg_lo:[1,0,0] neg_hi:[1,0,0]
	v_pk_fma_f32 v[26:27], v[240:241], v[40:41], 0 op_sel_hi:[0,1,0] neg_lo:[1,0,0] neg_hi:[1,0,0]
	v_cvt_pk_bf16_f32 v28, v28, v29
	v_cvt_pk_bf16_f32 v29, v26, v27
	ds_write_b64 v186, v[28:29] offset:2176
	s_waitcnt vmcnt(18)
	v_pk_fma_f32 v[18:19], v[242:243], v[18:19], 0 op_sel_hi:[0,1,0] neg_lo:[1,0,0] neg_hi:[1,0,0]
	v_pk_fma_f32 v[20:21], v[242:243], v[20:21], 0 op_sel_hi:[0,1,0] neg_lo:[1,0,0] neg_hi:[1,0,0]
	v_cvt_pk_bf16_f32 v18, v18, v19
	v_cvt_pk_bf16_f32 v19, v20, v21
	ds_write_b64 v186, v[18:19] offset:2720
	s_waitcnt vmcnt(17)
	v_pk_fma_f32 v[10:11], v[244:245], v[10:11], 0 op_sel_hi:[0,1,0] neg_lo:[1,0,0] neg_hi:[1,0,0]
	v_pk_fma_f32 v[12:13], v[244:245], v[12:13], 0 op_sel_hi:[0,1,0] neg_lo:[1,0,0] neg_hi:[1,0,0]
	v_cvt_pk_bf16_f32 v10, v10, v11
	v_cvt_pk_bf16_f32 v11, v12, v13
	ds_write_b64 v186, v[10:11] offset:3264
	s_waitcnt vmcnt(16)
	v_pk_fma_f32 v[2:3], v[246:247], v[2:3], 0 op_sel_hi:[0,1,0] neg_lo:[1,0,0] neg_hi:[1,0,0]
	v_pk_fma_f32 v[4:5], v[246:247], v[4:5], 0 op_sel_hi:[0,1,0] neg_lo:[1,0,0] neg_hi:[1,0,0]
	v_cvt_pk_bf16_f32 v2, v2, v3
	v_cvt_pk_bf16_f32 v3, v4, v5
	ds_write_b64 v186, v[2:3] offset:3808
	ds_read_b32 v232, v187 offset:0
	ds_read_b32 v234, v187 offset:8
	ds_read_b32 v236, v187 offset:16
	ds_read_b32 v238, v187 offset:24
	ds_read_b32 v240, v187 offset:32
	ds_read_b32 v242, v187 offset:40
	ds_read_b32 v244, v187 offset:48
	ds_read_b32 v246, v187 offset:56
	ds_read_b128 a[128:131], v1
	ds_read_b128 a[132:135], v1 offset:64
	ds_read_b128 a[136:139], v1 offset:128
	ds_read_b128 a[140:143], v1 offset:192
	v_lshl_add_u64 v[2:3], v[168:169], 0, s[24:25]
	v_lshl_add_u64 v[4:5], v[170:171], 0, s[24:25]
	v_lshl_add_u64 v[10:11], v[172:173], 0, s[24:25]
	v_lshl_add_u64 v[12:13], v[174:175], 0, s[24:25]
	v_lshl_add_u64 v[18:19], v[176:177], 0, s[24:25]
	v_lshl_add_u64 v[20:21], v[178:179], 0, s[24:25]
	v_lshl_add_u64 v[50:51], v[180:181], 0, s[24:25]
	v_lshl_add_u64 v[52:53], v[182:183], 0, s[24:25]
	global_load_dwordx4 v[114:117], v[2:3], off nt
	global_load_dwordx4 v[94:97], v[4:5], off nt
	global_load_dwordx4 v[82:85], v[10:11], off nt
	global_load_dwordx4 v[62:65], v[12:13], off nt
	global_load_dwordx4 v[38:41], v[18:19], off nt
	global_load_dwordx4 v[26:29], v[20:21], off nt
	s_nop 0
	global_load_dwordx4 v[10:13], v[50:51], off nt
	global_load_dwordx4 v[2:5], v[52:53], off nt
	v_mov_b32_e32 v18, v195
	s_waitcnt lgkmcnt(0)
	s_waitcnt vmcnt(23)
	v_pk_fma_f32 v[20:21], v[232:233], v[102:103], 0 op_sel_hi:[0,1,0] neg_lo:[1,0,0] neg_hi:[1,0,0]
	v_pk_fma_f32 v[18:19], v[232:233], v[104:105], 0 op_sel_hi:[0,1,0] neg_lo:[1,0,0] neg_hi:[1,0,0]
	v_cvt_pk_bf16_f32 v20, v20, v21
	v_cvt_pk_bf16_f32 v21, v18, v19
	ds_write_b64 v186, v[20:21]
	s_waitcnt vmcnt(22)
	v_pk_fma_f32 v[20:21], v[234:235], v[90:91], 0 op_sel_hi:[0,1,0] neg_lo:[1,0,0] neg_hi:[1,0,0]
	v_pk_fma_f32 v[18:19], v[234:235], v[92:93], 0 op_sel_hi:[0,1,0] neg_lo:[1,0,0] neg_hi:[1,0,0]
	v_cvt_pk_bf16_f32 v20, v20, v21
	v_cvt_pk_bf16_f32 v21, v18, v19
	ds_write_b64 v186, v[20:21] offset:544
	s_waitcnt vmcnt(21)
	v_pk_fma_f32 v[20:21], v[236:237], v[86:87], 0 op_sel_hi:[0,1,0] neg_lo:[1,0,0] neg_hi:[1,0,0]
	v_pk_fma_f32 v[18:19], v[236:237], v[88:89], 0 op_sel_hi:[0,1,0] neg_lo:[1,0,0] neg_hi:[1,0,0]
	v_cvt_pk_bf16_f32 v20, v20, v21
	v_cvt_pk_bf16_f32 v21, v18, v19
	ds_write_b64 v186, v[20:21] offset:1088
	s_waitcnt vmcnt(20)
	v_pk_fma_f32 v[20:21], v[238:239], v[70:71], 0 op_sel_hi:[0,1,0] neg_lo:[1,0,0] neg_hi:[1,0,0]
	v_pk_fma_f32 v[18:19], v[238:239], v[72:73], 0 op_sel_hi:[0,1,0] neg_lo:[1,0,0] neg_hi:[1,0,0]
	v_cvt_pk_bf16_f32 v20, v20, v21
	v_cvt_pk_bf16_f32 v21, v18, v19
	ds_write_b64 v186, v[20:21] offset:1632
	s_waitcnt vmcnt(19)
	v_pk_fma_f32 v[20:21], v[240:241], v[66:67], 0 op_sel_hi:[0,1,0] neg_lo:[1,0,0] neg_hi:[1,0,0]
	v_pk_fma_f32 v[18:19], v[240:241], v[68:69], 0 op_sel_hi:[0,1,0] neg_lo:[1,0,0] neg_hi:[1,0,0]
	v_cvt_pk_bf16_f32 v20, v20, v21
	v_cvt_pk_bf16_f32 v21, v18, v19
	ds_write_b64 v186, v[20:21] offset:2176
	s_waitcnt vmcnt(18)
	v_pk_fma_f32 v[20:21], v[242:243], v[46:47], 0 op_sel_hi:[0,1,0] neg_lo:[1,0,0] neg_hi:[1,0,0]
	v_pk_fma_f32 v[18:19], v[242:243], v[48:49], 0 op_sel_hi:[0,1,0] neg_lo:[1,0,0] neg_hi:[1,0,0]
	v_cvt_pk_bf16_f32 v20, v20, v21
	v_cvt_pk_bf16_f32 v21, v18, v19
	ds_write_b64 v186, v[20:21] offset:2720
	s_waitcnt vmcnt(17)
	v_pk_fma_f32 v[20:21], v[244:245], v[42:43], 0 op_sel_hi:[0,1,0] neg_lo:[1,0,0] neg_hi:[1,0,0]
	v_pk_fma_f32 v[18:19], v[244:245], v[44:45], 0 op_sel_hi:[0,1,0] neg_lo:[1,0,0] neg_hi:[1,0,0]
	v_cvt_pk_bf16_f32 v20, v20, v21
	v_cvt_pk_bf16_f32 v21, v18, v19
	ds_write_b64 v186, v[20:21] offset:3264
	s_waitcnt vmcnt(16)
	v_pk_fma_f32 v[20:21], v[246:247], v[30:31], 0 op_sel_hi:[0,1,0] neg_lo:[1,0,0] neg_hi:[1,0,0]
	v_pk_fma_f32 v[18:19], v[246:247], v[32:33], 0 op_sel_hi:[0,1,0] neg_lo:[1,0,0] neg_hi:[1,0,0]
	v_cvt_pk_bf16_f32 v20, v20, v21
	v_cvt_pk_bf16_f32 v21, v18, v19
	ds_write_b64 v186, v[20:21] offset:3808
	ds_read_b32 v232, v187 offset:64
	ds_read_b32 v234, v187 offset:72
	ds_read_b32 v236, v187 offset:80
	ds_read_b32 v238, v187 offset:88
	ds_read_b32 v240, v187 offset:96
	ds_read_b32 v242, v187 offset:104
	ds_read_b32 v244, v187 offset:112
	ds_read_b32 v246, v187 offset:120
	ds_read_b128 a[144:147], v1
	ds_read_b128 a[148:151], v1 offset:64
	ds_read_b128 a[152:155], v1 offset:128
	ds_read_b128 a[156:159], v1 offset:192
	v_lshl_add_u64 v[18:19], v[130:131], 0, s[22:23]
	v_add_co_u32_e32 v20, vcc, s7, v18
	s_nop 1
	v_addc_co_u32_e32 v21, vcc, 0, v19, vcc
	global_load_dwordx4 v[106:109], v[18:19], off nt
	global_load_dwordx4 v[90:93], v[20:21], off nt
	v_add_co_u32_e32 v20, vcc, s36, v18
	s_nop 1
	v_addc_co_u32_e32 v21, vcc, 0, v19, vcc
	v_add_co_u32_e32 v30, vcc, s37, v18
	s_nop 1
	v_addc_co_u32_e32 v31, vcc, 0, v19, vcc
	global_load_dwordx4 v[86:89], v[20:21], off nt
	global_load_dwordx4 v[74:77], v[30:31], off nt
	v_add_co_u32_e32 v20, vcc, s38, v18
	s_nop 1
	v_addc_co_u32_e32 v21, vcc, 0, v19, vcc
	v_add_co_u32_e32 v30, vcc, s39, v18
	s_nop 1
	v_addc_co_u32_e32 v31, vcc, 0, v19, vcc
	global_load_dwordx4 v[70:73], v[20:21], off nt
	global_load_dwordx4 v[54:57], v[30:31], off nt
	v_add_co_u32_e32 v20, vcc, s41, v18
	s_nop 1
	v_addc_co_u32_e32 v21, vcc, 0, v19, vcc
	v_add_co_u32_e32 v18, vcc, s42, v18
	s_nop 1
	v_addc_co_u32_e32 v19, vcc, 0, v19, vcc
	global_load_dwordx4 v[50:53], v[20:21], off nt
	global_load_dwordx4 v[46:49], v[18:19], off nt
	v_mov_b32_e32 v18, v195
	s_waitcnt lgkmcnt(0)
	s_waitcnt vmcnt(23)
	v_pk_fma_f32 v[20:21], v[232:233], v[110:111], 0 op_sel_hi:[0,1,0] neg_lo:[1,0,0] neg_hi:[1,0,0]
	v_pk_fma_f32 v[18:19], v[232:233], v[112:113], 0 op_sel_hi:[0,1,0] neg_lo:[1,0,0] neg_hi:[1,0,0]
	v_cvt_pk_bf16_f32 v20, v20, v21
	v_cvt_pk_bf16_f32 v21, v18, v19
	ds_write_b64 v186, v[20:21]
	s_waitcnt vmcnt(22)
	v_pk_fma_f32 v[20:21], v[234:235], v[98:99], 0 op_sel_hi:[0,1,0] neg_lo:[1,0,0] neg_hi:[1,0,0]
	v_pk_fma_f32 v[18:19], v[234:235], v[100:101], 0 op_sel_hi:[0,1,0] neg_lo:[1,0,0] neg_hi:[1,0,0]
	v_cvt_pk_bf16_f32 v20, v20, v21
	v_cvt_pk_bf16_f32 v21, v18, v19
	ds_write_b64 v186, v[20:21] offset:544
	s_waitcnt vmcnt(21)
	v_pk_fma_f32 v[20:21], v[236:237], v[78:79], 0 op_sel_hi:[0,1,0] neg_lo:[1,0,0] neg_hi:[1,0,0]
	v_pk_fma_f32 v[18:19], v[236:237], v[80:81], 0 op_sel_hi:[0,1,0] neg_lo:[1,0,0] neg_hi:[1,0,0]
	v_cvt_pk_bf16_f32 v20, v20, v21
	v_cvt_pk_bf16_f32 v21, v18, v19
	ds_write_b64 v186, v[20:21] offset:1088
	s_waitcnt vmcnt(20)
	v_pk_fma_f32 v[20:21], v[238:239], v[58:59], 0 op_sel_hi:[0,1,0] neg_lo:[1,0,0] neg_hi:[1,0,0]
	v_pk_fma_f32 v[18:19], v[238:239], v[60:61], 0 op_sel_hi:[0,1,0] neg_lo:[1,0,0] neg_hi:[1,0,0]
	v_cvt_pk_bf16_f32 v20, v20, v21
	v_cvt_pk_bf16_f32 v21, v18, v19
	ds_write_b64 v186, v[20:21] offset:1632
	s_waitcnt vmcnt(19)
	v_pk_fma_f32 v[20:21], v[240:241], v[34:35], 0 op_sel_hi:[0,1,0] neg_lo:[1,0,0] neg_hi:[1,0,0]
	v_pk_fma_f32 v[18:19], v[240:241], v[36:37], 0 op_sel_hi:[0,1,0] neg_lo:[1,0,0] neg_hi:[1,0,0]
	v_cvt_pk_bf16_f32 v20, v20, v21
	v_cvt_pk_bf16_f32 v21, v18, v19
	ds_write_b64 v186, v[20:21] offset:2176
	s_waitcnt vmcnt(18)
	v_pk_fma_f32 v[20:21], v[242:243], v[22:23], 0 op_sel_hi:[0,1,0] neg_lo:[1,0,0] neg_hi:[1,0,0]
	v_pk_fma_f32 v[18:19], v[242:243], v[24:25], 0 op_sel_hi:[0,1,0] neg_lo:[1,0,0] neg_hi:[1,0,0]
	v_cvt_pk_bf16_f32 v20, v20, v21
	v_cvt_pk_bf16_f32 v21, v18, v19
	ds_write_b64 v186, v[20:21] offset:2720
	s_waitcnt vmcnt(17)
	v_pk_fma_f32 v[14:15], v[244:245], v[14:15], 0 op_sel_hi:[0,1,0] neg_lo:[1,0,0] neg_hi:[1,0,0]
	v_pk_fma_f32 v[16:17], v[244:245], v[16:17], 0 op_sel_hi:[0,1,0] neg_lo:[1,0,0] neg_hi:[1,0,0]
	v_cvt_pk_bf16_f32 v14, v14, v15
	v_cvt_pk_bf16_f32 v15, v16, v17
	ds_write_b64 v186, v[14:15] offset:3264
	s_waitcnt vmcnt(16)
	v_pk_fma_f32 v[6:7], v[246:247], v[6:7], 0 op_sel_hi:[0,1,0] neg_lo:[1,0,0] neg_hi:[1,0,0]
	v_pk_fma_f32 v[8:9], v[246:247], v[8:9], 0 op_sel_hi:[0,1,0] neg_lo:[1,0,0] neg_hi:[1,0,0]
	v_cvt_pk_bf16_f32 v6, v6, v7
	v_cvt_pk_bf16_f32 v7, v8, v9
	ds_write_b64 v186, v[6:7] offset:3808
	ds_read_b32 v232, v187 offset:128
	ds_read_b32 v234, v187 offset:136
	ds_read_b32 v236, v187 offset:144
	ds_read_b32 v238, v187 offset:152
	ds_read_b32 v240, v187 offset:160
	ds_read_b32 v242, v187 offset:168
	ds_read_b32 v244, v187 offset:176
	ds_read_b32 v246, v187 offset:184
	ds_read_b128 a[160:163], v1
	ds_read_b128 a[164:167], v1 offset:64
	ds_read_b128 a[168:171], v1 offset:128
	ds_read_b128 a[172:175], v1 offset:192
	v_lshl_add_u64 v[6:7], v[150:151], 0, s[22:23]
	v_lshl_add_u64 v[18:19], v[160:161], 0, s[22:23]
	v_lshl_add_u64 v[20:21], v[162:163], 0, s[22:23]
	v_lshl_add_u64 v[22:23], v[164:165], 0, s[22:23]
	v_lshl_add_u64 v[8:9], v[152:153], 0, s[22:23]
	v_lshl_add_u64 v[14:15], v[156:157], 0, s[22:23]
	v_lshl_add_u64 v[16:17], v[158:159], 0, s[22:23]
	v_lshl_add_u64 v[34:35], v[166:167], 0, s[22:23]
	global_load_dwordx4 v[110:113], v[6:7], off nt
	global_load_dwordx4 v[98:101], v[8:9], off nt
	global_load_dwordx4 v[78:81], v[14:15], off nt
	global_load_dwordx4 v[66:69], v[16:17], off nt
	global_load_dwordx4 v[58:61], v[18:19], off nt
	global_load_dwordx4 v[30:33], v[20:21], off nt
	s_nop 0
	global_load_dwordx4 v[22:25], v[22:23], off nt
	s_nop 0
	global_load_dwordx4 v[18:21], v[34:35], off nt
	s_waitcnt lgkmcnt(0)
	s_waitcnt vmcnt(23)
	v_pk_fma_f32 v[8:9], v[232:233], v[114:115], 0 op_sel_hi:[0,1,0] neg_lo:[1,0,0] neg_hi:[1,0,0]
	v_pk_fma_f32 v[6:7], v[232:233], v[116:117], 0 op_sel_hi:[0,1,0] neg_lo:[1,0,0] neg_hi:[1,0,0]
	v_cvt_pk_bf16_f32 v8, v8, v9
	v_cvt_pk_bf16_f32 v9, v6, v7
	ds_write_b64 v186, v[8:9]
	s_waitcnt vmcnt(22)
	v_pk_fma_f32 v[8:9], v[234:235], v[94:95], 0 op_sel_hi:[0,1,0] neg_lo:[1,0,0] neg_hi:[1,0,0]
	v_pk_fma_f32 v[6:7], v[234:235], v[96:97], 0 op_sel_hi:[0,1,0] neg_lo:[1,0,0] neg_hi:[1,0,0]
	v_cvt_pk_bf16_f32 v8, v8, v9
	v_cvt_pk_bf16_f32 v9, v6, v7
	ds_write_b64 v186, v[8:9] offset:544
	s_waitcnt vmcnt(21)
	v_pk_fma_f32 v[8:9], v[236:237], v[82:83], 0 op_sel_hi:[0,1,0] neg_lo:[1,0,0] neg_hi:[1,0,0]
	v_pk_fma_f32 v[6:7], v[236:237], v[84:85], 0 op_sel_hi:[0,1,0] neg_lo:[1,0,0] neg_hi:[1,0,0]
	v_cvt_pk_bf16_f32 v8, v8, v9
	v_cvt_pk_bf16_f32 v9, v6, v7
	ds_write_b64 v186, v[8:9] offset:1088
	s_waitcnt vmcnt(20)
	v_pk_fma_f32 v[8:9], v[238:239], v[62:63], 0 op_sel_hi:[0,1,0] neg_lo:[1,0,0] neg_hi:[1,0,0]
	v_pk_fma_f32 v[6:7], v[238:239], v[64:65], 0 op_sel_hi:[0,1,0] neg_lo:[1,0,0] neg_hi:[1,0,0]
	v_cvt_pk_bf16_f32 v8, v8, v9
	v_cvt_pk_bf16_f32 v9, v6, v7
	ds_write_b64 v186, v[8:9] offset:1632
	s_waitcnt vmcnt(19)
	v_pk_fma_f32 v[8:9], v[240:241], v[38:39], 0 op_sel_hi:[0,1,0] neg_lo:[1,0,0] neg_hi:[1,0,0]
	v_pk_fma_f32 v[6:7], v[240:241], v[40:41], 0 op_sel_hi:[0,1,0] neg_lo:[1,0,0] neg_hi:[1,0,0]
	v_cvt_pk_bf16_f32 v8, v8, v9
	v_cvt_pk_bf16_f32 v9, v6, v7
	ds_write_b64 v186, v[8:9] offset:2176
	s_waitcnt vmcnt(18)
	v_pk_fma_f32 v[8:9], v[242:243], v[26:27], 0 op_sel_hi:[0,1,0] neg_lo:[1,0,0] neg_hi:[1,0,0]
	v_pk_fma_f32 v[6:7], v[242:243], v[28:29], 0 op_sel_hi:[0,1,0] neg_lo:[1,0,0] neg_hi:[1,0,0]
	v_cvt_pk_bf16_f32 v8, v8, v9
	v_cvt_pk_bf16_f32 v9, v6, v7
	ds_write_b64 v186, v[8:9] offset:2720
	s_waitcnt vmcnt(17)
	v_pk_fma_f32 v[8:9], v[244:245], v[10:11], 0 op_sel_hi:[0,1,0] neg_lo:[1,0,0] neg_hi:[1,0,0]
	v_pk_fma_f32 v[6:7], v[244:245], v[12:13], 0 op_sel_hi:[0,1,0] neg_lo:[1,0,0] neg_hi:[1,0,0]
	v_cvt_pk_bf16_f32 v8, v8, v9
	v_cvt_pk_bf16_f32 v9, v6, v7
	ds_write_b64 v186, v[8:9] offset:3264
	s_waitcnt vmcnt(16)
	v_pk_fma_f32 v[2:3], v[246:247], v[2:3], 0 op_sel_hi:[0,1,0] neg_lo:[1,0,0] neg_hi:[1,0,0]
	v_pk_fma_f32 v[4:5], v[246:247], v[4:5], 0 op_sel_hi:[0,1,0] neg_lo:[1,0,0] neg_hi:[1,0,0]
	v_cvt_pk_bf16_f32 v2, v2, v3
	v_cvt_pk_bf16_f32 v3, v4, v5
	ds_write_b64 v186, v[2:3] offset:3808
	ds_read_b32 v232, v187 offset:0
	ds_read_b32 v234, v187 offset:8
	ds_read_b32 v236, v187 offset:16
	ds_read_b32 v238, v187 offset:24
	ds_read_b32 v240, v187 offset:32
	ds_read_b32 v242, v187 offset:40
	ds_read_b32 v244, v187 offset:48
	ds_read_b32 v246, v187 offset:56
	ds_read_b128 a[176:179], v1
	ds_read_b128 a[180:183], v1 offset:64
	ds_read_b128 a[184:187], v1 offset:128
	ds_read_b128 a[188:191], v1 offset:192
	v_lshl_add_u64 v[2:3], v[168:169], 0, s[22:23]
	v_lshl_add_u64 v[4:5], v[170:171], 0, s[22:23]
	v_lshl_add_u64 v[6:7], v[172:173], 0, s[22:23]
	v_lshl_add_u64 v[8:9], v[174:175], 0, s[22:23]
	v_lshl_add_u64 v[10:11], v[176:177], 0, s[22:23]
	v_lshl_add_u64 v[12:13], v[178:179], 0, s[22:23]
	v_lshl_add_u64 v[14:15], v[180:181], 0, s[22:23]
	v_lshl_add_u64 v[16:17], v[182:183], 0, s[22:23]
	global_load_dwordx4 v[114:117], v[2:3], off nt
	global_load_dwordx4 v[102:105], v[4:5], off nt
	global_load_dwordx4 v[94:97], v[6:7], off nt
	global_load_dwordx4 v[82:85], v[8:9], off nt
	global_load_dwordx4 v[62:65], v[10:11], off nt
	global_load_dwordx4 v[42:45], v[12:13], off nt
	global_load_dwordx4 v[38:41], v[14:15], off nt
	global_load_dwordx4 v[34:37], v[16:17], off nt
	v_mov_b32_e32 v2, v194
	s_waitcnt lgkmcnt(0)
	s_waitcnt vmcnt(23)
	v_pk_fma_f32 v[4:5], v[232:233], v[106:107], 0 op_sel_hi:[0,1,0] neg_lo:[1,0,0] neg_hi:[1,0,0]
	v_pk_fma_f32 v[2:3], v[232:233], v[108:109], 0 op_sel_hi:[0,1,0] neg_lo:[1,0,0] neg_hi:[1,0,0]
	v_cvt_pk_bf16_f32 v4, v4, v5
	v_cvt_pk_bf16_f32 v5, v2, v3
	ds_write_b64 v186, v[4:5]
	s_waitcnt vmcnt(22)
	v_pk_fma_f32 v[4:5], v[234:235], v[90:91], 0 op_sel_hi:[0,1,0] neg_lo:[1,0,0] neg_hi:[1,0,0]
	v_pk_fma_f32 v[2:3], v[234:235], v[92:93], 0 op_sel_hi:[0,1,0] neg_lo:[1,0,0] neg_hi:[1,0,0]
	v_cvt_pk_bf16_f32 v4, v4, v5
	v_cvt_pk_bf16_f32 v5, v2, v3
	ds_write_b64 v186, v[4:5] offset:544
	s_waitcnt vmcnt(21)
	v_pk_fma_f32 v[4:5], v[236:237], v[86:87], 0 op_sel_hi:[0,1,0] neg_lo:[1,0,0] neg_hi:[1,0,0]
	v_pk_fma_f32 v[2:3], v[236:237], v[88:89], 0 op_sel_hi:[0,1,0] neg_lo:[1,0,0] neg_hi:[1,0,0]
	v_cvt_pk_bf16_f32 v4, v4, v5
	v_cvt_pk_bf16_f32 v5, v2, v3
	ds_write_b64 v186, v[4:5] offset:1088
	s_waitcnt vmcnt(20)
	v_pk_fma_f32 v[4:5], v[238:239], v[74:75], 0 op_sel_hi:[0,1,0] neg_lo:[1,0,0] neg_hi:[1,0,0]
	v_pk_fma_f32 v[2:3], v[238:239], v[76:77], 0 op_sel_hi:[0,1,0] neg_lo:[1,0,0] neg_hi:[1,0,0]
	v_cvt_pk_bf16_f32 v4, v4, v5
	v_cvt_pk_bf16_f32 v5, v2, v3
	ds_write_b64 v186, v[4:5] offset:1632
	s_waitcnt vmcnt(19)
	v_pk_fma_f32 v[4:5], v[240:241], v[70:71], 0 op_sel_hi:[0,1,0] neg_lo:[1,0,0] neg_hi:[1,0,0]
	v_pk_fma_f32 v[2:3], v[240:241], v[72:73], 0 op_sel_hi:[0,1,0] neg_lo:[1,0,0] neg_hi:[1,0,0]
	v_cvt_pk_bf16_f32 v4, v4, v5
	v_cvt_pk_bf16_f32 v5, v2, v3
	ds_write_b64 v186, v[4:5] offset:2176
	s_waitcnt vmcnt(18)
	v_pk_fma_f32 v[4:5], v[242:243], v[54:55], 0 op_sel_hi:[0,1,0] neg_lo:[1,0,0] neg_hi:[1,0,0]
	v_pk_fma_f32 v[2:3], v[242:243], v[56:57], 0 op_sel_hi:[0,1,0] neg_lo:[1,0,0] neg_hi:[1,0,0]
	v_cvt_pk_bf16_f32 v4, v4, v5
	v_cvt_pk_bf16_f32 v5, v2, v3
	ds_write_b64 v186, v[4:5] offset:2720
	s_waitcnt vmcnt(17)
	v_pk_fma_f32 v[4:5], v[244:245], v[50:51], 0 op_sel_hi:[0,1,0] neg_lo:[1,0,0] neg_hi:[1,0,0]
	v_pk_fma_f32 v[2:3], v[244:245], v[52:53], 0 op_sel_hi:[0,1,0] neg_lo:[1,0,0] neg_hi:[1,0,0]
	v_cvt_pk_bf16_f32 v4, v4, v5
	v_cvt_pk_bf16_f32 v5, v2, v3
	ds_write_b64 v186, v[4:5] offset:3264
	s_waitcnt vmcnt(16)
	v_pk_fma_f32 v[4:5], v[246:247], v[46:47], 0 op_sel_hi:[0,1,0] neg_lo:[1,0,0] neg_hi:[1,0,0]
	v_pk_fma_f32 v[2:3], v[246:247], v[48:49], 0 op_sel_hi:[0,1,0] neg_lo:[1,0,0] neg_hi:[1,0,0]
	v_cvt_pk_bf16_f32 v4, v4, v5
	v_cvt_pk_bf16_f32 v5, v2, v3
	ds_write_b64 v186, v[4:5] offset:3808
	ds_read_b32 v232, v187 offset:64
	ds_read_b32 v234, v187 offset:72
	ds_read_b32 v236, v187 offset:80
	ds_read_b32 v238, v187 offset:88
	ds_read_b32 v240, v187 offset:96
	ds_read_b32 v242, v187 offset:104
	ds_read_b32 v244, v187 offset:112
	ds_read_b32 v246, v187 offset:120
	ds_read_b128 a[192:195], v1
	ds_read_b128 a[196:199], v1 offset:64
	ds_read_b128 a[200:203], v1 offset:128
	ds_read_b128 a[204:207], v1 offset:192
	v_lshl_add_u64 v[118:119], v[130:131], 0, s[20:21]
	v_add_co_u32_e32 v126, vcc, s7, v118
	s_nop 1
	v_addc_co_u32_e32 v127, vcc, 0, v119, vcc
	v_add_co_u32_e32 v128, vcc, s36, v118
	global_load_dwordx4 v[90:93], v[118:119], off nt
	global_load_dwordx4 v[86:89], v[126:127], off nt
	v_addc_co_u32_e32 v129, vcc, 0, v119, vcc
	v_add_co_u32_e32 v134, vcc, s37, v118
	s_nop 1
	v_addc_co_u32_e32 v135, vcc, 0, v119, vcc
	v_add_co_u32_e32 v136, vcc, s38, v118
	global_load_dwordx4 v[54:57], v[128:129], off nt
	global_load_dwordx4 v[50:53], v[134:135], off nt
	v_addc_co_u32_e32 v137, vcc, 0, v119, vcc
	v_add_co_u32_e32 v138, vcc, s39, v118
	s_nop 1
	v_addc_co_u32_e32 v139, vcc, 0, v119, vcc
	v_add_co_u32_e32 v140, vcc, s41, v118
	global_load_dwordx4 v[14:17], v[136:137], off nt
	global_load_dwordx4 v[10:13], v[138:139], off nt
	v_addc_co_u32_e32 v141, vcc, 0, v119, vcc
	v_add_co_u32_e32 v142, vcc, s42, v118
	s_nop 1
	v_addc_co_u32_e32 v143, vcc, 0, v119, vcc
	global_load_dwordx4 v[6:9], v[140:141], off nt
	global_load_dwordx4 v[2:5], v[142:143], off nt
	v_mov_b32_e32 v26, v194
	s_waitcnt lgkmcnt(0)
	s_waitcnt vmcnt(23)
	v_pk_fma_f32 v[28:29], v[232:233], v[110:111], 0 op_sel_hi:[0,1,0] neg_lo:[1,0,0] neg_hi:[1,0,0]
	v_pk_fma_f32 v[26:27], v[232:233], v[112:113], 0 op_sel_hi:[0,1,0] neg_lo:[1,0,0] neg_hi:[1,0,0]
	v_cvt_pk_bf16_f32 v28, v28, v29
	v_cvt_pk_bf16_f32 v29, v26, v27
	ds_write_b64 v186, v[28:29]
	s_waitcnt vmcnt(22)
	v_pk_fma_f32 v[28:29], v[234:235], v[98:99], 0 op_sel_hi:[0,1,0] neg_lo:[1,0,0] neg_hi:[1,0,0]
	v_pk_fma_f32 v[26:27], v[234:235], v[100:101], 0 op_sel_hi:[0,1,0] neg_lo:[1,0,0] neg_hi:[1,0,0]
	v_cvt_pk_bf16_f32 v28, v28, v29
	v_cvt_pk_bf16_f32 v29, v26, v27
	ds_write_b64 v186, v[28:29] offset:544
	s_waitcnt vmcnt(21)
	v_pk_fma_f32 v[28:29], v[236:237], v[78:79], 0 op_sel_hi:[0,1,0] neg_lo:[1,0,0] neg_hi:[1,0,0]
	v_pk_fma_f32 v[26:27], v[236:237], v[80:81], 0 op_sel_hi:[0,1,0] neg_lo:[1,0,0] neg_hi:[1,0,0]
	v_cvt_pk_bf16_f32 v28, v28, v29
	v_cvt_pk_bf16_f32 v29, v26, v27
	ds_write_b64 v186, v[28:29] offset:1088
	s_waitcnt vmcnt(20)
	v_pk_fma_f32 v[28:29], v[238:239], v[66:67], 0 op_sel_hi:[0,1,0] neg_lo:[1,0,0] neg_hi:[1,0,0]
	v_pk_fma_f32 v[26:27], v[238:239], v[68:69], 0 op_sel_hi:[0,1,0] neg_lo:[1,0,0] neg_hi:[1,0,0]
	v_cvt_pk_bf16_f32 v28, v28, v29
	v_cvt_pk_bf16_f32 v29, v26, v27
	ds_write_b64 v186, v[28:29] offset:1632
	s_waitcnt vmcnt(19)
	v_pk_fma_f32 v[28:29], v[240:241], v[58:59], 0 op_sel_hi:[0,1,0] neg_lo:[1,0,0] neg_hi:[1,0,0]
	v_pk_fma_f32 v[26:27], v[240:241], v[60:61], 0 op_sel_hi:[0,1,0] neg_lo:[1,0,0] neg_hi:[1,0,0]
	v_cvt_pk_bf16_f32 v28, v28, v29
	v_cvt_pk_bf16_f32 v29, v26, v27
	ds_write_b64 v186, v[28:29] offset:2176
	s_waitcnt vmcnt(18)
	v_pk_fma_f32 v[28:29], v[242:243], v[30:31], 0 op_sel_hi:[0,1,0] neg_lo:[1,0,0] neg_hi:[1,0,0]
	v_pk_fma_f32 v[26:27], v[242:243], v[32:33], 0 op_sel_hi:[0,1,0] neg_lo:[1,0,0] neg_hi:[1,0,0]
	v_cvt_pk_bf16_f32 v28, v28, v29
	v_cvt_pk_bf16_f32 v29, v26, v27
	ds_write_b64 v186, v[28:29] offset:2720
	s_waitcnt vmcnt(17)
	v_pk_fma_f32 v[22:23], v[244:245], v[22:23], 0 op_sel_hi:[0,1,0] neg_lo:[1,0,0] neg_hi:[1,0,0]
	v_pk_fma_f32 v[24:25], v[244:245], v[24:25], 0 op_sel_hi:[0,1,0] neg_lo:[1,0,0] neg_hi:[1,0,0]
	v_cvt_pk_bf16_f32 v22, v22, v23
	v_cvt_pk_bf16_f32 v23, v24, v25
	ds_write_b64 v186, v[22:23] offset:3264
	s_waitcnt vmcnt(16)
	v_pk_fma_f32 v[18:19], v[246:247], v[18:19], 0 op_sel_hi:[0,1,0] neg_lo:[1,0,0] neg_hi:[1,0,0]
	v_pk_fma_f32 v[20:21], v[246:247], v[20:21], 0 op_sel_hi:[0,1,0] neg_lo:[1,0,0] neg_hi:[1,0,0]
	v_cvt_pk_bf16_f32 v18, v18, v19
	v_cvt_pk_bf16_f32 v19, v20, v21
	ds_write_b64 v186, v[18:19] offset:3808
	ds_read_b32 v232, v187 offset:128
	ds_read_b32 v234, v187 offset:136
	ds_read_b32 v236, v187 offset:144
	ds_read_b32 v238, v187 offset:152
	ds_read_b32 v240, v187 offset:160
	ds_read_b32 v242, v187 offset:168
	ds_read_b32 v244, v187 offset:176
	ds_read_b32 v246, v187 offset:184
	ds_read_b128 a[208:211], v1
	ds_read_b128 a[212:215], v1 offset:64
	ds_read_b128 a[216:219], v1 offset:128
	ds_read_b128 a[220:223], v1 offset:192
	v_lshl_add_u64 v[18:19], v[150:151], 0, s[20:21]
	v_lshl_add_u64 v[20:21], v[152:153], 0, s[20:21]
	v_lshl_add_u64 v[22:23], v[156:157], 0, s[20:21]
	v_lshl_add_u64 v[24:25], v[158:159], 0, s[20:21]
	v_lshl_add_u64 v[26:27], v[160:161], 0, s[20:21]
	v_lshl_add_u64 v[28:29], v[162:163], 0, s[20:21]
	v_lshl_add_u64 v[46:47], v[164:165], 0, s[20:21]
	v_lshl_add_u64 v[48:49], v[166:167], 0, s[20:21]
	global_load_dwordx4 v[78:81], v[18:19], off nt
	global_load_dwordx4 v[74:77], v[20:21], off nt
	global_load_dwordx4 v[70:73], v[22:23], off nt
	global_load_dwordx4 v[66:69], v[24:25], off nt
	global_load_dwordx4 v[30:33], v[26:27], off nt
	s_nop 0
	global_load_dwordx4 v[26:29], v[28:29], off nt
	s_nop 0
	global_load_dwordx4 v[22:25], v[46:47], off nt
	global_load_dwordx4 v[18:21], v[48:49], off nt
	s_waitcnt lgkmcnt(0)
	s_waitcnt vmcnt(23)
	v_pk_fma_f32 v[48:49], v[232:233], v[114:115], 0 op_sel_hi:[0,1,0] neg_lo:[1,0,0] neg_hi:[1,0,0]
	v_pk_fma_f32 v[46:47], v[232:233], v[116:117], 0 op_sel_hi:[0,1,0] neg_lo:[1,0,0] neg_hi:[1,0,0]
	v_cvt_pk_bf16_f32 v48, v48, v49
	v_cvt_pk_bf16_f32 v49, v46, v47
	ds_write_b64 v186, v[48:49]
	s_waitcnt vmcnt(22)
	v_pk_fma_f32 v[48:49], v[234:235], v[102:103], 0 op_sel_hi:[0,1,0] neg_lo:[1,0,0] neg_hi:[1,0,0]
	v_pk_fma_f32 v[46:47], v[234:235], v[104:105], 0 op_sel_hi:[0,1,0] neg_lo:[1,0,0] neg_hi:[1,0,0]
	v_cvt_pk_bf16_f32 v48, v48, v49
	v_cvt_pk_bf16_f32 v49, v46, v47
	ds_write_b64 v186, v[48:49] offset:544
	s_waitcnt vmcnt(21)
	v_pk_fma_f32 v[48:49], v[236:237], v[94:95], 0 op_sel_hi:[0,1,0] neg_lo:[1,0,0] neg_hi:[1,0,0]
	v_pk_fma_f32 v[46:47], v[236:237], v[96:97], 0 op_sel_hi:[0,1,0] neg_lo:[1,0,0] neg_hi:[1,0,0]
	v_cvt_pk_bf16_f32 v48, v48, v49
	v_cvt_pk_bf16_f32 v49, v46, v47
	ds_write_b64 v186, v[48:49] offset:1088
	s_waitcnt vmcnt(20)
	v_pk_fma_f32 v[48:49], v[238:239], v[82:83], 0 op_sel_hi:[0,1,0] neg_lo:[1,0,0] neg_hi:[1,0,0]
	v_pk_fma_f32 v[46:47], v[238:239], v[84:85], 0 op_sel_hi:[0,1,0] neg_lo:[1,0,0] neg_hi:[1,0,0]
	v_cvt_pk_bf16_f32 v48, v48, v49
	v_cvt_pk_bf16_f32 v49, v46, v47
	ds_write_b64 v186, v[48:49] offset:1632
	s_waitcnt vmcnt(19)
	v_pk_fma_f32 v[48:49], v[240:241], v[62:63], 0 op_sel_hi:[0,1,0] neg_lo:[1,0,0] neg_hi:[1,0,0]
	v_pk_fma_f32 v[46:47], v[240:241], v[64:65], 0 op_sel_hi:[0,1,0] neg_lo:[1,0,0] neg_hi:[1,0,0]
	v_cvt_pk_bf16_f32 v48, v48, v49
	v_cvt_pk_bf16_f32 v49, v46, v47
	ds_write_b64 v186, v[48:49] offset:2176
	s_waitcnt vmcnt(18)
	v_pk_fma_f32 v[42:43], v[242:243], v[42:43], 0 op_sel_hi:[0,1,0] neg_lo:[1,0,0] neg_hi:[1,0,0]
	v_pk_fma_f32 v[44:45], v[242:243], v[44:45], 0 op_sel_hi:[0,1,0] neg_lo:[1,0,0] neg_hi:[1,0,0]
	v_cvt_pk_bf16_f32 v42, v42, v43
	v_cvt_pk_bf16_f32 v43, v44, v45
	ds_write_b64 v186, v[42:43] offset:2720
	s_waitcnt vmcnt(17)
	v_pk_fma_f32 v[38:39], v[244:245], v[38:39], 0 op_sel_hi:[0,1,0] neg_lo:[1,0,0] neg_hi:[1,0,0]
	v_pk_fma_f32 v[40:41], v[244:245], v[40:41], 0 op_sel_hi:[0,1,0] neg_lo:[1,0,0] neg_hi:[1,0,0]
	v_cvt_pk_bf16_f32 v38, v38, v39
	v_cvt_pk_bf16_f32 v39, v40, v41
	ds_write_b64 v186, v[38:39] offset:3264
	s_waitcnt vmcnt(16)
	v_pk_fma_f32 v[34:35], v[246:247], v[34:35], 0 op_sel_hi:[0,1,0] neg_lo:[1,0,0] neg_hi:[1,0,0]
	v_pk_fma_f32 v[36:37], v[246:247], v[36:37], 0 op_sel_hi:[0,1,0] neg_lo:[1,0,0] neg_hi:[1,0,0]
	v_cvt_pk_bf16_f32 v34, v34, v35
	v_cvt_pk_bf16_f32 v35, v36, v37
	ds_write_b64 v186, v[34:35] offset:3808
	ds_read_b32 v232, v187 offset:0
	ds_read_b32 v234, v187 offset:8
	ds_read_b32 v236, v187 offset:16
	ds_read_b32 v238, v187 offset:24
	ds_read_b32 v240, v187 offset:32
	ds_read_b32 v242, v187 offset:40
	ds_read_b32 v244, v187 offset:48
	ds_read_b32 v246, v187 offset:56
	ds_read_b128 a[224:227], v1
	ds_read_b128 a[228:231], v1 offset:64
	ds_read_b128 a[232:235], v1 offset:128
	ds_read_b128 a[236:239], v1 offset:192
	v_lshl_add_u64 v[34:35], v[168:169], 0, s[20:21]
	v_lshl_add_u64 v[36:37], v[170:171], 0, s[20:21]
	v_lshl_add_u64 v[38:39], v[172:173], 0, s[20:21]
	v_lshl_add_u64 v[40:41], v[174:175], 0, s[20:21]
	v_lshl_add_u64 v[42:43], v[176:177], 0, s[20:21]
	v_lshl_add_u64 v[44:45], v[178:179], 0, s[20:21]
	v_lshl_add_u64 v[58:59], v[180:181], 0, s[20:21]
	v_lshl_add_u64 v[60:61], v[182:183], 0, s[20:21]
	global_load_dwordx4 v[122:125], v[34:35], off nt
	global_load_dwordx4 v[106:109], v[36:37], off nt
	global_load_dwordx4 v[94:97], v[38:39], off nt
	global_load_dwordx4 v[82:85], v[40:41], off nt
	global_load_dwordx4 v[46:49], v[42:43], off nt
	s_nop 0
	global_load_dwordx4 v[42:45], v[44:45], off nt
	s_nop 0
	global_load_dwordx4 v[38:41], v[58:59], off nt
	global_load_dwordx4 v[34:37], v[60:61], off nt
	v_mov_b32_e32 v98, v133
	v_add_u32_e32 v99, 1, v98
	v_cmp_eq_u32_e32 vcc, v98, v132
	s_nop 1
	v_cndmask_b32_e64 v60, 0, 1.0, vcc
	v_cmp_eq_u32_e32 vcc, v99, v132
	s_nop 1
	v_cndmask_b32_e64 v61, 0, 1.0, vcc
	s_waitcnt lgkmcnt(0)
	s_waitcnt vmcnt(23)
	v_pk_fma_f32 v[62:63], v[232:233], v[90:91], v[60:61] op_sel_hi:[0,1,1] neg_lo:[1,0,0] neg_hi:[1,0,0]
	v_add_u32_e32 v90, 3, v98
	v_add_u32_e32 v91, 2, v98
	v_cmp_eq_u32_e32 vcc, v90, v132
	v_cvt_pk_bf16_f32 v62, v62, v63
	s_nop 0
	v_cndmask_b32_e64 v65, 0, 1.0, vcc
	v_cmp_eq_u32_e32 vcc, v91, v132
	s_nop 1
	v_cndmask_b32_e64 v64, 0, 1.0, vcc
	v_pk_fma_f32 v[58:59], v[232:233], v[92:93], v[64:65] op_sel_hi:[0,1,1] neg_lo:[1,0,0] neg_hi:[1,0,0]
	v_cvt_pk_bf16_f32 v63, v58, v59
	ds_write_b64 v186, v[62:63]
	v_cmp_eq_u32_e32 vcc, v98, v193
	s_nop 1
	v_cndmask_b32_e64 v62, 0, 1.0, vcc
	v_cmp_eq_u32_e32 vcc, v99, v193
	s_nop 1
	v_cndmask_b32_e64 v63, 0, 1.0, vcc
	v_cmp_eq_u32_e32 vcc, v90, v193
	s_waitcnt vmcnt(22)
	v_pk_fma_f32 v[62:63], v[234:235], v[86:87], v[62:63] op_sel_hi:[0,1,1] neg_lo:[1,0,0] neg_hi:[1,0,0]
	v_cvt_pk_bf16_f32 v62, v62, v63
	v_cndmask_b32_e64 v61, 0, 1.0, vcc
	v_pk_fma_f32 v[58:59], v[234:235], v[88:89], v[60:61] op_sel_hi:[0,1,1] neg_lo:[1,0,0] neg_hi:[1,0,0]
	v_cvt_pk_bf16_f32 v63, v58, v59
	ds_write_b64 v186, v[62:63] offset:544
	v_cmp_eq_u32_e32 vcc, v98, v192
	s_nop 1
	v_cndmask_b32_e64 v60, 0, 1.0, vcc
	v_cmp_eq_u32_e32 vcc, v99, v192
	s_nop 1
	v_cndmask_b32_e64 v61, 0, 1.0, vcc
	v_cmp_eq_u32_e32 vcc, v90, v192
	s_waitcnt vmcnt(21)
	v_pk_fma_f32 v[54:55], v[236:237], v[54:55], v[60:61] op_sel_hi:[0,1,1] neg_lo:[1,0,0] neg_hi:[1,0,0]
	v_cvt_pk_bf16_f32 v54, v54, v55
	v_cndmask_b32_e64 v61, 0, 1.0, vcc
	v_cmp_eq_u32_e32 vcc, v91, v192
	s_nop 1
	v_cndmask_b32_e64 v60, 0, 1.0, vcc
	v_pk_fma_f32 v[56:57], v[236:237], v[56:57], v[60:61] op_sel_hi:[0,1,1] neg_lo:[1,0,0] neg_hi:[1,0,0]
	v_cvt_pk_bf16_f32 v55, v56, v57
	ds_write_b64 v186, v[54:55] offset:1088
	v_cmp_eq_u32_e32 vcc, v98, v190
	s_nop 1
	v_cndmask_b32_e64 v56, 0, 1.0, vcc
	v_cmp_eq_u32_e32 vcc, v99, v190
	s_nop 1
	v_cndmask_b32_e64 v57, 0, 1.0, vcc
	v_cmp_eq_u32_e32 vcc, v90, v190
	s_waitcnt vmcnt(20)
	v_pk_fma_f32 v[50:51], v[238:239], v[50:51], v[56:57] op_sel_hi:[0,1,1] neg_lo:[1,0,0] neg_hi:[1,0,0]
	v_cvt_pk_bf16_f32 v50, v50, v51
	v_cndmask_b32_e64 v57, 0, 1.0, vcc
	v_cmp_eq_u32_e32 vcc, v91, v190
	s_nop 1
	v_cndmask_b32_e64 v56, 0, 1.0, vcc
	v_pk_fma_f32 v[52:53], v[238:239], v[52:53], v[56:57] op_sel_hi:[0,1,1] neg_lo:[1,0,0] neg_hi:[1,0,0]
	v_cvt_pk_bf16_f32 v51, v52, v53
	ds_write_b64 v186, v[50:51] offset:1632
	v_cmp_eq_u32_e32 vcc, v98, v149
	s_nop 1
	v_cndmask_b32_e64 v52, 0, 1.0, vcc
	v_cmp_eq_u32_e32 vcc, v99, v149
	s_nop 1
	v_cndmask_b32_e64 v53, 0, 1.0, vcc
	v_cmp_eq_u32_e32 vcc, v90, v149
	s_waitcnt vmcnt(19)
	v_pk_fma_f32 v[14:15], v[240:241], v[14:15], v[52:53] op_sel_hi:[0,1,1] neg_lo:[1,0,0] neg_hi:[1,0,0]
	v_cvt_pk_bf16_f32 v14, v14, v15
	v_cndmask_b32_e64 v53, 0, 1.0, vcc
	v_cmp_eq_u32_e32 vcc, v91, v149
	s_nop 1
	v_cndmask_b32_e64 v52, 0, 1.0, vcc
	v_pk_fma_f32 v[16:17], v[240:241], v[16:17], v[52:53] op_sel_hi:[0,1,1] neg_lo:[1,0,0] neg_hi:[1,0,0]
	v_cvt_pk_bf16_f32 v15, v16, v17
	ds_write_b64 v186, v[14:15] offset:2176
	v_cmp_eq_u32_e32 vcc, v98, v148
	s_nop 1
	v_cndmask_b32_e64 v16, 0, 1.0, vcc
	v_cmp_eq_u32_e32 vcc, v99, v148
	s_nop 1
	v_cndmask_b32_e64 v17, 0, 1.0, vcc
	v_cmp_eq_u32_e32 vcc, v90, v148
	s_waitcnt vmcnt(18)
	v_pk_fma_f32 v[10:11], v[242:243], v[10:11], v[16:17] op_sel_hi:[0,1,1] neg_lo:[1,0,0] neg_hi:[1,0,0]
	v_cvt_pk_bf16_f32 v10, v10, v11
	v_cndmask_b32_e64 v17, 0, 1.0, vcc
	v_cmp_eq_u32_e32 vcc, v91, v148
	s_nop 1
	v_cndmask_b32_e64 v16, 0, 1.0, vcc
	v_pk_fma_f32 v[12:13], v[242:243], v[12:13], v[16:17] op_sel_hi:[0,1,1] neg_lo:[1,0,0] neg_hi:[1,0,0]
	v_cvt_pk_bf16_f32 v11, v12, v13
	ds_write_b64 v186, v[10:11] offset:2720
	v_cmp_eq_u32_e32 vcc, v98, v147
	s_nop 1
	v_cndmask_b32_e64 v12, 0, 1.0, vcc
	v_cmp_eq_u32_e32 vcc, v99, v147
	s_nop 1
	v_cndmask_b32_e64 v13, 0, 1.0, vcc
	v_cmp_eq_u32_e32 vcc, v90, v147
	s_waitcnt vmcnt(17)
	v_pk_fma_f32 v[6:7], v[244:245], v[6:7], v[12:13] op_sel_hi:[0,1,1] neg_lo:[1,0,0] neg_hi:[1,0,0]
	v_cvt_pk_bf16_f32 v6, v6, v7
	v_cndmask_b32_e64 v13, 0, 1.0, vcc
	v_cmp_eq_u32_e32 vcc, v91, v147
	s_nop 1
	v_cndmask_b32_e64 v12, 0, 1.0, vcc
	v_pk_fma_f32 v[8:9], v[244:245], v[8:9], v[12:13] op_sel_hi:[0,1,1] neg_lo:[1,0,0] neg_hi:[1,0,0]
	v_cvt_pk_bf16_f32 v7, v8, v9
	ds_write_b64 v186, v[6:7] offset:3264
	v_cmp_eq_u32_e32 vcc, v98, v146
	s_nop 1
	v_cndmask_b32_e64 v8, 0, 1.0, vcc
	v_cmp_eq_u32_e32 vcc, v99, v146
	s_nop 1
	v_cndmask_b32_e64 v9, 0, 1.0, vcc
	v_cmp_eq_u32_e32 vcc, v90, v146
	s_waitcnt vmcnt(16)
	v_pk_fma_f32 v[2:3], v[246:247], v[2:3], v[8:9] op_sel_hi:[0,1,1] neg_lo:[1,0,0] neg_hi:[1,0,0]
	v_cvt_pk_bf16_f32 v2, v2, v3
	v_cndmask_b32_e64 v9, 0, 1.0, vcc
	v_cmp_eq_u32_e32 vcc, v91, v146
	s_nop 1
	v_cndmask_b32_e64 v8, 0, 1.0, vcc
	v_pk_fma_f32 v[4:5], v[246:247], v[4:5], v[8:9] op_sel_hi:[0,1,1] neg_lo:[1,0,0] neg_hi:[1,0,0]
	v_cvt_pk_bf16_f32 v3, v4, v5
	ds_write_b64 v186, v[2:3] offset:3808
	ds_read_b32 v232, v187 offset:64
	ds_read_b32 v234, v187 offset:72
	ds_read_b32 v236, v187 offset:80
	ds_read_b32 v238, v187 offset:88
	ds_read_b32 v240, v187 offset:96
	ds_read_b32 v242, v187 offset:104
	ds_read_b32 v244, v187 offset:112
	ds_read_b32 v246, v187 offset:120
	ds_read_b128 v[2:5], v1
	ds_read_b128 v[6:9], v1 offset:64
	ds_read_b128 v[10:13], v1 offset:128
	ds_read_b128 v[14:17], v1 offset:192
	global_load_dwordx4 v[118:121], v[118:119], off offset:512 nt
	s_nop 0
	global_load_dwordx4 v[110:113], v[126:127], off offset:512 nt
	global_load_dwordx4 v[98:101], v[128:129], off offset:512 nt
	global_load_dwordx4 v[86:89], v[134:135], off offset:512 nt
	global_load_dwordx4 v[62:65], v[136:137], off offset:512 nt
	global_load_dwordx4 v[58:61], v[138:139], off offset:512 nt
	global_load_dwordx4 v[54:57], v[140:141], off offset:512 nt
	global_load_dwordx4 v[50:53], v[142:143], off offset:512 nt
	v_mov_b32_e32 v91, v133
	v_or_b32_e32 v138, 16, v132
	v_add_u32_e32 v102, 1, v91
	v_cmp_eq_u32_e32 vcc, v91, v138
	v_add_u32_e32 v103, 3, v91
	v_add_u32_e32 v104, 2, v91
	v_cndmask_b32_e64 v92, 0, 1.0, vcc
	v_cmp_eq_u32_e32 vcc, v102, v138
	v_or_b32_e32 v139, 18, v132
	v_or_b32_e32 v140, 20, v132
	v_cndmask_b32_e64 v93, 0, 1.0, vcc
	v_cmp_eq_u32_e32 vcc, v103, v138
	s_waitcnt lgkmcnt(0)
	s_waitcnt vmcnt(23)
	v_pk_fma_f32 v[78:79], v[232:233], v[78:79], v[92:93] op_sel_hi:[0,1,1] neg_lo:[1,0,0] neg_hi:[1,0,0]
	v_cvt_pk_bf16_f32 v78, v78, v79
	v_cndmask_b32_e64 v93, 0, 1.0, vcc
	v_cmp_eq_u32_e32 vcc, v104, v138
	v_or_b32_e32 v141, 22, v132
	v_or_b32_e32 v142, 24, v132
	v_cndmask_b32_e64 v92, 0, 1.0, vcc
	v_pk_fma_f32 v[80:81], v[232:233], v[80:81], v[92:93] op_sel_hi:[0,1,1] neg_lo:[1,0,0] neg_hi:[1,0,0]
	v_cvt_pk_bf16_f32 v79, v80, v81
	ds_write_b64 v186, v[78:79]
	v_cmp_eq_u32_e32 vcc, v91, v139
	v_or_b32_e32 v143, 26, v132
	v_or_b32_e32 v144, 28, v132
	v_cndmask_b32_e64 v80, 0, 1.0, vcc
	v_cmp_eq_u32_e32 vcc, v102, v139
	v_or_b32_e32 v145, 30, v132
	s_nop 0
	v_cndmask_b32_e64 v81, 0, 1.0, vcc
	v_cmp_eq_u32_e32 vcc, v103, v139
	s_waitcnt vmcnt(22)
	v_pk_fma_f32 v[74:75], v[234:235], v[74:75], v[80:81] op_sel_hi:[0,1,1] neg_lo:[1,0,0] neg_hi:[1,0,0]
	v_cvt_pk_bf16_f32 v74, v74, v75
	v_cndmask_b32_e64 v81, 0, 1.0, vcc
	v_cmp_eq_u32_e32 vcc, v104, v139
	s_nop 1
	v_cndmask_b32_e64 v80, 0, 1.0, vcc
	v_pk_fma_f32 v[76:77], v[234:235], v[76:77], v[80:81] op_sel_hi:[0,1,1] neg_lo:[1,0,0] neg_hi:[1,0,0]
	v_cvt_pk_bf16_f32 v75, v76, v77
	ds_write_b64 v186, v[74:75] offset:544
	v_cmp_eq_u32_e32 vcc, v91, v140
	s_nop 1
	v_cndmask_b32_e64 v76, 0, 1.0, vcc
	v_cmp_eq_u32_e32 vcc, v102, v140
	s_nop 1
	v_cndmask_b32_e64 v77, 0, 1.0, vcc
	v_cmp_eq_u32_e32 vcc, v103, v140
	s_waitcnt vmcnt(21)
	v_pk_fma_f32 v[70:71], v[236:237], v[70:71], v[76:77] op_sel_hi:[0,1,1] neg_lo:[1,0,0] neg_hi:[1,0,0]
	v_cvt_pk_bf16_f32 v70, v70, v71
	v_cndmask_b32_e64 v77, 0, 1.0, vcc
	v_cmp_eq_u32_e32 vcc, v104, v140
	s_nop 1
	v_cndmask_b32_e64 v76, 0, 1.0, vcc
	v_pk_fma_f32 v[72:73], v[236:237], v[72:73], v[76:77] op_sel_hi:[0,1,1] neg_lo:[1,0,0] neg_hi:[1,0,0]
	v_cvt_pk_bf16_f32 v71, v72, v73
	ds_write_b64 v186, v[70:71] offset:1088
	v_cmp_eq_u32_e32 vcc, v91, v141
	s_nop 1
	v_cndmask_b32_e64 v72, 0, 1.0, vcc
	v_cmp_eq_u32_e32 vcc, v102, v141
	s_nop 1
	v_cndmask_b32_e64 v73, 0, 1.0, vcc
	v_cmp_eq_u32_e32 vcc, v103, v141
	s_waitcnt vmcnt(20)
	v_pk_fma_f32 v[66:67], v[238:239], v[66:67], v[72:73] op_sel_hi:[0,1,1] neg_lo:[1,0,0] neg_hi:[1,0,0]
	v_cvt_pk_bf16_f32 v66, v66, v67
	v_cndmask_b32_e64 v73, 0, 1.0, vcc
	v_cmp_eq_u32_e32 vcc, v104, v141
	s_nop 1
	v_cndmask_b32_e64 v72, 0, 1.0, vcc
	v_pk_fma_f32 v[68:69], v[238:239], v[68:69], v[72:73] op_sel_hi:[0,1,1] neg_lo:[1,0,0] neg_hi:[1,0,0]
	v_cvt_pk_bf16_f32 v67, v68, v69
	ds_write_b64 v186, v[66:67] offset:1632
	v_cmp_eq_u32_e32 vcc, v91, v142
	s_nop 1
	v_cndmask_b32_e64 v68, 0, 1.0, vcc
	v_cmp_eq_u32_e32 vcc, v102, v142
	s_nop 1
	v_cndmask_b32_e64 v69, 0, 1.0, vcc
	v_cmp_eq_u32_e32 vcc, v103, v142
	s_waitcnt vmcnt(19)
	v_pk_fma_f32 v[30:31], v[240:241], v[30:31], v[68:69] op_sel_hi:[0,1,1] neg_lo:[1,0,0] neg_hi:[1,0,0]
	v_cvt_pk_bf16_f32 v30, v30, v31
	v_cndmask_b32_e64 v69, 0, 1.0, vcc
	v_cmp_eq_u32_e32 vcc, v104, v142
	s_nop 1
	v_cndmask_b32_e64 v68, 0, 1.0, vcc
	v_pk_fma_f32 v[32:33], v[240:241], v[32:33], v[68:69] op_sel_hi:[0,1,1] neg_lo:[1,0,0] neg_hi:[1,0,0]
	v_cvt_pk_bf16_f32 v31, v32, v33
	ds_write_b64 v186, v[30:31] offset:2176
	v_cmp_eq_u32_e32 vcc, v91, v143
	s_nop 1
	v_cndmask_b32_e64 v32, 0, 1.0, vcc
	v_cmp_eq_u32_e32 vcc, v102, v143
	s_nop 1
	v_cndmask_b32_e64 v33, 0, 1.0, vcc
	v_cmp_eq_u32_e32 vcc, v103, v143
	s_waitcnt vmcnt(18)
	v_pk_fma_f32 v[26:27], v[242:243], v[26:27], v[32:33] op_sel_hi:[0,1,1] neg_lo:[1,0,0] neg_hi:[1,0,0]
	v_cvt_pk_bf16_f32 v26, v26, v27
	v_cndmask_b32_e64 v33, 0, 1.0, vcc
	v_cmp_eq_u32_e32 vcc, v104, v143
	s_nop 1
	v_cndmask_b32_e64 v32, 0, 1.0, vcc
	v_pk_fma_f32 v[28:29], v[242:243], v[28:29], v[32:33] op_sel_hi:[0,1,1] neg_lo:[1,0,0] neg_hi:[1,0,0]
	v_cvt_pk_bf16_f32 v27, v28, v29
	ds_write_b64 v186, v[26:27] offset:2720
	v_cmp_eq_u32_e32 vcc, v91, v144
	s_nop 1
	v_cndmask_b32_e64 v28, 0, 1.0, vcc
	v_cmp_eq_u32_e32 vcc, v102, v144
	s_nop 1
	v_cndmask_b32_e64 v29, 0, 1.0, vcc
	v_cmp_eq_u32_e32 vcc, v103, v144
	s_waitcnt vmcnt(17)
	v_pk_fma_f32 v[22:23], v[244:245], v[22:23], v[28:29] op_sel_hi:[0,1,1] neg_lo:[1,0,0] neg_hi:[1,0,0]
	v_cvt_pk_bf16_f32 v22, v22, v23
	v_cndmask_b32_e64 v29, 0, 1.0, vcc
	v_cmp_eq_u32_e32 vcc, v104, v144
	s_nop 1
	v_cndmask_b32_e64 v28, 0, 1.0, vcc
	v_pk_fma_f32 v[24:25], v[244:245], v[24:25], v[28:29] op_sel_hi:[0,1,1] neg_lo:[1,0,0] neg_hi:[1,0,0]
	v_cvt_pk_bf16_f32 v23, v24, v25
	ds_write_b64 v186, v[22:23] offset:3264
	v_cmp_eq_u32_e32 vcc, v91, v145
	s_nop 1
	v_cndmask_b32_e64 v24, 0, 1.0, vcc
	v_cmp_eq_u32_e32 vcc, v102, v145
	s_nop 1
	v_cndmask_b32_e64 v25, 0, 1.0, vcc
	v_cmp_eq_u32_e32 vcc, v103, v145
	s_waitcnt vmcnt(16)
	v_pk_fma_f32 v[18:19], v[246:247], v[18:19], v[24:25] op_sel_hi:[0,1,1] neg_lo:[1,0,0] neg_hi:[1,0,0]
	v_cvt_pk_bf16_f32 v18, v18, v19
	v_cndmask_b32_e64 v25, 0, 1.0, vcc
	v_cmp_eq_u32_e32 vcc, v104, v145
	s_nop 1
	v_cndmask_b32_e64 v24, 0, 1.0, vcc
	v_pk_fma_f32 v[20:21], v[246:247], v[20:21], v[24:25] op_sel_hi:[0,1,1] neg_lo:[1,0,0] neg_hi:[1,0,0]
	v_cvt_pk_bf16_f32 v19, v20, v21
	ds_write_b64 v186, v[18:19] offset:3808
	ds_read_b32 v232, v187 offset:128
	ds_read_b32 v234, v187 offset:136
	ds_read_b32 v236, v187 offset:144
	ds_read_b32 v238, v187 offset:152
	ds_read_b32 v240, v187 offset:160
	ds_read_b32 v242, v187 offset:168
	ds_read_b32 v244, v187 offset:176
	ds_read_b32 v246, v187 offset:184
	ds_read_b128 v[18:21], v1
	ds_read_b128 v[22:25], v1 offset:64
	ds_read_b128 v[26:29], v1 offset:128
	ds_read_b128 v[30:33], v1 offset:192
	v_lshl_add_u64 v[66:67], v[150:151], 0, s[8:9]
	v_lshl_add_u64 v[68:69], v[152:153], 0, s[8:9]
	v_lshl_add_u64 v[70:71], v[156:157], 0, s[8:9]
	v_lshl_add_u64 v[72:73], v[158:159], 0, s[8:9]
	v_lshl_add_u64 v[74:75], v[160:161], 0, s[8:9]
	v_lshl_add_u64 v[76:77], v[162:163], 0, s[8:9]
	v_lshl_add_u64 v[134:135], v[164:165], 0, s[8:9]
	v_lshl_add_u64 v[136:137], v[166:167], 0, s[8:9]
	global_load_dwordx4 v[126:129], v[66:67], off nt
	global_load_dwordx4 v[114:117], v[68:69], off nt
	global_load_dwordx4 v[102:105], v[70:71], off nt
	global_load_dwordx4 v[90:93], v[72:73], off nt
	global_load_dwordx4 v[78:81], v[74:75], off nt
	s_nop 0
	global_load_dwordx4 v[74:77], v[76:77], off nt
	s_nop 0
	global_load_dwordx4 v[70:73], v[134:135], off nt
	global_load_dwordx4 v[66:69], v[136:137], off nt
	v_or_b32_e32 v194, 32, v132
	v_add_u32_e32 v135, 1, v133
	v_cmp_eq_u32_e32 vcc, v133, v194
	v_add_u32_e32 v202, 3, v133
	v_add_u32_e32 v203, 2, v133
	v_cndmask_b32_e64 v136, 0, 1.0, vcc
	v_cmp_eq_u32_e32 vcc, v135, v194
	v_or_b32_e32 v195, 34, v132
	v_or_b32_e32 v196, 36, v132
	v_cndmask_b32_e64 v137, 0, 1.0, vcc
	v_cmp_eq_u32_e32 vcc, v202, v194
	s_waitcnt lgkmcnt(0)
	s_waitcnt vmcnt(23)
	v_pk_fma_f32 v[122:123], v[232:233], v[122:123], v[136:137] op_sel_hi:[0,1,1] neg_lo:[1,0,0] neg_hi:[1,0,0]
	v_cvt_pk_bf16_f32 v122, v122, v123
	v_cndmask_b32_e64 v137, 0, 1.0, vcc
	v_cmp_eq_u32_e32 vcc, v203, v194
	v_or_b32_e32 v197, 38, v132
	v_or_b32_e32 v198, 40, v132
	v_cndmask_b32_e64 v136, 0, 1.0, vcc
	v_pk_fma_f32 v[124:125], v[232:233], v[124:125], v[136:137] op_sel_hi:[0,1,1] neg_lo:[1,0,0] neg_hi:[1,0,0]
	v_cvt_pk_bf16_f32 v123, v124, v125
	ds_write_b64 v186, v[122:123]
	v_cmp_eq_u32_e32 vcc, v133, v195
	v_or_b32_e32 v199, 42, v132
	v_or_b32_e32 v200, 44, v132
	v_cndmask_b32_e64 v124, 0, 1.0, vcc
	v_cmp_eq_u32_e32 vcc, v135, v195
	v_or_b32_e32 v201, 46, v132
	s_nop 0
	v_cndmask_b32_e64 v125, 0, 1.0, vcc
	v_cmp_eq_u32_e32 vcc, v202, v195
	s_waitcnt vmcnt(22)
	v_pk_fma_f32 v[106:107], v[234:235], v[106:107], v[124:125] op_sel_hi:[0,1,1] neg_lo:[1,0,0] neg_hi:[1,0,0]
	v_cvt_pk_bf16_f32 v106, v106, v107
	v_cndmask_b32_e64 v125, 0, 1.0, vcc
	v_cmp_eq_u32_e32 vcc, v203, v195
	s_nop 1
	v_cndmask_b32_e64 v124, 0, 1.0, vcc
	v_pk_fma_f32 v[108:109], v[234:235], v[108:109], v[124:125] op_sel_hi:[0,1,1] neg_lo:[1,0,0] neg_hi:[1,0,0]
	v_cvt_pk_bf16_f32 v107, v108, v109
	ds_write_b64 v186, v[106:107] offset:544
	v_cmp_eq_u32_e32 vcc, v133, v196
	s_nop 1
	v_cndmask_b32_e64 v108, 0, 1.0, vcc
	v_cmp_eq_u32_e32 vcc, v135, v196
	s_nop 1
	v_cndmask_b32_e64 v109, 0, 1.0, vcc
	v_cmp_eq_u32_e32 vcc, v202, v196
	s_waitcnt vmcnt(21)
	v_pk_fma_f32 v[94:95], v[236:237], v[94:95], v[108:109] op_sel_hi:[0,1,1] neg_lo:[1,0,0] neg_hi:[1,0,0]
	v_cvt_pk_bf16_f32 v94, v94, v95
	v_cndmask_b32_e64 v109, 0, 1.0, vcc
	v_cmp_eq_u32_e32 vcc, v203, v196
	s_nop 1
	v_cndmask_b32_e64 v108, 0, 1.0, vcc
	v_pk_fma_f32 v[96:97], v[236:237], v[96:97], v[108:109] op_sel_hi:[0,1,1] neg_lo:[1,0,0] neg_hi:[1,0,0]
	v_cvt_pk_bf16_f32 v95, v96, v97
	ds_write_b64 v186, v[94:95] offset:1088
	v_cmp_eq_u32_e32 vcc, v133, v197
	s_nop 1
	v_cndmask_b32_e64 v96, 0, 1.0, vcc
	v_cmp_eq_u32_e32 vcc, v135, v197
	s_nop 1
	v_cndmask_b32_e64 v97, 0, 1.0, vcc
	v_cmp_eq_u32_e32 vcc, v202, v197
	s_waitcnt vmcnt(20)
	v_pk_fma_f32 v[82:83], v[238:239], v[82:83], v[96:97] op_sel_hi:[0,1,1] neg_lo:[1,0,0] neg_hi:[1,0,0]
	v_cvt_pk_bf16_f32 v82, v82, v83
	v_cndmask_b32_e64 v97, 0, 1.0, vcc
	v_cmp_eq_u32_e32 vcc, v203, v197
	s_nop 1
	v_cndmask_b32_e64 v96, 0, 1.0, vcc
	v_pk_fma_f32 v[84:85], v[238:239], v[84:85], v[96:97] op_sel_hi:[0,1,1] neg_lo:[1,0,0] neg_hi:[1,0,0]
	v_cvt_pk_bf16_f32 v83, v84, v85
	ds_write_b64 v186, v[82:83] offset:1632
	v_cmp_eq_u32_e32 vcc, v133, v198
	s_nop 1
	v_cndmask_b32_e64 v84, 0, 1.0, vcc
	v_cmp_eq_u32_e32 vcc, v135, v198
	s_nop 1
	v_cndmask_b32_e64 v85, 0, 1.0, vcc
	v_cmp_eq_u32_e32 vcc, v202, v198
	s_waitcnt vmcnt(19)
	v_pk_fma_f32 v[46:47], v[240:241], v[46:47], v[84:85] op_sel_hi:[0,1,1] neg_lo:[1,0,0] neg_hi:[1,0,0]
	v_cvt_pk_bf16_f32 v46, v46, v47
	v_cndmask_b32_e64 v85, 0, 1.0, vcc
	v_cmp_eq_u32_e32 vcc, v203, v198
	s_nop 1
	v_cndmask_b32_e64 v84, 0, 1.0, vcc
	v_pk_fma_f32 v[48:49], v[240:241], v[48:49], v[84:85] op_sel_hi:[0,1,1] neg_lo:[1,0,0] neg_hi:[1,0,0]
	v_cvt_pk_bf16_f32 v47, v48, v49
	ds_write_b64 v186, v[46:47] offset:2176
	v_cmp_eq_u32_e32 vcc, v133, v199
	s_nop 1
	v_cndmask_b32_e64 v48, 0, 1.0, vcc
	v_cmp_eq_u32_e32 vcc, v135, v199
	s_nop 1
	v_cndmask_b32_e64 v49, 0, 1.0, vcc
	v_cmp_eq_u32_e32 vcc, v202, v199
	s_waitcnt vmcnt(18)
	v_pk_fma_f32 v[42:43], v[242:243], v[42:43], v[48:49] op_sel_hi:[0,1,1] neg_lo:[1,0,0] neg_hi:[1,0,0]
	v_cvt_pk_bf16_f32 v42, v42, v43
	v_cndmask_b32_e64 v49, 0, 1.0, vcc
	v_cmp_eq_u32_e32 vcc, v203, v199
	s_nop 1
	v_cndmask_b32_e64 v48, 0, 1.0, vcc
	v_pk_fma_f32 v[44:45], v[242:243], v[44:45], v[48:49] op_sel_hi:[0,1,1] neg_lo:[1,0,0] neg_hi:[1,0,0]
	v_cvt_pk_bf16_f32 v43, v44, v45
	ds_write_b64 v186, v[42:43] offset:2720
	v_cmp_eq_u32_e32 vcc, v133, v200
	s_nop 1
	v_cndmask_b32_e64 v44, 0, 1.0, vcc
	v_cmp_eq_u32_e32 vcc, v135, v200
	s_nop 1
	v_cndmask_b32_e64 v45, 0, 1.0, vcc
	v_cmp_eq_u32_e32 vcc, v202, v200
	s_waitcnt vmcnt(17)
	v_pk_fma_f32 v[38:39], v[244:245], v[38:39], v[44:45] op_sel_hi:[0,1,1] neg_lo:[1,0,0] neg_hi:[1,0,0]
	v_cvt_pk_bf16_f32 v38, v38, v39
	v_cndmask_b32_e64 v45, 0, 1.0, vcc
	v_cmp_eq_u32_e32 vcc, v203, v200
	s_nop 1
	v_cndmask_b32_e64 v44, 0, 1.0, vcc
	v_pk_fma_f32 v[40:41], v[244:245], v[40:41], v[44:45] op_sel_hi:[0,1,1] neg_lo:[1,0,0] neg_hi:[1,0,0]
	v_cvt_pk_bf16_f32 v39, v40, v41
	ds_write_b64 v186, v[38:39] offset:3264
	v_cmp_eq_u32_e32 vcc, v133, v201
	s_nop 1
	v_cndmask_b32_e64 v40, 0, 1.0, vcc
	v_cmp_eq_u32_e32 vcc, v135, v201
	s_nop 1
	v_cndmask_b32_e64 v41, 0, 1.0, vcc
	v_cmp_eq_u32_e32 vcc, v202, v201
	s_waitcnt vmcnt(16)
	v_pk_fma_f32 v[34:35], v[246:247], v[34:35], v[40:41] op_sel_hi:[0,1,1] neg_lo:[1,0,0] neg_hi:[1,0,0]
	v_cvt_pk_bf16_f32 v34, v34, v35
	v_cndmask_b32_e64 v41, 0, 1.0, vcc
	v_cmp_eq_u32_e32 vcc, v203, v201
	s_nop 1
	v_cndmask_b32_e64 v40, 0, 1.0, vcc
	v_pk_fma_f32 v[36:37], v[246:247], v[36:37], v[40:41] op_sel_hi:[0,1,1] neg_lo:[1,0,0] neg_hi:[1,0,0]
	v_cvt_pk_bf16_f32 v35, v36, v37
	ds_write_b64 v186, v[34:35] offset:3808
	ds_read_b32 v232, v187 offset:0
	ds_read_b32 v234, v187 offset:8
	ds_read_b32 v236, v187 offset:16
	ds_read_b32 v238, v187 offset:24
	ds_read_b32 v240, v187 offset:32
	ds_read_b32 v242, v187 offset:40
	ds_read_b32 v244, v187 offset:48
	ds_read_b32 v246, v187 offset:56
	ds_read_b128 v[34:37], v1
	ds_read_b128 v[38:41], v1 offset:64
	ds_read_b128 v[42:45], v1 offset:128
	ds_read_b128 v[46:49], v1 offset:192
	v_mov_b32_e32 v106, v189
	v_add_u32_e32 v107, 1, v106
	v_cmp_eq_u32_e32 vcc, v106, v132
	v_add_u32_e32 v108, 3, v106
	v_add_u32_e32 v109, 2, v106
	v_cndmask_b32_e64 v84, 0, 1.0, vcc
	v_cmp_eq_u32_e32 vcc, v107, v132
	s_nop 1
	v_cndmask_b32_e64 v85, 0, 1.0, vcc
	v_cmp_eq_u32_e32 vcc, v108, v132
	s_waitcnt lgkmcnt(0)
	s_waitcnt vmcnt(15)
	v_pk_fma_f32 v[94:95], v[232:233], v[118:119], v[84:85] op_sel_hi:[0,1,1] neg_lo:[1,0,0] neg_hi:[1,0,0]
	v_cvt_pk_bf16_f32 v94, v94, v95
	v_cndmask_b32_e64 v97, 0, 1.0, vcc
	v_cmp_eq_u32_e32 vcc, v109, v132
	s_nop 1
	v_cndmask_b32_e64 v96, 0, 1.0, vcc
	v_pk_fma_f32 v[82:83], v[232:233], v[120:121], v[96:97] op_sel_hi:[0,1,1] neg_lo:[1,0,0] neg_hi:[1,0,0]
	v_cvt_pk_bf16_f32 v95, v82, v83
	ds_write_b64 v186, v[94:95]
	v_cmp_eq_u32_e32 vcc, v106, v193
	s_nop 1
	v_cndmask_b32_e64 v94, 0, 1.0, vcc
	v_cmp_eq_u32_e32 vcc, v107, v193
	s_nop 1
	v_cndmask_b32_e64 v95, 0, 1.0, vcc
	v_cmp_eq_u32_e32 vcc, v108, v193
	s_waitcnt vmcnt(14)
	v_pk_fma_f32 v[94:95], v[234:235], v[110:111], v[94:95] op_sel_hi:[0,1,1] neg_lo:[1,0,0] neg_hi:[1,0,0]
	v_cvt_pk_bf16_f32 v94, v94, v95
	v_cndmask_b32_e64 v85, 0, 1.0, vcc
	v_pk_fma_f32 v[82:83], v[234:235], v[112:113], v[84:85] op_sel_hi:[0,1,1] neg_lo:[1,0,0] neg_hi:[1,0,0]
	v_cvt_pk_bf16_f32 v95, v82, v83
	ds_write_b64 v186, v[94:95] offset:544
	v_cmp_eq_u32_e32 vcc, v106, v192
	s_nop 1
	v_cndmask_b32_e64 v84, 0, 1.0, vcc
	v_cmp_eq_u32_e32 vcc, v107, v192
	s_nop 1
	v_cndmask_b32_e64 v85, 0, 1.0, vcc
	v_cmp_eq_u32_e32 vcc, v108, v192
	s_waitcnt vmcnt(13)
	v_pk_fma_f32 v[84:85], v[236:237], v[98:99], v[84:85] op_sel_hi:[0,1,1] neg_lo:[1,0,0] neg_hi:[1,0,0]
	v_cvt_pk_bf16_f32 v84, v84, v85
	v_cndmask_b32_e64 v95, 0, 1.0, vcc
	v_cmp_eq_u32_e32 vcc, v109, v192
	s_nop 1
	v_cndmask_b32_e64 v94, 0, 1.0, vcc
	v_pk_fma_f32 v[82:83], v[236:237], v[100:101], v[94:95] op_sel_hi:[0,1,1] neg_lo:[1,0,0] neg_hi:[1,0,0]
	v_cvt_pk_bf16_f32 v85, v82, v83
	ds_write_b64 v186, v[84:85] offset:1088
	v_cmp_eq_u32_e32 vcc, v106, v190
	s_nop 1
	v_cndmask_b32_e64 v84, 0, 1.0, vcc
	v_cmp_eq_u32_e32 vcc, v107, v190
	s_nop 1
	v_cndmask_b32_e64 v85, 0, 1.0, vcc
	v_cmp_eq_u32_e32 vcc, v108, v190
	s_waitcnt vmcnt(12)
	v_pk_fma_f32 v[84:85], v[238:239], v[86:87], v[84:85] op_sel_hi:[0,1,1] neg_lo:[1,0,0] neg_hi:[1,0,0]
	v_cvt_pk_bf16_f32 v84, v84, v85
	v_cndmask_b32_e64 v87, 0, 1.0, vcc
	v_cmp_eq_u32_e32 vcc, v109, v190
	s_nop 1
	v_cndmask_b32_e64 v86, 0, 1.0, vcc
	v_pk_fma_f32 v[82:83], v[238:239], v[88:89], v[86:87] op_sel_hi:[0,1,1] neg_lo:[1,0,0] neg_hi:[1,0,0]
	v_cvt_pk_bf16_f32 v85, v82, v83
	ds_write_b64 v186, v[84:85] offset:1632
	v_cmp_eq_u32_e32 vcc, v106, v149
	s_nop 1
	v_cndmask_b32_e64 v84, 0, 1.0, vcc
	v_cmp_eq_u32_e32 vcc, v107, v149
	s_nop 1
	v_cndmask_b32_e64 v85, 0, 1.0, vcc
	v_cmp_eq_u32_e32 vcc, v108, v149
	s_waitcnt vmcnt(11)
	v_pk_fma_f32 v[62:63], v[240:241], v[62:63], v[84:85] op_sel_hi:[0,1,1] neg_lo:[1,0,0] neg_hi:[1,0,0]
	v_cvt_pk_bf16_f32 v62, v62, v63
	v_cndmask_b32_e64 v85, 0, 1.0, vcc
	v_cmp_eq_u32_e32 vcc, v109, v149
	s_nop 1
	v_cndmask_b32_e64 v84, 0, 1.0, vcc
	v_pk_fma_f32 v[64:65], v[240:241], v[64:65], v[84:85] op_sel_hi:[0,1,1] neg_lo:[1,0,0] neg_hi:[1,0,0]
	v_cvt_pk_bf16_f32 v63, v64, v65
	ds_write_b64 v186, v[62:63] offset:2176
	v_cmp_eq_u32_e32 vcc, v106, v148
	s_nop 1
	v_cndmask_b32_e64 v64, 0, 1.0, vcc
	v_cmp_eq_u32_e32 vcc, v107, v148
	s_nop 1
	v_cndmask_b32_e64 v65, 0, 1.0, vcc
	v_cmp_eq_u32_e32 vcc, v108, v148
	s_waitcnt vmcnt(10)
	v_pk_fma_f32 v[58:59], v[242:243], v[58:59], v[64:65] op_sel_hi:[0,1,1] neg_lo:[1,0,0] neg_hi:[1,0,0]
	v_cvt_pk_bf16_f32 v58, v58, v59
	v_cndmask_b32_e64 v65, 0, 1.0, vcc
	v_cmp_eq_u32_e32 vcc, v109, v148
	s_nop 1
	v_cndmask_b32_e64 v64, 0, 1.0, vcc
	v_pk_fma_f32 v[60:61], v[242:243], v[60:61], v[64:65] op_sel_hi:[0,1,1] neg_lo:[1,0,0] neg_hi:[1,0,0]
	v_cvt_pk_bf16_f32 v59, v60, v61
	ds_write_b64 v186, v[58:59] offset:2720
	v_cmp_eq_u32_e32 vcc, v106, v147
	s_nop 1
	v_cndmask_b32_e64 v60, 0, 1.0, vcc
	v_cmp_eq_u32_e32 vcc, v107, v147
	s_nop 1
	v_cndmask_b32_e64 v61, 0, 1.0, vcc
	v_cmp_eq_u32_e32 vcc, v108, v147
	s_waitcnt vmcnt(9)
	v_pk_fma_f32 v[54:55], v[244:245], v[54:55], v[60:61] op_sel_hi:[0,1,1] neg_lo:[1,0,0] neg_hi:[1,0,0]
	v_cvt_pk_bf16_f32 v54, v54, v55
	v_cndmask_b32_e64 v61, 0, 1.0, vcc
	v_cmp_eq_u32_e32 vcc, v109, v147
	s_nop 1
	v_cndmask_b32_e64 v60, 0, 1.0, vcc
	v_pk_fma_f32 v[56:57], v[244:245], v[56:57], v[60:61] op_sel_hi:[0,1,1] neg_lo:[1,0,0] neg_hi:[1,0,0]
	v_cvt_pk_bf16_f32 v55, v56, v57
	ds_write_b64 v186, v[54:55] offset:3264
	v_cmp_eq_u32_e32 vcc, v106, v146
	s_nop 1
	v_cndmask_b32_e64 v56, 0, 1.0, vcc
	v_cmp_eq_u32_e32 vcc, v107, v146
	s_nop 1
	v_cndmask_b32_e64 v57, 0, 1.0, vcc
	v_cmp_eq_u32_e32 vcc, v108, v146
	s_waitcnt vmcnt(8)
	v_pk_fma_f32 v[50:51], v[246:247], v[50:51], v[56:57] op_sel_hi:[0,1,1] neg_lo:[1,0,0] neg_hi:[1,0,0]
	v_cvt_pk_bf16_f32 v50, v50, v51
	v_cndmask_b32_e64 v57, 0, 1.0, vcc
	v_cmp_eq_u32_e32 vcc, v109, v146
	s_nop 1
	v_cndmask_b32_e64 v56, 0, 1.0, vcc
	v_pk_fma_f32 v[52:53], v[246:247], v[52:53], v[56:57] op_sel_hi:[0,1,1] neg_lo:[1,0,0] neg_hi:[1,0,0]
	v_cvt_pk_bf16_f32 v51, v52, v53
	ds_write_b64 v186, v[50:51] offset:3808
	ds_read_b32 v232, v187 offset:64
	ds_read_b32 v234, v187 offset:72
	ds_read_b32 v236, v187 offset:80
	ds_read_b32 v238, v187 offset:88
	ds_read_b32 v240, v187 offset:96
	ds_read_b32 v242, v187 offset:104
	ds_read_b32 v244, v187 offset:112
	ds_read_b32 v246, v187 offset:120
	ds_read_b128 v[50:53], v1
	ds_read_b128 v[54:57], v1 offset:64
	ds_read_b128 v[58:61], v1 offset:128
	ds_read_b128 v[62:65], v1 offset:192
	v_lshl_add_u64 v[82:83], v[168:169], 0, s[8:9]
	v_lshl_add_u64 v[84:85], v[170:171], 0, s[8:9]
	v_lshl_add_u64 v[86:87], v[172:173], 0, s[8:9]
	v_lshl_add_u64 v[88:89], v[174:175], 0, s[8:9]
	v_lshl_add_u64 v[94:95], v[176:177], 0, s[8:9]
	v_lshl_add_u64 v[96:97], v[178:179], 0, s[8:9]
	v_lshl_add_u64 v[122:123], v[180:181], 0, s[8:9]
	v_lshl_add_u64 v[124:125], v[182:183], 0, s[8:9]
	global_load_dwordx4 v[134:137], v[82:83], off nt
	global_load_dwordx4 v[118:121], v[84:85], off nt
	global_load_dwordx4 v[110:113], v[86:87], off nt
	global_load_dwordx4 v[106:109], v[88:89], off nt
	global_load_dwordx4 v[98:101], v[94:95], off nt
	s_nop 0
	global_load_dwordx4 v[94:97], v[96:97], off nt
	s_nop 0
	global_load_dwordx4 v[86:89], v[122:123], off nt
	global_load_dwordx4 v[82:85], v[124:125], off nt
	v_mov_b32_e32 v132, v189
	v_add_u32_e32 v133, 1, v132
	v_cmp_eq_u32_e32 vcc, v132, v138
	v_add_u32_e32 v146, 3, v132
	v_add_u32_e32 v147, 2, v132
	v_cndmask_b32_e64 v124, 0, 1.0, vcc
	v_cmp_eq_u32_e32 vcc, v133, v138
	s_nop 1
	v_cndmask_b32_e64 v125, 0, 1.0, vcc
	v_cmp_eq_u32_e32 vcc, v146, v138
	s_waitcnt lgkmcnt(0)
	s_waitcnt vmcnt(15)
	v_pk_fma_f32 v[124:125], v[232:233], v[126:127], v[124:125] op_sel_hi:[0,1,1] neg_lo:[1,0,0] neg_hi:[1,0,0]
	v_cvt_pk_bf16_f32 v124, v124, v125
	v_cndmask_b32_e64 v127, 0, 1.0, vcc
	v_cmp_eq_u32_e32 vcc, v147, v138
	s_nop 1
	v_cndmask_b32_e64 v126, 0, 1.0, vcc
	v_pk_fma_f32 v[122:123], v[232:233], v[128:129], v[126:127] op_sel_hi:[0,1,1] neg_lo:[1,0,0] neg_hi:[1,0,0]
	v_cvt_pk_bf16_f32 v125, v122, v123
	ds_write_b64 v186, v[124:125]
	v_cmp_eq_u32_e32 vcc, v132, v139
	s_nop 1
	v_cndmask_b32_e64 v124, 0, 1.0, vcc
	v_cmp_eq_u32_e32 vcc, v133, v139
	s_nop 1
	v_cndmask_b32_e64 v125, 0, 1.0, vcc
	v_cmp_eq_u32_e32 vcc, v146, v139
	s_waitcnt vmcnt(14)
	v_pk_fma_f32 v[114:115], v[234:235], v[114:115], v[124:125] op_sel_hi:[0,1,1] neg_lo:[1,0,0] neg_hi:[1,0,0]
	v_cvt_pk_bf16_f32 v114, v114, v115
	v_cndmask_b32_e64 v125, 0, 1.0, vcc
	v_cmp_eq_u32_e32 vcc, v147, v139
	s_nop 1
	v_cndmask_b32_e64 v124, 0, 1.0, vcc
	v_pk_fma_f32 v[116:117], v[234:235], v[116:117], v[124:125] op_sel_hi:[0,1,1] neg_lo:[1,0,0] neg_hi:[1,0,0]
	v_cvt_pk_bf16_f32 v115, v116, v117
	ds_write_b64 v186, v[114:115] offset:544
	v_cmp_eq_u32_e32 vcc, v132, v140
	s_nop 1
	v_cndmask_b32_e64 v116, 0, 1.0, vcc
	v_cmp_eq_u32_e32 vcc, v133, v140
	s_nop 1
	v_cndmask_b32_e64 v117, 0, 1.0, vcc
	v_cmp_eq_u32_e32 vcc, v146, v140
	s_waitcnt vmcnt(13)
	v_pk_fma_f32 v[102:103], v[236:237], v[102:103], v[116:117] op_sel_hi:[0,1,1] neg_lo:[1,0,0] neg_hi:[1,0,0]
	v_cvt_pk_bf16_f32 v102, v102, v103
	v_cndmask_b32_e64 v117, 0, 1.0, vcc
	v_cmp_eq_u32_e32 vcc, v147, v140
	s_nop 1
	v_cndmask_b32_e64 v116, 0, 1.0, vcc
	v_pk_fma_f32 v[104:105], v[236:237], v[104:105], v[116:117] op_sel_hi:[0,1,1] neg_lo:[1,0,0] neg_hi:[1,0,0]
	v_cvt_pk_bf16_f32 v103, v104, v105
	ds_write_b64 v186, v[102:103] offset:1088
	v_cmp_eq_u32_e32 vcc, v132, v141
	s_nop 1
	v_cndmask_b32_e64 v104, 0, 1.0, vcc
	v_cmp_eq_u32_e32 vcc, v133, v141
	s_nop 1
	v_cndmask_b32_e64 v105, 0, 1.0, vcc
	v_cmp_eq_u32_e32 vcc, v146, v141
	s_waitcnt vmcnt(12)
	v_pk_fma_f32 v[90:91], v[238:239], v[90:91], v[104:105] op_sel_hi:[0,1,1] neg_lo:[1,0,0] neg_hi:[1,0,0]
	v_cvt_pk_bf16_f32 v90, v90, v91
	v_cndmask_b32_e64 v105, 0, 1.0, vcc
	v_cmp_eq_u32_e32 vcc, v147, v141
	s_nop 1
	v_cndmask_b32_e64 v104, 0, 1.0, vcc
	v_pk_fma_f32 v[92:93], v[238:239], v[92:93], v[104:105] op_sel_hi:[0,1,1] neg_lo:[1,0,0] neg_hi:[1,0,0]
	v_cvt_pk_bf16_f32 v91, v92, v93
	ds_write_b64 v186, v[90:91] offset:1632
	v_cmp_eq_u32_e32 vcc, v132, v142
	s_nop 1
	v_cndmask_b32_e64 v92, 0, 1.0, vcc
	v_cmp_eq_u32_e32 vcc, v133, v142
	s_nop 1
	v_cndmask_b32_e64 v93, 0, 1.0, vcc
	v_cmp_eq_u32_e32 vcc, v146, v142
	s_waitcnt vmcnt(11)
	v_pk_fma_f32 v[78:79], v[240:241], v[78:79], v[92:93] op_sel_hi:[0,1,1] neg_lo:[1,0,0] neg_hi:[1,0,0]
	v_cvt_pk_bf16_f32 v78, v78, v79
	v_cndmask_b32_e64 v93, 0, 1.0, vcc
	v_cmp_eq_u32_e32 vcc, v147, v142
	s_nop 1
	v_cndmask_b32_e64 v92, 0, 1.0, vcc
	v_pk_fma_f32 v[80:81], v[240:241], v[80:81], v[92:93] op_sel_hi:[0,1,1] neg_lo:[1,0,0] neg_hi:[1,0,0]
	v_cvt_pk_bf16_f32 v79, v80, v81
	ds_write_b64 v186, v[78:79] offset:2176
	v_cmp_eq_u32_e32 vcc, v132, v143
	s_nop 1
	v_cndmask_b32_e64 v80, 0, 1.0, vcc
	v_cmp_eq_u32_e32 vcc, v133, v143
	s_nop 1
	v_cndmask_b32_e64 v81, 0, 1.0, vcc
	v_cmp_eq_u32_e32 vcc, v146, v143
	s_waitcnt vmcnt(10)
	v_pk_fma_f32 v[74:75], v[242:243], v[74:75], v[80:81] op_sel_hi:[0,1,1] neg_lo:[1,0,0] neg_hi:[1,0,0]
	v_cvt_pk_bf16_f32 v74, v74, v75
	v_cndmask_b32_e64 v81, 0, 1.0, vcc
	v_cmp_eq_u32_e32 vcc, v147, v143
	s_nop 1
	v_cndmask_b32_e64 v80, 0, 1.0, vcc
	v_pk_fma_f32 v[76:77], v[242:243], v[76:77], v[80:81] op_sel_hi:[0,1,1] neg_lo:[1,0,0] neg_hi:[1,0,0]
	v_cvt_pk_bf16_f32 v75, v76, v77
	ds_write_b64 v186, v[74:75] offset:2720
	v_cmp_eq_u32_e32 vcc, v132, v144
	s_nop 1
	v_cndmask_b32_e64 v76, 0, 1.0, vcc
	v_cmp_eq_u32_e32 vcc, v133, v144
	s_nop 1
	v_cndmask_b32_e64 v77, 0, 1.0, vcc
	v_cmp_eq_u32_e32 vcc, v146, v144
	s_waitcnt vmcnt(9)
	v_pk_fma_f32 v[70:71], v[244:245], v[70:71], v[76:77] op_sel_hi:[0,1,1] neg_lo:[1,0,0] neg_hi:[1,0,0]
	v_cvt_pk_bf16_f32 v70, v70, v71
	v_cndmask_b32_e64 v77, 0, 1.0, vcc
	v_cmp_eq_u32_e32 vcc, v147, v144
	s_nop 1
	v_cndmask_b32_e64 v76, 0, 1.0, vcc
	v_pk_fma_f32 v[72:73], v[244:245], v[72:73], v[76:77] op_sel_hi:[0,1,1] neg_lo:[1,0,0] neg_hi:[1,0,0]
	v_cvt_pk_bf16_f32 v71, v72, v73
	ds_write_b64 v186, v[70:71] offset:3264
	v_cmp_eq_u32_e32 vcc, v132, v145
	s_nop 1
	v_cndmask_b32_e64 v72, 0, 1.0, vcc
	v_cmp_eq_u32_e32 vcc, v133, v145
	s_nop 1
	v_cndmask_b32_e64 v73, 0, 1.0, vcc
	v_cmp_eq_u32_e32 vcc, v146, v145
	s_waitcnt vmcnt(8)
	v_pk_fma_f32 v[66:67], v[246:247], v[66:67], v[72:73] op_sel_hi:[0,1,1] neg_lo:[1,0,0] neg_hi:[1,0,0]
	v_cvt_pk_bf16_f32 v66, v66, v67
	v_cndmask_b32_e64 v73, 0, 1.0, vcc
	v_cmp_eq_u32_e32 vcc, v147, v145
	s_nop 1
	v_cndmask_b32_e64 v72, 0, 1.0, vcc
	v_pk_fma_f32 v[68:69], v[246:247], v[68:69], v[72:73] op_sel_hi:[0,1,1] neg_lo:[1,0,0] neg_hi:[1,0,0]
	v_cvt_pk_bf16_f32 v67, v68, v69
	ds_write_b64 v186, v[66:67] offset:3808
	ds_read_b32 v232, v187 offset:128
	ds_read_b32 v234, v187 offset:136
	ds_read_b32 v236, v187 offset:144
	ds_read_b32 v238, v187 offset:152
	ds_read_b32 v240, v187 offset:160
	ds_read_b32 v242, v187 offset:168
	ds_read_b32 v244, v187 offset:176
	ds_read_b32 v246, v187 offset:184
	ds_read_b128 v[66:69], v1
	ds_read_b128 v[70:73], v1 offset:64
	ds_read_b128 v[74:77], v1 offset:128
	ds_read_b128 v[78:81], v1 offset:192
	v_lshl_add_u64 v[90:91], v[130:131], 0, s[0:1]
	v_add_co_u32_e32 v92, vcc, s7, v90
	s_nop 1
	v_addc_co_u32_e32 v93, vcc, 0, v91, vcc
	global_load_dwordx4 v[146:149], v[90:91], off nt
	global_load_dwordx4 v[142:145], v[92:93], off nt
	v_add_co_u32_e32 v92, vcc, s36, v90
	s_nop 1
	v_addc_co_u32_e32 v93, vcc, 0, v91, vcc
	v_add_co_u32_e32 v102, vcc, s37, v90
	s_nop 1
	v_addc_co_u32_e32 v103, vcc, 0, v91, vcc
	global_load_dwordx4 v[138:141], v[92:93], off nt
	global_load_dwordx4 v[130:133], v[102:103], off nt
	v_add_co_u32_e32 v92, vcc, s38, v90
	s_nop 1
	v_addc_co_u32_e32 v93, vcc, 0, v91, vcc
	v_add_co_u32_e32 v102, vcc, s39, v90
	s_nop 1
	v_addc_co_u32_e32 v103, vcc, 0, v91, vcc
	global_load_dwordx4 v[126:129], v[92:93], off nt
	global_load_dwordx4 v[122:125], v[102:103], off nt
	v_add_co_u32_e32 v92, vcc, s41, v90
	s_nop 1
	v_addc_co_u32_e32 v93, vcc, 0, v91, vcc
	v_add_co_u32_e32 v90, vcc, s42, v90
	s_nop 1
	v_addc_co_u32_e32 v91, vcc, 0, v91, vcc
	global_load_dwordx4 v[114:117], v[92:93], off nt
	global_load_dwordx4 v[102:105], v[90:91], off nt
	v_add_u32_e32 v190, 1, v189
	v_cmp_eq_u32_e32 vcc, v189, v194
	v_add_u32_e32 v192, 3, v189
	v_add_u32_e32 v193, 2, v189
	v_cndmask_b32_e64 v92, 0, 1.0, vcc
	v_cmp_eq_u32_e32 vcc, v190, v194
	s_nop 1
	v_cndmask_b32_e64 v93, 0, 1.0, vcc
	v_cmp_eq_u32_e32 vcc, v192, v194
	s_waitcnt lgkmcnt(0)
	s_waitcnt vmcnt(15)
	v_pk_fma_f32 v[92:93], v[232:233], v[134:135], v[92:93] op_sel_hi:[0,1,1] neg_lo:[1,0,0] neg_hi:[1,0,0]
	v_cvt_pk_bf16_f32 v92, v92, v93
	v_cndmask_b32_e64 v135, 0, 1.0, vcc
	v_cmp_eq_u32_e32 vcc, v193, v194
	s_nop 1
	v_cndmask_b32_e64 v134, 0, 1.0, vcc
	v_pk_fma_f32 v[90:91], v[232:233], v[136:137], v[134:135] op_sel_hi:[0,1,1] neg_lo:[1,0,0] neg_hi:[1,0,0]
	v_cvt_pk_bf16_f32 v93, v90, v91
	ds_write_b64 v186, v[92:93]
	v_cmp_eq_u32_e32 vcc, v189, v195
	s_nop 1
	v_cndmask_b32_e64 v92, 0, 1.0, vcc
	v_cmp_eq_u32_e32 vcc, v190, v195
	s_nop 1
	v_cndmask_b32_e64 v93, 0, 1.0, vcc
	v_cmp_eq_u32_e32 vcc, v192, v195
	s_waitcnt vmcnt(14)
	v_pk_fma_f32 v[92:93], v[234:235], v[118:119], v[92:93] op_sel_hi:[0,1,1] neg_lo:[1,0,0] neg_hi:[1,0,0]
	v_cvt_pk_bf16_f32 v92, v92, v93
	v_cndmask_b32_e64 v119, 0, 1.0, vcc
	v_cmp_eq_u32_e32 vcc, v193, v195
	s_nop 1
	v_cndmask_b32_e64 v118, 0, 1.0, vcc
	v_pk_fma_f32 v[90:91], v[234:235], v[120:121], v[118:119] op_sel_hi:[0,1,1] neg_lo:[1,0,0] neg_hi:[1,0,0]
	v_cvt_pk_bf16_f32 v93, v90, v91
	ds_write_b64 v186, v[92:93] offset:544
	v_cmp_eq_u32_e32 vcc, v189, v196
	s_nop 1
	v_cndmask_b32_e64 v92, 0, 1.0, vcc
	v_cmp_eq_u32_e32 vcc, v190, v196
	s_nop 1
	v_cndmask_b32_e64 v93, 0, 1.0, vcc
	v_cmp_eq_u32_e32 vcc, v192, v196
	s_waitcnt vmcnt(13)
	v_pk_fma_f32 v[92:93], v[236:237], v[110:111], v[92:93] op_sel_hi:[0,1,1] neg_lo:[1,0,0] neg_hi:[1,0,0]
	v_cvt_pk_bf16_f32 v92, v92, v93
	v_cndmask_b32_e64 v111, 0, 1.0, vcc
	v_cmp_eq_u32_e32 vcc, v193, v196
	s_nop 1
	v_cndmask_b32_e64 v110, 0, 1.0, vcc
	v_pk_fma_f32 v[90:91], v[236:237], v[112:113], v[110:111] op_sel_hi:[0,1,1] neg_lo:[1,0,0] neg_hi:[1,0,0]
	v_cvt_pk_bf16_f32 v93, v90, v91
	ds_write_b64 v186, v[92:93] offset:1088
	v_cmp_eq_u32_e32 vcc, v189, v197
	s_nop 1
	v_cndmask_b32_e64 v92, 0, 1.0, vcc
	v_cmp_eq_u32_e32 vcc, v190, v197
	s_nop 1
	v_cndmask_b32_e64 v93, 0, 1.0, vcc
	v_cmp_eq_u32_e32 vcc, v192, v197
	s_waitcnt vmcnt(12)
	v_pk_fma_f32 v[92:93], v[238:239], v[106:107], v[92:93] op_sel_hi:[0,1,1] neg_lo:[1,0,0] neg_hi:[1,0,0]
	v_cvt_pk_bf16_f32 v92, v92, v93
	v_cndmask_b32_e64 v107, 0, 1.0, vcc
	v_cmp_eq_u32_e32 vcc, v193, v197
	s_nop 1
	v_cndmask_b32_e64 v106, 0, 1.0, vcc
	v_pk_fma_f32 v[90:91], v[238:239], v[108:109], v[106:107] op_sel_hi:[0,1,1] neg_lo:[1,0,0] neg_hi:[1,0,0]
	v_cvt_pk_bf16_f32 v93, v90, v91
	ds_write_b64 v186, v[92:93] offset:1632
	v_cmp_eq_u32_e32 vcc, v189, v198
	s_nop 1
	v_cndmask_b32_e64 v92, 0, 1.0, vcc
	v_cmp_eq_u32_e32 vcc, v190, v198
	s_nop 1
	v_cndmask_b32_e64 v93, 0, 1.0, vcc
	v_cmp_eq_u32_e32 vcc, v192, v198
	s_waitcnt vmcnt(11)
	v_pk_fma_f32 v[92:93], v[240:241], v[98:99], v[92:93] op_sel_hi:[0,1,1] neg_lo:[1,0,0] neg_hi:[1,0,0]
	v_cvt_pk_bf16_f32 v92, v92, v93
	v_cndmask_b32_e64 v99, 0, 1.0, vcc
	v_cmp_eq_u32_e32 vcc, v193, v198
	s_nop 1
	v_cndmask_b32_e64 v98, 0, 1.0, vcc
	v_pk_fma_f32 v[90:91], v[240:241], v[100:101], v[98:99] op_sel_hi:[0,1,1] neg_lo:[1,0,0] neg_hi:[1,0,0]
	v_cvt_pk_bf16_f32 v93, v90, v91
	ds_write_b64 v186, v[92:93] offset:2176
	v_cmp_eq_u32_e32 vcc, v189, v199
	s_nop 1
	v_cndmask_b32_e64 v92, 0, 1.0, vcc
	v_cmp_eq_u32_e32 vcc, v190, v199
	s_nop 1
	v_cndmask_b32_e64 v93, 0, 1.0, vcc
	v_cmp_eq_u32_e32 vcc, v192, v199
	s_waitcnt vmcnt(10)
	v_pk_fma_f32 v[92:93], v[242:243], v[94:95], v[92:93] op_sel_hi:[0,1,1] neg_lo:[1,0,0] neg_hi:[1,0,0]
	v_cvt_pk_bf16_f32 v92, v92, v93
	v_cndmask_b32_e64 v95, 0, 1.0, vcc
	v_cmp_eq_u32_e32 vcc, v193, v199
	s_nop 1
	v_cndmask_b32_e64 v94, 0, 1.0, vcc
	v_pk_fma_f32 v[90:91], v[242:243], v[96:97], v[94:95] op_sel_hi:[0,1,1] neg_lo:[1,0,0] neg_hi:[1,0,0]
	v_cvt_pk_bf16_f32 v93, v90, v91
	ds_write_b64 v186, v[92:93] offset:2720
	v_cmp_eq_u32_e32 vcc, v189, v200
	s_nop 1
	v_cndmask_b32_e64 v92, 0, 1.0, vcc
	v_cmp_eq_u32_e32 vcc, v190, v200
	s_nop 1
	v_cndmask_b32_e64 v93, 0, 1.0, vcc
	v_cmp_eq_u32_e32 vcc, v192, v200
	s_waitcnt vmcnt(9)
	v_pk_fma_f32 v[86:87], v[244:245], v[86:87], v[92:93] op_sel_hi:[0,1,1] neg_lo:[1,0,0] neg_hi:[1,0,0]
	v_cvt_pk_bf16_f32 v86, v86, v87
	v_cndmask_b32_e64 v93, 0, 1.0, vcc
	v_cmp_eq_u32_e32 vcc, v193, v200
	s_nop 1
	v_cndmask_b32_e64 v92, 0, 1.0, vcc
	v_pk_fma_f32 v[88:89], v[244:245], v[88:89], v[92:93] op_sel_hi:[0,1,1] neg_lo:[1,0,0] neg_hi:[1,0,0]
	v_cvt_pk_bf16_f32 v87, v88, v89
	ds_write_b64 v186, v[86:87] offset:3264
	v_cmp_eq_u32_e32 vcc, v189, v201
	s_nop 1
	v_cndmask_b32_e64 v88, 0, 1.0, vcc
	v_cmp_eq_u32_e32 vcc, v190, v201
	s_nop 1
	v_cndmask_b32_e64 v89, 0, 1.0, vcc
	v_cmp_eq_u32_e32 vcc, v192, v201
	s_waitcnt vmcnt(8)
	v_pk_fma_f32 v[82:83], v[246:247], v[82:83], v[88:89] op_sel_hi:[0,1,1] neg_lo:[1,0,0] neg_hi:[1,0,0]
	v_cvt_pk_bf16_f32 v82, v82, v83
	v_cndmask_b32_e64 v89, 0, 1.0, vcc
	v_cmp_eq_u32_e32 vcc, v193, v201
	s_nop 1
	v_cndmask_b32_e64 v88, 0, 1.0, vcc
	v_pk_fma_f32 v[84:85], v[246:247], v[84:85], v[88:89] op_sel_hi:[0,1,1] neg_lo:[1,0,0] neg_hi:[1,0,0]
	v_cvt_pk_bf16_f32 v83, v84, v85
	ds_write_b64 v186, v[82:83] offset:3808
	ds_read_b32 v232, v187 offset:0
	ds_read_b32 v234, v187 offset:8
	ds_read_b32 v236, v187 offset:16
	ds_read_b32 v238, v187 offset:24
	ds_read_b32 v240, v187 offset:32
	ds_read_b32 v242, v187 offset:40
	ds_read_b32 v244, v187 offset:48
	ds_read_b32 v246, v187 offset:56
	ds_read_b128 v[82:85], v1
	ds_read_b128 v[86:89], v1 offset:64
	ds_read_b128 v[90:93], v1 offset:128
	ds_read_b128 v[94:97], v1 offset:192
	v_lshl_add_u64 v[98:99], v[150:151], 0, s[0:1]
	v_lshl_add_u64 v[192:193], v[164:165], 0, s[0:1]
	v_lshl_add_u64 v[196:197], v[166:167], 0, s[0:1]
	v_lshl_add_u64 v[100:101], v[152:153], 0, s[0:1]
	v_lshl_add_u64 v[106:107], v[156:157], 0, s[0:1]
	v_lshl_add_u64 v[108:109], v[158:159], 0, s[0:1]
	v_lshl_add_u64 v[110:111], v[160:161], 0, s[0:1]
	v_lshl_add_u64 v[112:113], v[162:163], 0, s[0:1]
	global_load_dwordx4 v[118:121], v[98:99], off nt
	global_load_dwordx4 v[134:137], v[100:101], off nt
	global_load_dwordx4 v[150:153], v[106:107], off nt
	global_load_dwordx4 v[156:159], v[108:109], off nt
	global_load_dwordx4 v[160:163], v[110:111], off nt
	global_load_dwordx4 v[164:167], v[112:113], off nt
	s_nop 0
	global_load_dwordx4 v[192:195], v[192:193], off nt
	s_nop 0
	global_load_dwordx4 v[196:199], v[196:197], off nt
	v_mov_b32_e32 v98, v188
	s_waitcnt lgkmcnt(0)
	s_waitcnt vmcnt(15)
	v_pk_fma_f32 v[100:101], v[232:233], v[146:147], 0 op_sel_hi:[0,1,0] neg_lo:[1,0,0] neg_hi:[1,0,0]
	v_pk_fma_f32 v[98:99], v[232:233], v[148:149], 0 op_sel_hi:[0,1,0] neg_lo:[1,0,0] neg_hi:[1,0,0]
	v_cvt_pk_bf16_f32 v100, v100, v101
	v_cvt_pk_bf16_f32 v101, v98, v99
	ds_write_b64 v186, v[100:101]
	s_waitcnt vmcnt(14)
	v_pk_fma_f32 v[100:101], v[234:235], v[142:143], 0 op_sel_hi:[0,1,0] neg_lo:[1,0,0] neg_hi:[1,0,0]
	v_pk_fma_f32 v[98:99], v[234:235], v[144:145], 0 op_sel_hi:[0,1,0] neg_lo:[1,0,0] neg_hi:[1,0,0]
	v_cvt_pk_bf16_f32 v100, v100, v101
	v_cvt_pk_bf16_f32 v101, v98, v99
	ds_write_b64 v186, v[100:101] offset:544
	s_waitcnt vmcnt(13)
	v_pk_fma_f32 v[100:101], v[236:237], v[138:139], 0 op_sel_hi:[0,1,0] neg_lo:[1,0,0] neg_hi:[1,0,0]
	v_pk_fma_f32 v[98:99], v[236:237], v[140:141], 0 op_sel_hi:[0,1,0] neg_lo:[1,0,0] neg_hi:[1,0,0]
	v_cvt_pk_bf16_f32 v100, v100, v101
	v_cvt_pk_bf16_f32 v101, v98, v99
	ds_write_b64 v186, v[100:101] offset:1088
	s_waitcnt vmcnt(12)
	v_pk_fma_f32 v[100:101], v[238:239], v[130:131], 0 op_sel_hi:[0,1,0] neg_lo:[1,0,0] neg_hi:[1,0,0]
	v_pk_fma_f32 v[98:99], v[238:239], v[132:133], 0 op_sel_hi:[0,1,0] neg_lo:[1,0,0] neg_hi:[1,0,0]
	v_cvt_pk_bf16_f32 v100, v100, v101
	v_cvt_pk_bf16_f32 v101, v98, v99
	ds_write_b64 v186, v[100:101] offset:1632
	s_waitcnt vmcnt(11)
	v_pk_fma_f32 v[100:101], v[240:241], v[126:127], 0 op_sel_hi:[0,1,0] neg_lo:[1,0,0] neg_hi:[1,0,0]
	v_pk_fma_f32 v[98:99], v[240:241], v[128:129], 0 op_sel_hi:[0,1,0] neg_lo:[1,0,0] neg_hi:[1,0,0]
	v_cvt_pk_bf16_f32 v100, v100, v101
	v_cvt_pk_bf16_f32 v101, v98, v99
	ds_write_b64 v186, v[100:101] offset:2176
	s_waitcnt vmcnt(10)
	v_pk_fma_f32 v[100:101], v[242:243], v[122:123], 0 op_sel_hi:[0,1,0] neg_lo:[1,0,0] neg_hi:[1,0,0]
	v_pk_fma_f32 v[98:99], v[242:243], v[124:125], 0 op_sel_hi:[0,1,0] neg_lo:[1,0,0] neg_hi:[1,0,0]
	v_cvt_pk_bf16_f32 v100, v100, v101
	v_cvt_pk_bf16_f32 v101, v98, v99
	ds_write_b64 v186, v[100:101] offset:2720
	s_waitcnt vmcnt(9)
	v_pk_fma_f32 v[100:101], v[244:245], v[114:115], 0 op_sel_hi:[0,1,0] neg_lo:[1,0,0] neg_hi:[1,0,0]
	v_pk_fma_f32 v[98:99], v[244:245], v[116:117], 0 op_sel_hi:[0,1,0] neg_lo:[1,0,0] neg_hi:[1,0,0]
	v_cvt_pk_bf16_f32 v100, v100, v101
	v_cvt_pk_bf16_f32 v101, v98, v99
	ds_write_b64 v186, v[100:101] offset:3264
	s_waitcnt vmcnt(8)
	v_pk_fma_f32 v[100:101], v[246:247], v[102:103], 0 op_sel_hi:[0,1,0] neg_lo:[1,0,0] neg_hi:[1,0,0]
	v_pk_fma_f32 v[98:99], v[246:247], v[104:105], 0 op_sel_hi:[0,1,0] neg_lo:[1,0,0] neg_hi:[1,0,0]
	v_cvt_pk_bf16_f32 v100, v100, v101
	v_cvt_pk_bf16_f32 v101, v98, v99
	ds_write_b64 v186, v[100:101] offset:3808
	ds_read_b32 v232, v187 offset:64
	ds_read_b32 v234, v187 offset:72
	ds_read_b32 v236, v187 offset:80
	ds_read_b32 v238, v187 offset:88
	ds_read_b32 v240, v187 offset:96
	ds_read_b32 v242, v187 offset:104
	ds_read_b32 v244, v187 offset:112
	ds_read_b32 v246, v187 offset:120
	ds_read_b128 v[98:101], v1
	ds_read_b128 v[102:105], v1 offset:64
	ds_read_b128 v[106:109], v1 offset:128
	ds_read_b128 v[110:113], v1 offset:192
	v_lshl_add_u64 v[114:115], v[168:169], 0, s[0:1]
	v_lshl_add_u64 v[126:127], v[176:177], 0, s[0:1]
	v_lshl_add_u64 v[176:177], v[180:181], 0, s[0:1]
	v_lshl_add_u64 v[180:181], v[182:183], 0, s[0:1]
	v_lshl_add_u64 v[116:117], v[170:171], 0, s[0:1]
	v_lshl_add_u64 v[122:123], v[172:173], 0, s[0:1]
	v_lshl_add_u64 v[124:125], v[174:175], 0, s[0:1]
	v_lshl_add_u64 v[128:129], v[178:179], 0, s[0:1]
	global_load_dwordx4 v[130:133], v[114:115], off nt
	global_load_dwordx4 v[138:141], v[116:117], off nt
	global_load_dwordx4 v[142:145], v[122:123], off nt
	global_load_dwordx4 v[146:149], v[124:125], off nt
	global_load_dwordx4 v[168:171], v[126:127], off nt
	global_load_dwordx4 v[172:175], v[128:129], off nt
	s_nop 0
	global_load_dwordx4 v[176:179], v[176:177], off nt
	s_nop 0
	global_load_dwordx4 v[180:183], v[180:181], off nt
	v_mov_b32_e32 v114, v188
	s_waitcnt lgkmcnt(0)
	s_waitcnt vmcnt(15)
	v_pk_fma_f32 v[116:117], v[232:233], v[118:119], 0 op_sel_hi:[0,1,0] neg_lo:[1,0,0] neg_hi:[1,0,0]
	v_pk_fma_f32 v[114:115], v[232:233], v[120:121], 0 op_sel_hi:[0,1,0] neg_lo:[1,0,0] neg_hi:[1,0,0]
	v_cvt_pk_bf16_f32 v116, v116, v117
	v_cvt_pk_bf16_f32 v117, v114, v115
	ds_write_b64 v186, v[116:117]
	s_waitcnt vmcnt(14)
	v_pk_fma_f32 v[116:117], v[234:235], v[134:135], 0 op_sel_hi:[0,1,0] neg_lo:[1,0,0] neg_hi:[1,0,0]
	v_pk_fma_f32 v[114:115], v[234:235], v[136:137], 0 op_sel_hi:[0,1,0] neg_lo:[1,0,0] neg_hi:[1,0,0]
	v_cvt_pk_bf16_f32 v116, v116, v117
	v_cvt_pk_bf16_f32 v117, v114, v115
	ds_write_b64 v186, v[116:117] offset:544
	s_waitcnt vmcnt(13)
	v_pk_fma_f32 v[116:117], v[236:237], v[150:151], 0 op_sel_hi:[0,1,0] neg_lo:[1,0,0] neg_hi:[1,0,0]
	v_pk_fma_f32 v[114:115], v[236:237], v[152:153], 0 op_sel_hi:[0,1,0] neg_lo:[1,0,0] neg_hi:[1,0,0]
	v_cvt_pk_bf16_f32 v116, v116, v117
	v_cvt_pk_bf16_f32 v117, v114, v115
	ds_write_b64 v186, v[116:117] offset:1088
	s_waitcnt vmcnt(12)
	v_pk_fma_f32 v[116:117], v[238:239], v[156:157], 0 op_sel_hi:[0,1,0] neg_lo:[1,0,0] neg_hi:[1,0,0]
	v_pk_fma_f32 v[114:115], v[238:239], v[158:159], 0 op_sel_hi:[0,1,0] neg_lo:[1,0,0] neg_hi:[1,0,0]
	v_cvt_pk_bf16_f32 v116, v116, v117
	v_cvt_pk_bf16_f32 v117, v114, v115
	ds_write_b64 v186, v[116:117] offset:1632
	s_waitcnt vmcnt(11)
	v_pk_fma_f32 v[116:117], v[240:241], v[160:161], 0 op_sel_hi:[0,1,0] neg_lo:[1,0,0] neg_hi:[1,0,0]
	v_pk_fma_f32 v[114:115], v[240:241], v[162:163], 0 op_sel_hi:[0,1,0] neg_lo:[1,0,0] neg_hi:[1,0,0]
	v_cvt_pk_bf16_f32 v116, v116, v117
	v_cvt_pk_bf16_f32 v117, v114, v115
	ds_write_b64 v186, v[116:117] offset:2176
	s_waitcnt vmcnt(10)
	v_pk_fma_f32 v[116:117], v[242:243], v[164:165], 0 op_sel_hi:[0,1,0] neg_lo:[1,0,0] neg_hi:[1,0,0]
	v_pk_fma_f32 v[114:115], v[242:243], v[166:167], 0 op_sel_hi:[0,1,0] neg_lo:[1,0,0] neg_hi:[1,0,0]
	v_cvt_pk_bf16_f32 v116, v116, v117
	v_cvt_pk_bf16_f32 v117, v114, v115
	ds_write_b64 v186, v[116:117] offset:2720
	s_waitcnt vmcnt(9)
	v_pk_fma_f32 v[116:117], v[244:245], v[192:193], 0 op_sel_hi:[0,1,0] neg_lo:[1,0,0] neg_hi:[1,0,0]
	v_pk_fma_f32 v[114:115], v[244:245], v[194:195], 0 op_sel_hi:[0,1,0] neg_lo:[1,0,0] neg_hi:[1,0,0]
	v_cvt_pk_bf16_f32 v116, v116, v117
	v_cvt_pk_bf16_f32 v117, v114, v115
	ds_write_b64 v186, v[116:117] offset:3264
	s_waitcnt vmcnt(8)
	v_pk_fma_f32 v[116:117], v[246:247], v[196:197], 0 op_sel_hi:[0,1,0] neg_lo:[1,0,0] neg_hi:[1,0,0]
	v_pk_fma_f32 v[114:115], v[246:247], v[198:199], 0 op_sel_hi:[0,1,0] neg_lo:[1,0,0] neg_hi:[1,0,0]
	v_cvt_pk_bf16_f32 v116, v116, v117
	v_cvt_pk_bf16_f32 v117, v114, v115
	ds_write_b64 v186, v[116:117] offset:3808
	ds_read_b32 v232, v187 offset:128
	ds_read_b32 v234, v187 offset:136
	ds_read_b32 v236, v187 offset:144
	ds_read_b32 v238, v187 offset:152
	ds_read_b32 v240, v187 offset:160
	ds_read_b32 v242, v187 offset:168
	ds_read_b32 v244, v187 offset:176
	ds_read_b32 v246, v187 offset:184
	ds_read_b128 v[114:117], v1
	ds_read_b128 v[118:121], v1 offset:64
	ds_read_b128 v[122:125], v1 offset:128
	ds_read_b128 v[126:129], v1 offset:192
	s_waitcnt lgkmcnt(0)
	s_waitcnt vmcnt(7)
	v_pk_fma_f32 v[130:131], v[232:233], v[130:131], 0 op_sel_hi:[0,1,0] neg_lo:[1,0,0] neg_hi:[1,0,0]
	v_pk_fma_f32 v[132:133], v[232:233], v[132:133], 0 op_sel_hi:[0,1,0] neg_lo:[1,0,0] neg_hi:[1,0,0]
	v_cvt_pk_bf16_f32 v130, v130, v131
	v_cvt_pk_bf16_f32 v131, v132, v133
	ds_write_b64 v186, v[130:131]
	s_waitcnt vmcnt(6)
	v_pk_fma_f32 v[132:133], v[234:235], v[138:139], 0 op_sel_hi:[0,1,0] neg_lo:[1,0,0] neg_hi:[1,0,0]
	v_pk_fma_f32 v[130:131], v[234:235], v[140:141], 0 op_sel_hi:[0,1,0] neg_lo:[1,0,0] neg_hi:[1,0,0]
	v_cvt_pk_bf16_f32 v132, v132, v133
	v_cvt_pk_bf16_f32 v133, v130, v131
	ds_write_b64 v186, v[132:133] offset:544
	s_waitcnt vmcnt(5)
	v_pk_fma_f32 v[132:133], v[236:237], v[142:143], 0 op_sel_hi:[0,1,0] neg_lo:[1,0,0] neg_hi:[1,0,0]
	v_pk_fma_f32 v[130:131], v[236:237], v[144:145], 0 op_sel_hi:[0,1,0] neg_lo:[1,0,0] neg_hi:[1,0,0]
	v_cvt_pk_bf16_f32 v132, v132, v133
	v_cvt_pk_bf16_f32 v133, v130, v131
	ds_write_b64 v186, v[132:133] offset:1088
	s_waitcnt vmcnt(4)
	v_pk_fma_f32 v[132:133], v[238:239], v[146:147], 0 op_sel_hi:[0,1,0] neg_lo:[1,0,0] neg_hi:[1,0,0]
	v_pk_fma_f32 v[130:131], v[238:239], v[148:149], 0 op_sel_hi:[0,1,0] neg_lo:[1,0,0] neg_hi:[1,0,0]
	v_cvt_pk_bf16_f32 v132, v132, v133
	v_cvt_pk_bf16_f32 v133, v130, v131
	ds_write_b64 v186, v[132:133] offset:1632
	s_waitcnt vmcnt(3)
	v_pk_fma_f32 v[132:133], v[240:241], v[168:169], 0 op_sel_hi:[0,1,0] neg_lo:[1,0,0] neg_hi:[1,0,0]
	v_pk_fma_f32 v[130:131], v[240:241], v[170:171], 0 op_sel_hi:[0,1,0] neg_lo:[1,0,0] neg_hi:[1,0,0]
	v_cvt_pk_bf16_f32 v132, v132, v133
	v_cvt_pk_bf16_f32 v133, v130, v131
	ds_write_b64 v186, v[132:133] offset:2176
	s_waitcnt vmcnt(2)
	v_pk_fma_f32 v[132:133], v[242:243], v[172:173], 0 op_sel_hi:[0,1,0] neg_lo:[1,0,0] neg_hi:[1,0,0]
	v_pk_fma_f32 v[130:131], v[242:243], v[174:175], 0 op_sel_hi:[0,1,0] neg_lo:[1,0,0] neg_hi:[1,0,0]
	v_cvt_pk_bf16_f32 v132, v132, v133
	v_cvt_pk_bf16_f32 v133, v130, v131
	ds_write_b64 v186, v[132:133] offset:2720
	s_waitcnt vmcnt(1)
	v_pk_fma_f32 v[132:133], v[244:245], v[176:177], 0 op_sel_hi:[0,1,0] neg_lo:[1,0,0] neg_hi:[1,0,0]
	v_pk_fma_f32 v[130:131], v[244:245], v[178:179], 0 op_sel_hi:[0,1,0] neg_lo:[1,0,0] neg_hi:[1,0,0]
	v_cvt_pk_bf16_f32 v132, v132, v133
	v_cvt_pk_bf16_f32 v133, v130, v131
	ds_write_b64 v186, v[132:133] offset:3264
	s_waitcnt vmcnt(0)
	v_pk_fma_f32 v[132:133], v[246:247], v[180:181], 0 op_sel_hi:[0,1,0] neg_lo:[1,0,0] neg_hi:[1,0,0]
	v_pk_fma_f32 v[130:131], v[246:247], v[182:183], 0 op_sel_hi:[0,1,0] neg_lo:[1,0,0] neg_hi:[1,0,0]
	v_cvt_pk_bf16_f32 v132, v132, v133
	v_cvt_pk_bf16_f32 v133, v130, v131
	ds_write_b64 v186, v[132:133] offset:3808
	ds_read_b128 v[130:133], v1
	ds_read_b128 v[134:137], v1 offset:64
	ds_read_b128 v[138:141], v1 offset:128
	ds_read_b128 v[142:145], v1 offset:192
	ds_read_b128 v[166:169], v184 offset:0
	ds_read_b128 v[170:173], v184 offset:1024
	ds_read_b128 v[174:177], v184 offset:2048
	ds_read_b128 v[178:181], v184 offset:3072
	s_ashr_i32 s7, s6, 31
	s_lshl_b64 s[0:1], s[6:7], 2
	s_add_u32 s0, s4, s0
	s_addc_u32 s1, s5, s1
	v_lshlrev_b32_e32 v1, 4, v0
	s_add_i32 s20, s34, 1
	s_add_i32 s34, s34, -1
	v_or_b32_e32 v153, s10, v206
	s_xor_b32 s26, s3, 2
	s_lshl_b64 s[10:11], s[10:11], 3
	s_and_b32 s20, s20, 3
	s_and_b32 s27, s34, 3
	s_add_u32 s10, s14, s10
	s_addc_u32 s11, s15, s11
	s_lshl_b32 s42, s35, 2
	s_add_i32 s41, s42, 0x26a20
	s_add_i32 s42, s42, 0x26a00
	v_lshlrev_b32_e32 v190, 3, v206
	s_cmp_eq_u32 s35, 3
	v_lshlrev_b32_e32 v150, 3, v0
	v_and_b32_e32 v151, 1, v0
	v_lshl_add_u64 v[0:1], v[154:155], 3, s[14:15]
	v_lshl_add_u64 v[192:193], s[10:11], 0, v[190:191]
	s_cselect_b64 s[10:11], -1, 0
	s_lshl_b32 s14, s3, 2
	s_add_u32 s24, s16, s14
	v_or_b32_e32 v155, 0x20000, v150
	v_add_u32_e32 v156, 0x20880, v150
	v_lshlrev_b32_e32 v150, 1, v153
	s_addc_u32 s25, s17, 0
	s_lshl_b32 s43, s3, 9
	v_lshl_add_u32 v212, s26, 9, v150
	s_lshl_b32 s15, s26, 8
	s_add_i32 s26, s43, 0x200
	v_mov_b32_e32 v152, 0x880
	v_cmp_lt_u32_e64 s[0:1], 15, v206
	v_cmp_eq_u32_e32 vcc, 1, v151
	s_and_b32 s45, s26, 0x600
	s_add_i32 s26, s43, 0x500
	v_cndmask_b32_e32 v211, 0, v152, vcc
	s_and_b32 s56, s26, 0x700
	s_add_i32 s26, s43, 0x540
	v_lshl_add_u32 v213, s20, 9, v150
	v_lshl_add_u32 v214, s27, 9, v150
	s_and_b32 s57, s26, 0x740
	s_add_i32 s26, s43, 0x580
	s_and_b32 s58, s26, 0x780
	s_add_i32 s26, s43, 0x5c0
	s_and_b32 s59, s26, 0x7c0
	s_add_i32 s26, s43, 0x600
	s_and_b32 s60, s26, 0x600
	s_add_i32 s26, s43, 0x640
	s_and_b32 s61, s26, 0x640
	s_add_i32 s26, s43, 0x680
	s_and_b32 s62, s26, 0x680
	s_add_i32 s26, s43, 0x6c0
	s_and_b32 s63, s26, 0x6c0
	s_add_i32 s26, s43, 0x700
	s_and_b32 s64, s26, 0x700
	s_add_i32 s26, s43, 0x740
	s_and_b32 s65, s26, 0x740
	s_add_i32 s26, s43, 0x780
	s_lshl_b32 s14, s27, 8
	s_lshl_b32 s20, s20, 8
	s_add_i32 s27, s43, 0x240
	s_add_i32 s28, s43, 0x280
	s_add_i32 s29, s43, 0x2c0
	s_add_i32 s30, s43, 0x300
	s_add_i32 s31, s43, 0x340
	s_add_i32 s34, s43, 0x380
	s_add_i32 s35, s43, 0x3c0
	s_add_i32 s36, s43, 0x440
	s_add_i32 s37, s43, 0x480
	s_add_i32 s38, s43, 0x4c0
	s_and_b32 s66, s26, 0x780
	s_add_i32 s26, s43, 0x7c0
	s_mul_hi_i32 s23, s18, 0x65
	s_mul_i32 s22, s18, 0x65
	v_cmp_eq_u32_e64 s[4:5], 1, v185
	v_cmp_eq_u32_e64 s[6:7], 2, v185
	v_cmp_eq_u32_e64 s[8:9], 63, v206
	s_xor_b32 s44, s43, 0x400
	s_and_b32 s46, s27, 0x640
	s_and_b32 s47, s28, 0x680
	s_waitcnt lgkmcnt(0)
	v_mov_b32_e32 v146, 0x20000
	s_and_b32 s48, s29, 0x6c0
	s_and_b32 s49, s30, 0x700
	s_and_b32 s50, s31, 0x740
	s_and_b32 s51, s34, 0x780
	s_and_b32 s52, s35, 0x7c0
	s_and_b32 s53, s36, 0x640
	s_and_b32 s54, s37, 0x680
	s_and_b32 s55, s38, 0x6c0
	s_and_b32 s67, s26, 0x7c0
	s_and_b64 s[26:27], s[10:11], s[12:13]
	v_lshl_add_u32 v215, v154, 1, v146
	v_mov_b32_e32 v216, 1
	s_lshl_b32 s28, s14, 3
	s_lshl_b32 s30, s15, 3
	s_lshl_b32 s34, s20, 3
	s_movk_i32 s68, 0x7fff
	s_mov_b32 s69, 0
	v_and_b32_e32 v220, 24, v206
	v_lshlrev_b32_e32 v220, 2, v220
	v_and_b32_e32 v221, 2, v206
	v_lshl_or_b32 v220, v221, 3, v220
	v_and_b32_e32 v221, 32, v206
	v_lshrrev_b32_e32 v221, 2, v221
	v_or_b32_e32 v220, v220, v221
	v_and_b32_e32 v221, 4, v206
	v_or_b32_e32 v220, v220, v221
	v_and_b32_e32 v221, 1, v206
	v_lshl_or_b32 v220, v221, 1, v220
	v_mov_b32_e32 v220, v254
	s_lshr_b32 s76, s19, 8
	s_add_i32 s76, s76, 0x20000
	v_add_u32_e32 v220, s76, v220
	v_add_u32_e32 v225, s45, v220
	v_add_u32_e32 v226, s44, v220
	v_add_u32_e32 v227, s60, v220
	v_add_u32_e32 v228, s43, v220
	v_and_b32_e32 v221, 1, v206
	v_mul_u32_u24_e32 v221, 0x880, v221
	v_lshrrev_b32_e32 v220, 4, v206
	v_lshl_add_u32 v221, v220, 5, v221
	v_and_b32_e32 v220, 2, v206
	v_lshl_add_u32 v221, v220, 3, v221
	v_add_u32_e32 v222, 0x20000, v221
	v_cmp_ne_u32_e32 vcc, 0, v220
	v_mov_b32_e32 v220, 0x44444444
	v_mov_b32_e32 v221, 0xeeeeeeee
	s_nop 1
	v_cndmask_b32_e32 v223, v220, v221, vcc
	v_cmp_lt_u32_e64 s[74:75], 47, v206
	s_lshr_b32 s82, s19, 15
	s_mul_i32 s83, s82, 0x1100
	s_add_i32 s83, s83, 0x22200
	v_lshl_add_u32 v254, v206, 2, s83
	v_mov_b32_e32 v220, s41
	s_nop 1
	v_cndmask_b32_e64 v254, v254, v220, s[12:13]
	v_mov_b32_e32 v224, v184
	s_mov_b32 s86, 0x55555555
	s_mov_b32 s87, 0x55555555
	s_lshr_b32 s78, s19, 15
	s_lshl_b32 s79, s78, 11
	v_add_u32_e32 v255, s79, v224
	ds_read_b128 v[182:185], v224 offset:4096
	ds_read_b128 v[186:189], v224 offset:5120
	s_mov_b32 s20, 0
